# RG-LRU: one workgroup barrier per chunk (tile of chunk c+1 waited before the exchange barrier, chunk c+2 requested right after it); in-proj-0 conversion by hand-written routine
# speedup vs baseline: 1.0014x; 1.0014x over previous
.LBB0_1451:
	s_load_dwordx4 s[0:3], s[8:9], 0x138
	s_waitcnt lgkmcnt(0)
	s_mov_b64 s[4:5], s[0:1]
	s_cmp_lt_i32 s4, 12
	s_cselect_b64 s[0:1], -1, 0
	s_cmp_gt_i32 s5, 11
	s_cselect_b64 s[2:3], -1, 0
	s_and_b64 s[0:1], s[0:1], s[2:3]
	s_andn2_b64 vcc, exec, s[0:1]
	s_cbranch_vccnz .LBB0_1535
	s_mov_b64 s[24:25], s[8:9]
	v_mbcnt_lo_u32_b32 v202, -1, 0
	v_mbcnt_hi_u32_b32 v202, -1, v202
	s_load_dword s0, s[8:9], 0x148
	s_waitcnt lgkmcnt(0)
	v_writelane_b32 v241, s0, 18
	s_nop 1
	v_writelane_b32 v241, s1, 19
	s_add_u32 s0, s8, 0x148
	s_addc_u32 s1, s9, 0
	v_writelane_b32 v241, s0, 34
	s_nop 1
	v_writelane_b32 v241, s1, 35
	v_readlane_b32 s0, v243, 0
	s_cmpk_gt_i32 s0, 0xff
	v_readlane_b32 s1, v243, 1
	s_cbranch_scc1 .LBB0_1482
	v_readlane_b32 s0, v243, 7
	v_readlane_b32 s1, v243, 8
	v_readlane_b32 s4, v243, 0
	v_readlane_b32 s6, v243, 12
	s_load_dwordx2 s[2:3], s[0:1], 0x130
	s_lshr_b32 s7, s6, 2
	s_and_b32 s8, s6, 3
	s_bfe_u32 s11, s4, 0x20003
	s_lshr_b32 s50, s4, 5
	s_lshl_b32 s50, s50, 3
	s_and_b32 s51, s4, 7
	s_or_b32 s50, s50, s51
	s_lshr_b32 s9, s50, 2
	s_and_b32 s10, s50, 3
	v_and_b32_e32 v160, 15, v202
	v_lshrrev_b32_e32 v161, 4, v202
	v_lshlrev_b32_e32 v209, 2, v202
	s_lshl_b32 s50, s7, 15
	v_xor_b32_e32 v178, v161, v160
	v_lshlrev_b32_e32 v178, 4, v178
	v_lshl_add_u32 v162, v160, 9, v178
	v_add_u32_e32 v162, s50, v162
	s_lshl_b32 s51, s11, 6
	s_lshl_b32 s52, s8, 4
	s_add_i32 s51, s51, s52
	v_add_u32_e32 v179, s51, v160
	v_lshrrev_b32_e32 v180, 3, v179
	v_and_b32_e32 v181, 7, v179
	v_lshlrev_b32_e32 v181, 1, v181
	v_lshlrev_b32_e32 v182, 2, v161
	v_add_u32_e32 v183, 0, v182
	v_xor_b32_e32 v184, v180, v183
	v_lshlrev_b32_e32 v184, 4, v184
	v_lshl_add_u32 v184, v183, 9, v184
	v_add3_u32 v165, v184, v181, s50
	v_add_u32_e32 v183, 1, v182
	v_xor_b32_e32 v184, v180, v183
	v_lshlrev_b32_e32 v184, 4, v184
	v_lshl_add_u32 v184, v183, 9, v184
	v_add3_u32 v166, v184, v181, s50
	v_add_u32_e32 v183, 2, v182
	v_xor_b32_e32 v184, v180, v183
	v_lshlrev_b32_e32 v184, 4, v184
	v_lshl_add_u32 v184, v183, 9, v184
	v_add3_u32 v167, v184, v181, s50
	v_add_u32_e32 v183, 3, v182
	v_xor_b32_e32 v184, v180, v183
	v_lshlrev_b32_e32 v184, 4, v184
	v_lshl_add_u32 v184, v183, 9, v184
	v_add3_u32 v168, v184, v181, s50
	v_lshrrev_b32_e32 v185, 5, v202
	v_and_b32_e32 v186, 31, v202
	s_lshl_b32 s51, s6, 4
	v_add_u32_e32 v187, 0, v185
	v_xor_b32_e32 v188, v186, v187
	v_lshlrev_b32_e32 v188, 4, v188
	v_add_u32_e32 v187, s51, v187
	v_lshl_add_u32 v211, v187, 11, v188
	v_add_u32_e32 v187, 2, v185
	v_xor_b32_e32 v188, v186, v187
	v_lshlrev_b32_e32 v188, 4, v188
	v_add_u32_e32 v187, s51, v187
	v_lshl_add_u32 v212, v187, 11, v188
	v_add_u32_e32 v187, 4, v185
	v_xor_b32_e32 v188, v186, v187
	v_lshlrev_b32_e32 v188, 4, v188
	v_add_u32_e32 v187, s51, v187
	v_lshl_add_u32 v213, v187, 11, v188
	v_add_u32_e32 v187, 6, v185
	v_xor_b32_e32 v188, v186, v187
	v_lshlrev_b32_e32 v188, 4, v188
	v_add_u32_e32 v187, s51, v187
	v_lshl_add_u32 v214, v187, 11, v188
	v_add_u32_e32 v187, 8, v185
	v_xor_b32_e32 v188, v186, v187
	v_lshlrev_b32_e32 v188, 4, v188
	v_add_u32_e32 v187, s51, v187
	v_lshl_add_u32 v215, v187, 11, v188
	v_add_u32_e32 v187, 10, v185
	v_xor_b32_e32 v188, v186, v187
	v_lshlrev_b32_e32 v188, 4, v188
	v_add_u32_e32 v187, s51, v187
	v_lshl_add_u32 v216, v187, 11, v188
	v_add_u32_e32 v187, 12, v185
	v_xor_b32_e32 v188, v186, v187
	v_lshlrev_b32_e32 v188, 4, v188
	v_add_u32_e32 v187, s51, v187
	v_lshl_add_u32 v217, v187, 11, v188
	v_add_u32_e32 v187, 14, v185
	v_xor_b32_e32 v188, v186, v187
	v_lshlrev_b32_e32 v188, 4, v188
	v_add_u32_e32 v187, s51, v187
	v_lshl_add_u32 v218, v187, 11, v188
	s_lshl_b32 s51, s6, 7
	s_add_i32 s51, s51, 0x20000
	v_lshl_add_u32 v207, v160, 3, s51
	s_lshl_b32 s51, s8, 7
	s_add_i32 s51, s51, 0x20000
	v_lshl_add_u32 v208, v160, 3, s51
	s_lshl_b32 s51, s7, 6
	v_add_u32_e32 v189, s51, v182
	s_lshl_b32 s51, s8, 4
	v_add_u32_e32 v190, s51, v160
	v_lshlrev_b32_e32 v190, 1, v190
	v_lshl_add_u32 v210, v189, 11, v190
	s_waitcnt lgkmcnt(0)
	s_lshl_b32 s50, s10, 9
	s_add_u32 s16, s2, s50
	s_addc_u32 s17, s3, 0
	s_add_u32 s16, s16, 0x1b900000
	s_addc_u32 s17, s17, 0
	s_lshl_b32 s50, s10, 9
	s_lshl_b32 s51, s11, 7
	s_add_i32 s50, s50, s51
	s_add_u32 s18, s2, s50
	s_addc_u32 s19, s3, 0
	s_add_u32 s18, s18, 0x13100000
	s_addc_u32 s19, s19, 0
	s_add_u32 s20, s2, s50
	s_addc_u32 s21, s3, 0
	s_add_u32 s20, s20, 0x29100000
	s_addc_u32 s21, s21, 0
	s_lshl_b32 s50, s4, 18
	s_add_u32 s22, s2, s50
	s_addc_u32 s23, s3, 0
	s_add_u32 s22, s22, 0x20100000
	s_addc_u32 s23, s23, 0
	s_lshl_b32 s50, s10, 10
	s_lshl_b32 s51, s11, 6
	s_add_i32 s50, s50, s51
	s_lshl_b32 s51, s8, 4
	s_add_i32 s50, s50, s51
	s_add_i32 s50, s50, 0
	s_lshl_b32 s50, s50, 9
	s_add_u32 s46, s2, s50
	s_addc_u32 s47, s3, 0
	s_add_u32 s46, s46, 0x1000000
	s_addc_u32 s47, s47, 0
	s_add_u32 s48, s46, 0x20000
	s_addc_u32 s49, s47, 0
	v_lshlrev_b32_e32 v178, 9, v160
	v_lshl_add_u32 v178, v161, 4, v178
	global_load_dwordx4 v[0:3], v178, s[46:47]
	global_load_dwordx4 v[4:7], v178, s[46:47] offset:64
	global_load_dwordx4 v[8:11], v178, s[46:47] offset:128
	global_load_dwordx4 v[12:15], v178, s[46:47] offset:192
	global_load_dwordx4 v[16:19], v178, s[46:47] offset:256
	global_load_dwordx4 v[20:23], v178, s[46:47] offset:320
	global_load_dwordx4 v[24:27], v178, s[46:47] offset:384
	global_load_dwordx4 v[28:31], v178, s[46:47] offset:448
	global_load_dwordx4 v[32:35], v178, s[48:49]
	global_load_dwordx4 v[36:39], v178, s[48:49] offset:64
	global_load_dwordx4 v[40:43], v178, s[48:49] offset:128
	global_load_dwordx4 v[44:47], v178, s[48:49] offset:192
	global_load_dwordx4 v[48:51], v178, s[48:49] offset:256
	global_load_dwordx4 v[52:55], v178, s[48:49] offset:320
	global_load_dwordx4 v[56:59], v178, s[48:49] offset:384
	global_load_dwordx4 v[60:63], v178, s[48:49] offset:448
	s_load_dwordx2 s[46:47], s[0:1], 0xa0
	s_load_dwordx2 s[48:49], s[0:1], 0xb0
	s_load_dwordx2 s[40:41], s[0:1], 0xb8
	s_lshl_b32 s50, s10, 8
	s_lshl_b32 s51, s11, 6
	s_add_i32 s50, s50, s51
	s_lshl_b32 s51, s8, 4
	s_add_i32 s50, s50, s51
	v_add_u32_e32 v179, s50, v160
	v_lshlrev_b32_e32 v179, 2, v179
	s_waitcnt lgkmcnt(0)
	global_load_dword v173, v179, s[46:47]
	global_load_dword v174, v179, s[48:49]
	global_load_dword v175, v179, s[40:41]
	v_cmp_le_u32_e64 s[34:35], 16, v202
	v_cmp_le_u32_e64 s[36:37], 32, v202
	v_add_u32_e32 v204, -16, v202
	v_add_u32_e32 v205, -32, v202
	v_add_u32_e32 v206, 48, v160
	s_cmp_eq_u32 s7, 1
	s_cselect_b64 s[38:39], -1, 0
	v_and_b32_e32 v204, 63, v204
	v_lshlrev_b32_e32 v204, 2, v204
	v_and_b32_e32 v205, 63, v205
	v_lshlrev_b32_e32 v205, 2, v205
	v_and_b32_e32 v206, 63, v206
	v_lshlrev_b32_e32 v206, 2, v206
	v_mov_b32_e32 v176, 0
	s_mov_b32 s53, 0xbfb8aa3b
	s_waitcnt vmcnt(0)
	v_mul_f32_e32 v173, s53, v173
	v_mul_f32_e32 v174, s53, v174
	v_mul_f32_e32 v175, s53, v175
	v_exp_f32_e32 v175, v175
	s_nop 0
	v_add_f32_e32 v180, 1.0, v175
	v_log_f32_e32 v180, v180
	v_mov_b32_e32 v181, 0x3eaaaaab
	v_fma_f32 v181, v175, v181, -0.5
	v_fma_f32 v181, v175, v181, 1.0
	v_mul_f32_e32 v181, v175, v181
	v_mul_f32_e32 v181, 0x3fb8aa3b, v181
	v_cmp_gt_f32_e32 vcc, 0x3cf5c28f, v175
	s_nop 1
	v_cndmask_b32_e32 v175, v180, v181, vcc
	v_mul_f32_e32 v175, 0xc1000000, v175
	s_mov_b32 s13, 0
	s_barrier
	s_cmp_lt_u32 s13, 2
	s_lshl_b32 s50, s13, 7
	s_lshl_b32 s51, s9, 8
	s_add_i32 s51, s51, 0x8000
	s_add_i32 s51, s51, s50
	s_lshl_b32 s59, s9, 11
	s_add_i32 s59, s59, s50
	s_addk_i32 s59, 0xff00
	s_cmp_lt_u32 s13, 2
	s_cselect_b32 s59, s51, s59
	s_lshl_b32 s52, s59, 11
	s_add_u32 s46, s16, s52
	s_addc_u32 s47, s17, 0
	s_lshl_b32 s52, s6, 13
	s_mov_b32 m0, s52
	s_add_i32 s52, s52, 0x400
	global_load_lds_dwordx4 v211, s[46:47]
	s_mov_b32 m0, s52
	s_add_i32 s52, s52, 0x400
	global_load_lds_dwordx4 v212, s[46:47]
	s_mov_b32 m0, s52
	s_add_i32 s52, s52, 0x400
	global_load_lds_dwordx4 v213, s[46:47]
	s_mov_b32 m0, s52
	s_add_i32 s52, s52, 0x400
	global_load_lds_dwordx4 v214, s[46:47]
	s_mov_b32 m0, s52
	s_add_i32 s52, s52, 0x400
	global_load_lds_dwordx4 v215, s[46:47]
	s_mov_b32 m0, s52
	s_add_i32 s52, s52, 0x400
	global_load_lds_dwordx4 v216, s[46:47]
	s_mov_b32 m0, s52
	s_add_i32 s52, s52, 0x400
	global_load_lds_dwordx4 v217, s[46:47]
	s_mov_b32 m0, s52
	s_nop 0
	global_load_lds_dwordx4 v218, s[46:47]
	s_mov_b32 s58, 1
	s_cmp_lt_u32 s58, 2
	s_lshl_b32 s50, s58, 7
	s_lshl_b32 s51, s9, 8
	s_add_i32 s51, s51, 0x8000
	s_add_i32 s51, s51, s50
	s_lshl_b32 s59, s9, 11
	s_add_i32 s59, s59, s50
	s_addk_i32 s59, 0xff00
	s_cmp_lt_u32 s58, 2
	s_cselect_b32 s59, s51, s59
	s_lshl_b32 s52, s59, 11
	s_add_u32 s46, s16, s52
	s_addc_u32 s47, s17, 0
	s_lshl_b32 s52, s6, 13
	s_add_i32 s52, s52, 0x10000
	s_mov_b32 m0, s52
	s_add_i32 s52, s52, 0x400
	global_load_lds_dwordx4 v211, s[46:47]
	s_mov_b32 m0, s52
	s_add_i32 s52, s52, 0x400
	global_load_lds_dwordx4 v212, s[46:47]
	s_mov_b32 m0, s52
	s_add_i32 s52, s52, 0x400
	global_load_lds_dwordx4 v213, s[46:47]
	s_mov_b32 m0, s52
	s_add_i32 s52, s52, 0x400
	global_load_lds_dwordx4 v214, s[46:47]
	s_mov_b32 m0, s52
	s_add_i32 s52, s52, 0x400
	global_load_lds_dwordx4 v215, s[46:47]
	s_mov_b32 m0, s52
	s_add_i32 s52, s52, 0x400
	global_load_lds_dwordx4 v216, s[46:47]
	s_mov_b32 m0, s52
	s_add_i32 s52, s52, 0x400
	global_load_lds_dwordx4 v217, s[46:47]
	s_mov_b32 m0, s52
	s_nop 0
	global_load_lds_dwordx4 v218, s[46:47]
	s_waitcnt vmcnt(8)
	s_barrier
	v_mov_b32_e32 v163, v162
	ds_read_b128 v[96:99], v163
	ds_read_b128 v[100:103], v163 offset:8192
	ds_read_b128 v[104:107], v163 offset:16384
	ds_read_b128 v[108:111], v163 offset:24576
	v_xor_b32_e32 v164, 0x40, v163
	ds_read_b128 v[112:115], v164
	ds_read_b128 v[116:119], v164 offset:8192
	ds_read_b128 v[120:123], v164 offset:16384
	ds_read_b128 v[124:127], v164 offset:24576
	s_waitcnt lgkmcnt(7)
	v_mfma_f32_16x16x32_bf16 v[64:67], v[96:99], v[0:3], 0
	v_mfma_f32_16x16x32_bf16 v[68:71], v[96:99], v[32:35], 0
	v_xor_b32_e32 v164, 0x80, v163
	ds_read_b128 v[96:99], v164
	s_waitcnt lgkmcnt(7)
	v_mfma_f32_16x16x32_bf16 v[72:75], v[100:103], v[0:3], 0
	v_mfma_f32_16x16x32_bf16 v[76:79], v[100:103], v[32:35], 0
	ds_read_b128 v[100:103], v164 offset:8192
	s_waitcnt lgkmcnt(7)
	v_mfma_f32_16x16x32_bf16 v[80:83], v[104:107], v[0:3], 0
	v_mfma_f32_16x16x32_bf16 v[84:87], v[104:107], v[32:35], 0
	ds_read_b128 v[104:107], v164 offset:16384
	s_waitcnt lgkmcnt(7)
	v_mfma_f32_16x16x32_bf16 v[88:91], v[108:111], v[0:3], 0
	v_mfma_f32_16x16x32_bf16 v[92:95], v[108:111], v[32:35], 0
	ds_read_b128 v[108:111], v164 offset:24576
	s_waitcnt lgkmcnt(7)
	v_mfma_f32_16x16x32_bf16 v[64:67], v[112:115], v[4:7], v[64:67]
	v_mfma_f32_16x16x32_bf16 v[68:71], v[112:115], v[36:39], v[68:71]
	v_xor_b32_e32 v164, 0xc0, v163
	ds_read_b128 v[112:115], v164
	s_waitcnt lgkmcnt(7)
	v_mfma_f32_16x16x32_bf16 v[72:75], v[116:119], v[4:7], v[72:75]
	v_mfma_f32_16x16x32_bf16 v[76:79], v[116:119], v[36:39], v[76:79]
	ds_read_b128 v[116:119], v164 offset:8192
	s_waitcnt lgkmcnt(7)
	v_mfma_f32_16x16x32_bf16 v[80:83], v[120:123], v[4:7], v[80:83]
	v_mfma_f32_16x16x32_bf16 v[84:87], v[120:123], v[36:39], v[84:87]
	ds_read_b128 v[120:123], v164 offset:16384
	s_waitcnt lgkmcnt(7)
	v_mfma_f32_16x16x32_bf16 v[88:91], v[124:127], v[4:7], v[88:91]
	v_mfma_f32_16x16x32_bf16 v[92:95], v[124:127], v[36:39], v[92:95]
	ds_read_b128 v[124:127], v164 offset:24576
	s_waitcnt lgkmcnt(7)
	v_mfma_f32_16x16x32_bf16 v[64:67], v[96:99], v[8:11], v[64:67]
	v_mfma_f32_16x16x32_bf16 v[68:71], v[96:99], v[40:43], v[68:71]
	v_xor_b32_e32 v164, 0x100, v163
	ds_read_b128 v[96:99], v164
	s_waitcnt lgkmcnt(7)
	v_mfma_f32_16x16x32_bf16 v[72:75], v[100:103], v[8:11], v[72:75]
	v_mfma_f32_16x16x32_bf16 v[76:79], v[100:103], v[40:43], v[76:79]
	ds_read_b128 v[100:103], v164 offset:8192
	s_waitcnt lgkmcnt(7)
	v_mfma_f32_16x16x32_bf16 v[80:83], v[104:107], v[8:11], v[80:83]
	v_mfma_f32_16x16x32_bf16 v[84:87], v[104:107], v[40:43], v[84:87]
	ds_read_b128 v[104:107], v164 offset:16384
	s_waitcnt lgkmcnt(7)
	v_mfma_f32_16x16x32_bf16 v[88:91], v[108:111], v[8:11], v[88:91]
	v_mfma_f32_16x16x32_bf16 v[92:95], v[108:111], v[40:43], v[92:95]
	ds_read_b128 v[108:111], v164 offset:24576
	s_waitcnt lgkmcnt(7)
	v_mfma_f32_16x16x32_bf16 v[64:67], v[112:115], v[12:15], v[64:67]
	v_mfma_f32_16x16x32_bf16 v[68:71], v[112:115], v[44:47], v[68:71]
	v_xor_b32_e32 v164, 0x140, v163
	ds_read_b128 v[112:115], v164
	s_waitcnt lgkmcnt(7)
	v_mfma_f32_16x16x32_bf16 v[72:75], v[116:119], v[12:15], v[72:75]
	v_mfma_f32_16x16x32_bf16 v[76:79], v[116:119], v[44:47], v[76:79]
	ds_read_b128 v[116:119], v164 offset:8192
	s_waitcnt lgkmcnt(7)
	v_mfma_f32_16x16x32_bf16 v[80:83], v[120:123], v[12:15], v[80:83]
	v_mfma_f32_16x16x32_bf16 v[84:87], v[120:123], v[44:47], v[84:87]
	ds_read_b128 v[120:123], v164 offset:16384
	s_waitcnt lgkmcnt(7)
	v_mfma_f32_16x16x32_bf16 v[88:91], v[124:127], v[12:15], v[88:91]
	v_mfma_f32_16x16x32_bf16 v[92:95], v[124:127], v[44:47], v[92:95]
	ds_read_b128 v[124:127], v164 offset:24576
	s_waitcnt lgkmcnt(7)
	v_mfma_f32_16x16x32_bf16 v[64:67], v[96:99], v[16:19], v[64:67]
	v_mfma_f32_16x16x32_bf16 v[68:71], v[96:99], v[48:51], v[68:71]
	v_xor_b32_e32 v164, 0x180, v163
	ds_read_b128 v[96:99], v164
	s_waitcnt lgkmcnt(7)
	v_mfma_f32_16x16x32_bf16 v[72:75], v[100:103], v[16:19], v[72:75]
	v_mfma_f32_16x16x32_bf16 v[76:79], v[100:103], v[48:51], v[76:79]
	ds_read_b128 v[100:103], v164 offset:8192
	s_waitcnt lgkmcnt(7)
	v_mfma_f32_16x16x32_bf16 v[80:83], v[104:107], v[16:19], v[80:83]
	v_mfma_f32_16x16x32_bf16 v[84:87], v[104:107], v[48:51], v[84:87]
	ds_read_b128 v[104:107], v164 offset:16384
	s_waitcnt lgkmcnt(7)
	v_mfma_f32_16x16x32_bf16 v[88:91], v[108:111], v[16:19], v[88:91]
	v_mfma_f32_16x16x32_bf16 v[92:95], v[108:111], v[48:51], v[92:95]
	ds_read_b128 v[108:111], v164 offset:24576
	s_waitcnt lgkmcnt(7)
	v_mfma_f32_16x16x32_bf16 v[64:67], v[112:115], v[20:23], v[64:67]
	v_mfma_f32_16x16x32_bf16 v[68:71], v[112:115], v[52:55], v[68:71]
	v_xor_b32_e32 v164, 0x1c0, v163
	ds_read_b128 v[112:115], v164
	s_waitcnt lgkmcnt(7)
	v_mfma_f32_16x16x32_bf16 v[72:75], v[116:119], v[20:23], v[72:75]
	v_mfma_f32_16x16x32_bf16 v[76:79], v[116:119], v[52:55], v[76:79]
	ds_read_b128 v[116:119], v164 offset:8192
	s_waitcnt lgkmcnt(7)
	v_mfma_f32_16x16x32_bf16 v[80:83], v[120:123], v[20:23], v[80:83]
	v_mfma_f32_16x16x32_bf16 v[84:87], v[120:123], v[52:55], v[84:87]
	ds_read_b128 v[120:123], v164 offset:16384
	s_waitcnt lgkmcnt(7)
	v_mfma_f32_16x16x32_bf16 v[88:91], v[124:127], v[20:23], v[88:91]
	v_mfma_f32_16x16x32_bf16 v[92:95], v[124:127], v[52:55], v[92:95]
	ds_read_b128 v[124:127], v164 offset:24576
	s_waitcnt lgkmcnt(7)
	v_mfma_f32_16x16x32_bf16 v[64:67], v[96:99], v[24:27], v[64:67]
	v_mfma_f32_16x16x32_bf16 v[68:71], v[96:99], v[56:59], v[68:71]
	s_waitcnt lgkmcnt(6)
	v_mfma_f32_16x16x32_bf16 v[72:75], v[100:103], v[24:27], v[72:75]
	v_mfma_f32_16x16x32_bf16 v[76:79], v[100:103], v[56:59], v[76:79]
	s_waitcnt lgkmcnt(5)
	v_mfma_f32_16x16x32_bf16 v[80:83], v[104:107], v[24:27], v[80:83]
	v_mfma_f32_16x16x32_bf16 v[84:87], v[104:107], v[56:59], v[84:87]
	s_waitcnt lgkmcnt(4)
	v_mfma_f32_16x16x32_bf16 v[88:91], v[108:111], v[24:27], v[88:91]
	v_mfma_f32_16x16x32_bf16 v[92:95], v[108:111], v[56:59], v[92:95]
	s_waitcnt lgkmcnt(3)
	v_mfma_f32_16x16x32_bf16 v[64:67], v[112:115], v[28:31], v[64:67]
	v_mfma_f32_16x16x32_bf16 v[68:71], v[112:115], v[60:63], v[68:71]
	s_waitcnt lgkmcnt(2)
	v_mfma_f32_16x16x32_bf16 v[72:75], v[116:119], v[28:31], v[72:75]
	v_mfma_f32_16x16x32_bf16 v[76:79], v[116:119], v[60:63], v[76:79]
	s_waitcnt lgkmcnt(1)
	v_mfma_f32_16x16x32_bf16 v[80:83], v[120:123], v[28:31], v[80:83]
	v_mfma_f32_16x16x32_bf16 v[84:87], v[120:123], v[60:63], v[84:87]
	s_waitcnt lgkmcnt(0)
	v_mfma_f32_16x16x32_bf16 v[88:91], v[124:127], v[28:31], v[88:91]
	v_mfma_f32_16x16x32_bf16 v[92:95], v[124:127], v[60:63], v[92:95]
	v_mov_b32_e32 v169, v165
	v_mov_b32_e32 v170, v166
	v_mov_b32_e32 v171, v167
	v_mov_b32_e32 v172, v168
	ds_read_u16 v144, v169
	ds_read_u16 v145, v170
	ds_read_u16 v146, v171
	ds_read_u16 v147, v172
	ds_read_u16 v148, v169 offset:8192
	ds_read_u16 v149, v170 offset:8192
	ds_read_u16 v150, v171 offset:8192
	ds_read_u16 v151, v172 offset:8192
	ds_read_u16 v152, v169 offset:16384
	ds_read_u16 v153, v170 offset:16384
	ds_read_u16 v154, v171 offset:16384
	ds_read_u16 v155, v172 offset:16384
	ds_read_u16 v156, v169 offset:24576
	ds_read_u16 v157, v170 offset:24576
	ds_read_u16 v158, v171 offset:24576
	ds_read_u16 v159, v172 offset:24576
	s_nop 7
	v_fma_f32 v178, v64, s53, v173
	v_fma_f32 v179, v65, s53, v173
	v_fma_f32 v180, v66, s53, v173
	v_fma_f32 v181, v67, s53, v173
	v_fma_f32 v182, v72, s53, v173
	v_fma_f32 v183, v73, s53, v173
	v_fma_f32 v184, v74, s53, v173
	v_fma_f32 v185, v75, s53, v173
	v_fma_f32 v186, v68, s53, v174
	v_fma_f32 v187, v69, s53, v174
	v_fma_f32 v188, v70, s53, v174
	v_fma_f32 v189, v71, s53, v174
	v_fma_f32 v190, v76, s53, v174
	v_fma_f32 v191, v77, s53, v174
	v_fma_f32 v192, v78, s53, v174
	v_fma_f32 v193, v79, s53, v174
	v_exp_f32_e32 v178, v178
	v_exp_f32_e32 v179, v179
	v_exp_f32_e32 v180, v180
	v_exp_f32_e32 v181, v181
	v_exp_f32_e32 v182, v182
	v_exp_f32_e32 v183, v183
	v_exp_f32_e32 v184, v184
	v_exp_f32_e32 v185, v185
	v_exp_f32_e32 v186, v186
	v_exp_f32_e32 v187, v187
	v_exp_f32_e32 v188, v188
	v_exp_f32_e32 v189, v189
	v_exp_f32_e32 v190, v190
	v_exp_f32_e32 v191, v191
	v_exp_f32_e32 v192, v192
	v_exp_f32_e32 v193, v193
	v_add_f32_e32 v178, 1.0, v178
	v_add_f32_e32 v179, 1.0, v179
	v_add_f32_e32 v180, 1.0, v180
	v_add_f32_e32 v181, 1.0, v181
	v_add_f32_e32 v182, 1.0, v182
	v_add_f32_e32 v183, 1.0, v183
	v_add_f32_e32 v184, 1.0, v184
	v_add_f32_e32 v185, 1.0, v185
	v_add_f32_e32 v186, 1.0, v186
	v_add_f32_e32 v187, 1.0, v187
	v_add_f32_e32 v188, 1.0, v188
	v_add_f32_e32 v189, 1.0, v189
	v_add_f32_e32 v190, 1.0, v190
	v_add_f32_e32 v191, 1.0, v191
	v_add_f32_e32 v192, 1.0, v192
	v_add_f32_e32 v193, 1.0, v193
	v_rcp_f32_e32 v178, v178
	v_rcp_f32_e32 v179, v179
	v_rcp_f32_e32 v180, v180
	v_rcp_f32_e32 v181, v181
	v_rcp_f32_e32 v182, v182
	v_rcp_f32_e32 v183, v183
	v_rcp_f32_e32 v184, v184
	v_rcp_f32_e32 v185, v185
	v_rcp_f32_e32 v186, v186
	v_rcp_f32_e32 v187, v187
	v_rcp_f32_e32 v188, v188
	v_rcp_f32_e32 v189, v189
	v_rcp_f32_e32 v190, v190
	v_rcp_f32_e32 v191, v191
	v_rcp_f32_e32 v192, v192
	v_rcp_f32_e32 v193, v193
	v_mul_f32_e32 v178, v175, v178
	v_mul_f32_e32 v179, v175, v179
	v_mul_f32_e32 v180, v175, v180
	v_mul_f32_e32 v181, v175, v181
	v_mul_f32_e32 v182, v175, v182
	v_mul_f32_e32 v183, v175, v183
	v_mul_f32_e32 v184, v175, v184
	v_mul_f32_e32 v185, v175, v185
	v_exp_f32_e32 v96, v178
	v_exp_f32_e32 v97, v179
	v_exp_f32_e32 v98, v180
	v_exp_f32_e32 v99, v181
	v_exp_f32_e32 v100, v182
	v_exp_f32_e32 v101, v183
	v_exp_f32_e32 v102, v184
	v_exp_f32_e32 v103, v185
	s_nop 0
	v_fma_f32 v194, -v96, v96, 1.0
	v_fma_f32 v195, -v97, v97, 1.0
	v_fma_f32 v196, -v98, v98, 1.0
	v_fma_f32 v197, -v99, v99, 1.0
	v_fma_f32 v198, -v100, v100, 1.0
	v_fma_f32 v199, -v101, v101, 1.0
	v_fma_f32 v200, -v102, v102, 1.0
	v_fma_f32 v201, -v103, v103, 1.0
	v_max_f32_e32 v194, 0, v194
	v_max_f32_e32 v195, 0, v195
	v_max_f32_e32 v196, 0, v196
	v_max_f32_e32 v197, 0, v197
	v_max_f32_e32 v198, 0, v198
	v_max_f32_e32 v199, 0, v199
	v_max_f32_e32 v200, 0, v200
	v_max_f32_e32 v201, 0, v201
	v_sqrt_f32_e32 v194, v194
	v_sqrt_f32_e32 v195, v195
	v_sqrt_f32_e32 v196, v196
	v_sqrt_f32_e32 v197, v197
	v_sqrt_f32_e32 v198, v198
	v_sqrt_f32_e32 v199, v199
	v_sqrt_f32_e32 v200, v200
	v_sqrt_f32_e32 v201, v201
	s_waitcnt lgkmcnt(8)
	v_lshlrev_b32_e32 v144, 16, v144
	v_lshlrev_b32_e32 v145, 16, v145
	v_lshlrev_b32_e32 v146, 16, v146
	v_lshlrev_b32_e32 v147, 16, v147
	v_lshlrev_b32_e32 v148, 16, v148
	v_lshlrev_b32_e32 v149, 16, v149
	v_lshlrev_b32_e32 v150, 16, v150
	v_lshlrev_b32_e32 v151, 16, v151
	v_mul_f32_e32 v194, v194, v186
	v_mul_f32_e32 v195, v195, v187
	v_mul_f32_e32 v196, v196, v188
	v_mul_f32_e32 v197, v197, v189
	v_mul_f32_e32 v198, v198, v190
	v_mul_f32_e32 v199, v199, v191
	v_mul_f32_e32 v200, v200, v192
	v_mul_f32_e32 v201, v201, v193
	v_mul_f32_e32 v144, v194, v144
	v_mul_f32_e32 v145, v195, v145
	v_mul_f32_e32 v146, v196, v146
	v_mul_f32_e32 v147, v197, v147
	v_mul_f32_e32 v148, v198, v148
	v_mul_f32_e32 v149, v199, v149
	v_mul_f32_e32 v150, v200, v150
	v_mul_f32_e32 v151, v201, v151
	v_fma_f32 v178, v80, s53, v173
	v_fma_f32 v179, v81, s53, v173
	v_fma_f32 v180, v82, s53, v173
	v_fma_f32 v181, v83, s53, v173
	v_fma_f32 v182, v88, s53, v173
	v_fma_f32 v183, v89, s53, v173
	v_fma_f32 v184, v90, s53, v173
	v_fma_f32 v185, v91, s53, v173
	v_fma_f32 v186, v84, s53, v174
	v_fma_f32 v187, v85, s53, v174
	v_fma_f32 v188, v86, s53, v174
	v_fma_f32 v189, v87, s53, v174
	v_fma_f32 v190, v92, s53, v174
	v_fma_f32 v191, v93, s53, v174
	v_fma_f32 v192, v94, s53, v174
	v_fma_f32 v193, v95, s53, v174
	v_exp_f32_e32 v178, v178
	v_exp_f32_e32 v179, v179
	v_exp_f32_e32 v180, v180
	v_exp_f32_e32 v181, v181
	v_exp_f32_e32 v182, v182
	v_exp_f32_e32 v183, v183
	v_exp_f32_e32 v184, v184
	v_exp_f32_e32 v185, v185
	v_exp_f32_e32 v186, v186
	v_exp_f32_e32 v187, v187
	v_exp_f32_e32 v188, v188
	v_exp_f32_e32 v189, v189
	v_exp_f32_e32 v190, v190
	v_exp_f32_e32 v191, v191
	v_exp_f32_e32 v192, v192
	v_exp_f32_e32 v193, v193
	v_add_f32_e32 v178, 1.0, v178
	v_add_f32_e32 v179, 1.0, v179
	v_add_f32_e32 v180, 1.0, v180
	v_add_f32_e32 v181, 1.0, v181
	v_add_f32_e32 v182, 1.0, v182
	v_add_f32_e32 v183, 1.0, v183
	v_add_f32_e32 v184, 1.0, v184
	v_add_f32_e32 v185, 1.0, v185
	v_add_f32_e32 v186, 1.0, v186
	v_add_f32_e32 v187, 1.0, v187
	v_add_f32_e32 v188, 1.0, v188
	v_add_f32_e32 v189, 1.0, v189
	v_add_f32_e32 v190, 1.0, v190
	v_add_f32_e32 v191, 1.0, v191
	v_add_f32_e32 v192, 1.0, v192
	v_add_f32_e32 v193, 1.0, v193
	v_rcp_f32_e32 v178, v178
	v_rcp_f32_e32 v179, v179
	v_rcp_f32_e32 v180, v180
	v_rcp_f32_e32 v181, v181
	v_rcp_f32_e32 v182, v182
	v_rcp_f32_e32 v183, v183
	v_rcp_f32_e32 v184, v184
	v_rcp_f32_e32 v185, v185
	v_rcp_f32_e32 v186, v186
	v_rcp_f32_e32 v187, v187
	v_rcp_f32_e32 v188, v188
	v_rcp_f32_e32 v189, v189
	v_rcp_f32_e32 v190, v190
	v_rcp_f32_e32 v191, v191
	v_rcp_f32_e32 v192, v192
	v_rcp_f32_e32 v193, v193
	v_mul_f32_e32 v178, v175, v178
	v_mul_f32_e32 v179, v175, v179
	v_mul_f32_e32 v180, v175, v180
	v_mul_f32_e32 v181, v175, v181
	v_mul_f32_e32 v182, v175, v182
	v_mul_f32_e32 v183, v175, v183
	v_mul_f32_e32 v184, v175, v184
	v_mul_f32_e32 v185, v175, v185
	v_exp_f32_e32 v104, v178
	v_exp_f32_e32 v105, v179
	v_exp_f32_e32 v106, v180
	v_exp_f32_e32 v107, v181
	v_exp_f32_e32 v108, v182
	v_exp_f32_e32 v109, v183
	v_exp_f32_e32 v110, v184
	v_exp_f32_e32 v111, v185
	s_nop 0
	v_fma_f32 v194, -v104, v104, 1.0
	v_fma_f32 v195, -v105, v105, 1.0
	v_fma_f32 v196, -v106, v106, 1.0
	v_fma_f32 v197, -v107, v107, 1.0
	v_fma_f32 v198, -v108, v108, 1.0
	v_fma_f32 v199, -v109, v109, 1.0
	v_fma_f32 v200, -v110, v110, 1.0
	v_fma_f32 v201, -v111, v111, 1.0
	v_max_f32_e32 v194, 0, v194
	v_max_f32_e32 v195, 0, v195
	v_max_f32_e32 v196, 0, v196
	v_max_f32_e32 v197, 0, v197
	v_max_f32_e32 v198, 0, v198
	v_max_f32_e32 v199, 0, v199
	v_max_f32_e32 v200, 0, v200
	v_max_f32_e32 v201, 0, v201
	v_sqrt_f32_e32 v194, v194
	v_sqrt_f32_e32 v195, v195
	v_sqrt_f32_e32 v196, v196
	v_sqrt_f32_e32 v197, v197
	v_sqrt_f32_e32 v198, v198
	v_sqrt_f32_e32 v199, v199
	v_sqrt_f32_e32 v200, v200
	v_sqrt_f32_e32 v201, v201
	s_waitcnt lgkmcnt(0)
	v_lshlrev_b32_e32 v152, 16, v152
	v_lshlrev_b32_e32 v153, 16, v153
	v_lshlrev_b32_e32 v154, 16, v154
	v_lshlrev_b32_e32 v155, 16, v155
	v_lshlrev_b32_e32 v156, 16, v156
	v_lshlrev_b32_e32 v157, 16, v157
	v_lshlrev_b32_e32 v158, 16, v158
	v_lshlrev_b32_e32 v159, 16, v159
	v_mul_f32_e32 v194, v194, v186
	v_mul_f32_e32 v195, v195, v187
	v_mul_f32_e32 v196, v196, v188
	v_mul_f32_e32 v197, v197, v189
	v_mul_f32_e32 v198, v198, v190
	v_mul_f32_e32 v199, v199, v191
	v_mul_f32_e32 v200, v200, v192
	v_mul_f32_e32 v201, v201, v193
	v_mul_f32_e32 v152, v194, v152
	v_mul_f32_e32 v153, v195, v153
	v_mul_f32_e32 v154, v196, v154
	v_mul_f32_e32 v155, v197, v155
	v_mul_f32_e32 v156, v198, v156
	v_mul_f32_e32 v157, v199, v157
	v_mul_f32_e32 v158, v200, v158
	v_mul_f32_e32 v159, v201, v159
	v_fma_f32 v145, v97, v144, v145
	v_fma_f32 v149, v101, v148, v149
	v_fma_f32 v153, v105, v152, v153
	v_fma_f32 v157, v109, v156, v157
	v_mul_f32_e32 v97, v97, v96
	v_mul_f32_e32 v101, v101, v100
	v_mul_f32_e32 v105, v105, v104
	v_mul_f32_e32 v109, v109, v108
	v_fma_f32 v146, v98, v145, v146
	v_fma_f32 v150, v102, v149, v150
	v_fma_f32 v154, v106, v153, v154
	v_fma_f32 v158, v110, v157, v158
	v_mul_f32_e32 v98, v98, v97
	v_mul_f32_e32 v102, v102, v101
	v_mul_f32_e32 v106, v106, v105
	v_mul_f32_e32 v110, v110, v109
	v_fma_f32 v147, v99, v146, v147
	v_fma_f32 v151, v103, v150, v151
	v_fma_f32 v155, v107, v154, v155
	v_fma_f32 v159, v111, v158, v159
	v_mul_f32_e32 v99, v99, v98
	v_mul_f32_e32 v103, v103, v102
	v_mul_f32_e32 v107, v107, v106
	v_mul_f32_e32 v111, v111, v110
	ds_bpermute_b32 v178, v204, v99
	ds_bpermute_b32 v182, v204, v147
	ds_bpermute_b32 v179, v204, v103
	ds_bpermute_b32 v183, v204, v151
	ds_bpermute_b32 v180, v204, v107
	ds_bpermute_b32 v184, v204, v155
	ds_bpermute_b32 v181, v204, v111
	ds_bpermute_b32 v185, v204, v159
	s_waitcnt lgkmcnt(0)
	v_fma_f32 v186, v182, v99, v147
	v_cndmask_b32_e64 v178, 1.0, v178, s[34:35]
	v_fma_f32 v187, v183, v103, v151
	v_cndmask_b32_e64 v179, 1.0, v179, s[34:35]
	v_fma_f32 v188, v184, v107, v155
	v_cndmask_b32_e64 v180, 1.0, v180, s[34:35]
	v_fma_f32 v189, v185, v111, v159
	v_cndmask_b32_e64 v181, 1.0, v181, s[34:35]
	v_cndmask_b32_e64 v223, v147, v186, s[34:35]
	v_mul_f32_e32 v219, v99, v178
	v_cndmask_b32_e64 v224, v151, v187, s[34:35]
	v_mul_f32_e32 v220, v103, v179
	v_cndmask_b32_e64 v225, v155, v188, s[34:35]
	v_mul_f32_e32 v221, v107, v180
	v_cndmask_b32_e64 v226, v159, v189, s[34:35]
	v_mul_f32_e32 v222, v111, v181
	ds_bpermute_b32 v178, v205, v219
	ds_bpermute_b32 v182, v205, v223
	ds_bpermute_b32 v179, v205, v220
	ds_bpermute_b32 v183, v205, v224
	ds_bpermute_b32 v180, v205, v221
	ds_bpermute_b32 v184, v205, v225
	ds_bpermute_b32 v181, v205, v222
	ds_bpermute_b32 v185, v205, v226
	s_waitcnt lgkmcnt(0)
	v_fma_f32 v186, v182, v219, v223
	v_cndmask_b32_e64 v178, 1.0, v178, s[36:37]
	v_fma_f32 v187, v183, v220, v224
	v_cndmask_b32_e64 v179, 1.0, v179, s[36:37]
	v_fma_f32 v188, v184, v221, v225
	v_cndmask_b32_e64 v180, 1.0, v180, s[36:37]
	v_fma_f32 v189, v185, v222, v226
	v_cndmask_b32_e64 v181, 1.0, v181, s[36:37]
	v_cndmask_b32_e64 v223, v223, v186, s[36:37]
	v_mul_f32_e32 v219, v219, v178
	v_cndmask_b32_e64 v224, v224, v187, s[36:37]
	v_mul_f32_e32 v220, v220, v179
	v_cndmask_b32_e64 v225, v225, v188, s[36:37]
	v_mul_f32_e32 v221, v221, v180
	v_cndmask_b32_e64 v226, v226, v189, s[36:37]
	v_mul_f32_e32 v222, v222, v181
	ds_bpermute_b32 v227, v204, v219
	ds_bpermute_b32 v231, v204, v223
	ds_bpermute_b32 v235, v206, v219
	ds_bpermute_b32 v239, v206, v223
	ds_bpermute_b32 v228, v204, v220
	ds_bpermute_b32 v232, v204, v224
	ds_bpermute_b32 v236, v206, v220
	ds_bpermute_b32 v244, v206, v224
	ds_bpermute_b32 v229, v204, v221
	ds_bpermute_b32 v233, v204, v225
	ds_bpermute_b32 v237, v206, v221
	ds_bpermute_b32 v245, v206, v225
	ds_bpermute_b32 v230, v204, v222
	ds_bpermute_b32 v234, v204, v226
	ds_bpermute_b32 v238, v206, v222
	ds_bpermute_b32 v246, v206, v226
	s_waitcnt lgkmcnt(0)
	v_cndmask_b32_e64 v227, 1.0, v227, s[34:35]
	v_cndmask_b32_e64 v231, 0, v231, s[34:35]
	v_cndmask_b32_e64 v228, 1.0, v228, s[34:35]
	v_cndmask_b32_e64 v232, 0, v232, s[34:35]
	v_cndmask_b32_e64 v229, 1.0, v229, s[34:35]
	v_cndmask_b32_e64 v233, 0, v233, s[34:35]
	v_cndmask_b32_e64 v230, 1.0, v230, s[34:35]
	v_cndmask_b32_e64 v234, 0, v234, s[34:35]
	v_mov_b32_e32 v190, v235
	v_mov_b32_e32 v194, v239
	v_mov_b32_e32 v198, v190
	v_mov_b32_e32 v201, v194
	v_fma_f32 v194, v194, v236, v244
	v_mul_f32_e32 v190, v190, v236
	v_mov_b32_e32 v199, v190
	v_mov_b32_e32 v177, v194
	v_fma_f32 v194, v194, v237, v245
	v_mul_f32_e32 v190, v190, v237
	v_mov_b32_e32 v200, v190
	v_mov_b32_e32 v203, v194
	v_fma_f32 v194, v194, v238, v246
	v_mul_f32_e32 v190, v190, v238
	v_mov_b32_e32 v191, v194
	ds_write_b64 v207, v[190:191]
	s_waitcnt vmcnt(0)
	s_waitcnt lgkmcnt(0)
	s_barrier
	s_cmp_gt_u32 s13, 15
	s_cbranch_scc1 .Lmylru_nodma_1
	s_add_i32 s58, s13, 2
	s_cmp_lt_u32 s58, 2
	s_lshl_b32 s50, s58, 7
	s_lshl_b32 s51, s9, 8
	s_add_i32 s51, s51, 0x8000
	s_add_i32 s51, s51, s50
	s_lshl_b32 s59, s9, 11
	s_add_i32 s59, s59, s50
	s_addk_i32 s59, 0xff00
	s_cmp_lt_u32 s58, 2
	s_cselect_b32 s59, s51, s59
	s_lshl_b32 s52, s59, 11
	s_add_u32 s46, s16, s52
	s_addc_u32 s47, s17, 0
	s_lshl_b32 s52, s6, 13
	s_mov_b32 m0, s52
	s_add_i32 s52, s52, 0x400
	global_load_lds_dwordx4 v211, s[46:47]
	s_mov_b32 m0, s52
	s_add_i32 s52, s52, 0x400
	global_load_lds_dwordx4 v212, s[46:47]
	s_mov_b32 m0, s52
	s_add_i32 s52, s52, 0x400
	global_load_lds_dwordx4 v213, s[46:47]
	s_mov_b32 m0, s52
	s_add_i32 s52, s52, 0x400
	global_load_lds_dwordx4 v214, s[46:47]
	s_mov_b32 m0, s52
	s_add_i32 s52, s52, 0x400
	global_load_lds_dwordx4 v215, s[46:47]
	s_mov_b32 m0, s52
	s_add_i32 s52, s52, 0x400
	global_load_lds_dwordx4 v216, s[46:47]
	s_mov_b32 m0, s52
	s_add_i32 s52, s52, 0x400
	global_load_lds_dwordx4 v217, s[46:47]
	s_mov_b32 m0, s52
	s_nop 0
	global_load_lds_dwordx4 v218, s[46:47]
.Lmylru_nodma_1:
	ds_read_b64 v[178:179], v208
	ds_read_b64 v[180:181], v208 offset:512
	s_waitcnt lgkmcnt(0)
	v_fma_f32 v182, v176, v178, v179
	v_cndmask_b32_e64 v183, v176, v182, s[38:39]
	v_fma_f32 v176, v182, v180, v181
	s_add_i32 s13, s13, 1
	v_or_b32_e32 v163, 0x10000, v162
	ds_read_b128 v[96:99], v163
	ds_read_b128 v[100:103], v163 offset:8192
	ds_read_b128 v[104:107], v163 offset:16384
	ds_read_b128 v[108:111], v163 offset:24576
	v_xor_b32_e32 v164, 0x40, v163
	ds_read_b128 v[112:115], v164
	ds_read_b128 v[116:119], v164 offset:8192
	ds_read_b128 v[120:123], v164 offset:16384
	ds_read_b128 v[124:127], v164 offset:24576
	s_waitcnt lgkmcnt(7)
	v_mfma_f32_16x16x32_bf16 v[64:67], v[96:99], v[0:3], 0
	v_mfma_f32_16x16x32_bf16 v[68:71], v[96:99], v[32:35], 0
	v_xor_b32_e32 v164, 0x80, v163
	ds_read_b128 v[96:99], v164
	s_waitcnt lgkmcnt(7)
	v_mfma_f32_16x16x32_bf16 v[72:75], v[100:103], v[0:3], 0
	v_mfma_f32_16x16x32_bf16 v[76:79], v[100:103], v[32:35], 0
	ds_read_b128 v[100:103], v164 offset:8192
	s_waitcnt lgkmcnt(7)
	v_mfma_f32_16x16x32_bf16 v[80:83], v[104:107], v[0:3], 0
	v_mfma_f32_16x16x32_bf16 v[84:87], v[104:107], v[32:35], 0
	ds_read_b128 v[104:107], v164 offset:16384
	s_waitcnt lgkmcnt(7)
	v_mfma_f32_16x16x32_bf16 v[88:91], v[108:111], v[0:3], 0
	v_mfma_f32_16x16x32_bf16 v[92:95], v[108:111], v[32:35], 0
	ds_read_b128 v[108:111], v164 offset:24576
	s_waitcnt lgkmcnt(7)
	v_mfma_f32_16x16x32_bf16 v[64:67], v[112:115], v[4:7], v[64:67]
	v_mfma_f32_16x16x32_bf16 v[68:71], v[112:115], v[36:39], v[68:71]
	v_xor_b32_e32 v164, 0xc0, v163
	ds_read_b128 v[112:115], v164
	s_waitcnt lgkmcnt(7)
	v_mfma_f32_16x16x32_bf16 v[72:75], v[116:119], v[4:7], v[72:75]
	v_mfma_f32_16x16x32_bf16 v[76:79], v[116:119], v[36:39], v[76:79]
	ds_read_b128 v[116:119], v164 offset:8192
	s_waitcnt lgkmcnt(7)
	v_mfma_f32_16x16x32_bf16 v[80:83], v[120:123], v[4:7], v[80:83]
	v_mfma_f32_16x16x32_bf16 v[84:87], v[120:123], v[36:39], v[84:87]
	ds_read_b128 v[120:123], v164 offset:16384
	s_waitcnt lgkmcnt(7)
	v_mfma_f32_16x16x32_bf16 v[88:91], v[124:127], v[4:7], v[88:91]
	v_mfma_f32_16x16x32_bf16 v[92:95], v[124:127], v[36:39], v[92:95]
	ds_read_b128 v[124:127], v164 offset:24576
	s_waitcnt lgkmcnt(7)
	v_mfma_f32_16x16x32_bf16 v[64:67], v[96:99], v[8:11], v[64:67]
	v_mfma_f32_16x16x32_bf16 v[68:71], v[96:99], v[40:43], v[68:71]
	v_xor_b32_e32 v164, 0x100, v163
	ds_read_b128 v[96:99], v164
	s_waitcnt lgkmcnt(7)
	v_mfma_f32_16x16x32_bf16 v[72:75], v[100:103], v[8:11], v[72:75]
	v_mfma_f32_16x16x32_bf16 v[76:79], v[100:103], v[40:43], v[76:79]
	ds_read_b128 v[100:103], v164 offset:8192
	s_waitcnt lgkmcnt(7)
	v_mfma_f32_16x16x32_bf16 v[80:83], v[104:107], v[8:11], v[80:83]
	v_mfma_f32_16x16x32_bf16 v[84:87], v[104:107], v[40:43], v[84:87]
	ds_read_b128 v[104:107], v164 offset:16384
	s_waitcnt lgkmcnt(7)
	v_mfma_f32_16x16x32_bf16 v[88:91], v[108:111], v[8:11], v[88:91]
	v_mfma_f32_16x16x32_bf16 v[92:95], v[108:111], v[40:43], v[92:95]
	ds_read_b128 v[108:111], v164 offset:24576
	s_waitcnt lgkmcnt(7)
	v_mfma_f32_16x16x32_bf16 v[64:67], v[112:115], v[12:15], v[64:67]
	v_mfma_f32_16x16x32_bf16 v[68:71], v[112:115], v[44:47], v[68:71]
	v_xor_b32_e32 v164, 0x140, v163
	ds_read_b128 v[112:115], v164
	s_waitcnt lgkmcnt(7)
	v_mfma_f32_16x16x32_bf16 v[72:75], v[116:119], v[12:15], v[72:75]
	v_mfma_f32_16x16x32_bf16 v[76:79], v[116:119], v[44:47], v[76:79]
	ds_read_b128 v[116:119], v164 offset:8192
	s_waitcnt lgkmcnt(7)
	v_mfma_f32_16x16x32_bf16 v[80:83], v[120:123], v[12:15], v[80:83]
	v_mfma_f32_16x16x32_bf16 v[84:87], v[120:123], v[44:47], v[84:87]
	ds_read_b128 v[120:123], v164 offset:16384
	s_waitcnt lgkmcnt(7)
	v_mfma_f32_16x16x32_bf16 v[88:91], v[124:127], v[12:15], v[88:91]
	v_mfma_f32_16x16x32_bf16 v[92:95], v[124:127], v[44:47], v[92:95]
	ds_read_b128 v[124:127], v164 offset:24576
	s_waitcnt lgkmcnt(7)
	v_mfma_f32_16x16x32_bf16 v[64:67], v[96:99], v[16:19], v[64:67]
	v_mfma_f32_16x16x32_bf16 v[68:71], v[96:99], v[48:51], v[68:71]
	v_xor_b32_e32 v164, 0x180, v163
	ds_read_b128 v[96:99], v164
	s_waitcnt lgkmcnt(7)
	v_mfma_f32_16x16x32_bf16 v[72:75], v[100:103], v[16:19], v[72:75]
	v_mfma_f32_16x16x32_bf16 v[76:79], v[100:103], v[48:51], v[76:79]
	ds_read_b128 v[100:103], v164 offset:8192
	s_waitcnt lgkmcnt(7)
	v_mfma_f32_16x16x32_bf16 v[80:83], v[104:107], v[16:19], v[80:83]
	v_mfma_f32_16x16x32_bf16 v[84:87], v[104:107], v[48:51], v[84:87]
	ds_read_b128 v[104:107], v164 offset:16384
	s_waitcnt lgkmcnt(7)
	v_mfma_f32_16x16x32_bf16 v[88:91], v[108:111], v[16:19], v[88:91]
	v_mfma_f32_16x16x32_bf16 v[92:95], v[108:111], v[48:51], v[92:95]
	ds_read_b128 v[108:111], v164 offset:24576
	s_waitcnt lgkmcnt(7)
	v_mfma_f32_16x16x32_bf16 v[64:67], v[112:115], v[20:23], v[64:67]
	v_mfma_f32_16x16x32_bf16 v[68:71], v[112:115], v[52:55], v[68:71]
	v_xor_b32_e32 v164, 0x1c0, v163
	ds_read_b128 v[112:115], v164
	s_waitcnt lgkmcnt(7)
	v_mfma_f32_16x16x32_bf16 v[72:75], v[116:119], v[20:23], v[72:75]
	v_mfma_f32_16x16x32_bf16 v[76:79], v[116:119], v[52:55], v[76:79]
	ds_read_b128 v[116:119], v164 offset:8192
	s_waitcnt lgkmcnt(7)
	v_mfma_f32_16x16x32_bf16 v[80:83], v[120:123], v[20:23], v[80:83]
	v_mfma_f32_16x16x32_bf16 v[84:87], v[120:123], v[52:55], v[84:87]
	ds_read_b128 v[120:123], v164 offset:16384
	s_waitcnt lgkmcnt(7)
	v_mfma_f32_16x16x32_bf16 v[88:91], v[124:127], v[20:23], v[88:91]
	v_mfma_f32_16x16x32_bf16 v[92:95], v[124:127], v[52:55], v[92:95]
	ds_read_b128 v[124:127], v164 offset:24576
	s_waitcnt lgkmcnt(7)
	v_mfma_f32_16x16x32_bf16 v[64:67], v[96:99], v[24:27], v[64:67]
	v_mfma_f32_16x16x32_bf16 v[68:71], v[96:99], v[56:59], v[68:71]
	s_waitcnt lgkmcnt(6)
	v_mfma_f32_16x16x32_bf16 v[72:75], v[100:103], v[24:27], v[72:75]
	v_mfma_f32_16x16x32_bf16 v[76:79], v[100:103], v[56:59], v[76:79]
	s_waitcnt lgkmcnt(5)
	v_mfma_f32_16x16x32_bf16 v[80:83], v[104:107], v[24:27], v[80:83]
	v_mfma_f32_16x16x32_bf16 v[84:87], v[104:107], v[56:59], v[84:87]
	s_waitcnt lgkmcnt(4)
	v_mfma_f32_16x16x32_bf16 v[88:91], v[108:111], v[24:27], v[88:91]
	v_mfma_f32_16x16x32_bf16 v[92:95], v[108:111], v[56:59], v[92:95]
	s_waitcnt lgkmcnt(3)
	v_mfma_f32_16x16x32_bf16 v[64:67], v[112:115], v[28:31], v[64:67]
	v_mfma_f32_16x16x32_bf16 v[68:71], v[112:115], v[60:63], v[68:71]
	s_waitcnt lgkmcnt(2)
	v_mfma_f32_16x16x32_bf16 v[72:75], v[116:119], v[28:31], v[72:75]
	v_mfma_f32_16x16x32_bf16 v[76:79], v[116:119], v[60:63], v[76:79]
	s_waitcnt lgkmcnt(1)
	v_mfma_f32_16x16x32_bf16 v[80:83], v[120:123], v[28:31], v[80:83]
	v_mfma_f32_16x16x32_bf16 v[84:87], v[120:123], v[60:63], v[84:87]
	s_waitcnt lgkmcnt(0)
	v_mfma_f32_16x16x32_bf16 v[88:91], v[124:127], v[28:31], v[88:91]
	v_mfma_f32_16x16x32_bf16 v[92:95], v[124:127], v[60:63], v[92:95]
	v_or_b32_e32 v169, 0x10000, v165
	v_or_b32_e32 v170, 0x10000, v166
	v_or_b32_e32 v171, 0x10000, v167
	v_or_b32_e32 v172, 0x10000, v168
	ds_read_u16 v144, v169
	ds_read_u16 v145, v170
	ds_read_u16 v146, v171
	ds_read_u16 v147, v172
	ds_read_u16 v148, v169 offset:8192
	ds_read_u16 v149, v170 offset:8192
	ds_read_u16 v150, v171 offset:8192
	ds_read_u16 v151, v172 offset:8192
	ds_read_u16 v152, v169 offset:16384
	ds_read_u16 v153, v170 offset:16384
	ds_read_u16 v154, v171 offset:16384
	ds_read_u16 v155, v172 offset:16384
	ds_read_u16 v156, v169 offset:24576
	ds_read_u16 v157, v170 offset:24576
	ds_read_u16 v158, v171 offset:24576
	ds_read_u16 v159, v172 offset:24576
	s_nop 7
	v_fma_f32 v178, v64, s53, v173
	v_fma_f32 v179, v65, s53, v173
	v_fma_f32 v180, v66, s53, v173
	v_fma_f32 v181, v67, s53, v173
	v_fma_f32 v182, v72, s53, v173
	v_fma_f32 v183, v73, s53, v173
	v_fma_f32 v184, v74, s53, v173
	v_fma_f32 v185, v75, s53, v173
	v_fma_f32 v186, v68, s53, v174
	v_fma_f32 v187, v69, s53, v174
	v_fma_f32 v188, v70, s53, v174
	v_fma_f32 v189, v71, s53, v174
	v_fma_f32 v190, v76, s53, v174
	v_fma_f32 v191, v77, s53, v174
	v_fma_f32 v192, v78, s53, v174
	v_fma_f32 v193, v79, s53, v174
	v_exp_f32_e32 v178, v178
	v_exp_f32_e32 v179, v179
	v_exp_f32_e32 v180, v180
	v_exp_f32_e32 v181, v181
	v_exp_f32_e32 v182, v182
	v_exp_f32_e32 v183, v183
	v_exp_f32_e32 v184, v184
	v_exp_f32_e32 v185, v185
	v_exp_f32_e32 v186, v186
	v_exp_f32_e32 v187, v187
	v_exp_f32_e32 v188, v188
	v_exp_f32_e32 v189, v189
	v_exp_f32_e32 v190, v190
	v_exp_f32_e32 v191, v191
	v_exp_f32_e32 v192, v192
	v_exp_f32_e32 v193, v193
	v_add_f32_e32 v178, 1.0, v178
	v_add_f32_e32 v179, 1.0, v179
	v_add_f32_e32 v180, 1.0, v180
	v_add_f32_e32 v181, 1.0, v181
	v_add_f32_e32 v182, 1.0, v182
	v_add_f32_e32 v183, 1.0, v183
	v_add_f32_e32 v184, 1.0, v184
	v_add_f32_e32 v185, 1.0, v185
	v_add_f32_e32 v186, 1.0, v186
	v_add_f32_e32 v187, 1.0, v187
	v_add_f32_e32 v188, 1.0, v188
	v_add_f32_e32 v189, 1.0, v189
	v_add_f32_e32 v190, 1.0, v190
	v_add_f32_e32 v191, 1.0, v191
	v_add_f32_e32 v192, 1.0, v192
	v_add_f32_e32 v193, 1.0, v193
	v_rcp_f32_e32 v178, v178
	v_rcp_f32_e32 v179, v179
	v_rcp_f32_e32 v180, v180
	v_rcp_f32_e32 v181, v181
	v_rcp_f32_e32 v182, v182
	v_rcp_f32_e32 v183, v183
	v_rcp_f32_e32 v184, v184
	v_rcp_f32_e32 v185, v185
	v_rcp_f32_e32 v186, v186
	v_rcp_f32_e32 v187, v187
	v_rcp_f32_e32 v188, v188
	v_rcp_f32_e32 v189, v189
	v_rcp_f32_e32 v190, v190
	v_rcp_f32_e32 v191, v191
	v_rcp_f32_e32 v192, v192
	v_rcp_f32_e32 v193, v193
	v_mul_f32_e32 v178, v175, v178
	v_mul_f32_e32 v179, v175, v179
	v_mul_f32_e32 v180, v175, v180
	v_mul_f32_e32 v181, v175, v181
	v_mul_f32_e32 v182, v175, v182
	v_mul_f32_e32 v183, v175, v183
	v_mul_f32_e32 v184, v175, v184
	v_mul_f32_e32 v185, v175, v185
	v_exp_f32_e32 v96, v178
	v_exp_f32_e32 v97, v179
	v_exp_f32_e32 v98, v180
	v_exp_f32_e32 v99, v181
	v_exp_f32_e32 v100, v182
	v_exp_f32_e32 v101, v183
	v_exp_f32_e32 v102, v184
	v_exp_f32_e32 v103, v185
	s_nop 0
	v_fma_f32 v194, -v96, v96, 1.0
	v_fma_f32 v195, -v97, v97, 1.0
	v_fma_f32 v196, -v98, v98, 1.0
	v_fma_f32 v197, -v99, v99, 1.0
	v_fma_f32 v198, -v100, v100, 1.0
	v_fma_f32 v199, -v101, v101, 1.0
	v_fma_f32 v200, -v102, v102, 1.0
	v_fma_f32 v201, -v103, v103, 1.0
	v_max_f32_e32 v194, 0, v194
	v_max_f32_e32 v195, 0, v195
	v_max_f32_e32 v196, 0, v196
	v_max_f32_e32 v197, 0, v197
	v_max_f32_e32 v198, 0, v198
	v_max_f32_e32 v199, 0, v199
	v_max_f32_e32 v200, 0, v200
	v_max_f32_e32 v201, 0, v201
	v_sqrt_f32_e32 v194, v194
	v_sqrt_f32_e32 v195, v195
	v_sqrt_f32_e32 v196, v196
	v_sqrt_f32_e32 v197, v197
	v_sqrt_f32_e32 v198, v198
	v_sqrt_f32_e32 v199, v199
	v_sqrt_f32_e32 v200, v200
	v_sqrt_f32_e32 v201, v201
	s_waitcnt lgkmcnt(8)
	v_lshlrev_b32_e32 v144, 16, v144
	v_lshlrev_b32_e32 v145, 16, v145
	v_lshlrev_b32_e32 v146, 16, v146
	v_lshlrev_b32_e32 v147, 16, v147
	v_lshlrev_b32_e32 v148, 16, v148
	v_lshlrev_b32_e32 v149, 16, v149
	v_lshlrev_b32_e32 v150, 16, v150
	v_lshlrev_b32_e32 v151, 16, v151
	v_mul_f32_e32 v194, v194, v186
	v_mul_f32_e32 v195, v195, v187
	v_mul_f32_e32 v196, v196, v188
	v_mul_f32_e32 v197, v197, v189
	v_mul_f32_e32 v198, v198, v190
	v_mul_f32_e32 v199, v199, v191
	v_mul_f32_e32 v200, v200, v192
	v_mul_f32_e32 v201, v201, v193
	v_mul_f32_e32 v144, v194, v144
	v_mul_f32_e32 v145, v195, v145
	v_mul_f32_e32 v146, v196, v146
	v_mul_f32_e32 v147, v197, v147
	v_mul_f32_e32 v148, v198, v148
	v_mul_f32_e32 v149, v199, v149
	v_mul_f32_e32 v150, v200, v150
	v_mul_f32_e32 v151, v201, v151
	v_fma_f32 v178, v80, s53, v173
	v_fma_f32 v179, v81, s53, v173
	v_fma_f32 v180, v82, s53, v173
	v_fma_f32 v181, v83, s53, v173
	v_fma_f32 v182, v88, s53, v173
	v_fma_f32 v183, v89, s53, v173
	v_fma_f32 v184, v90, s53, v173
	v_fma_f32 v185, v91, s53, v173
	v_fma_f32 v186, v84, s53, v174
	v_fma_f32 v187, v85, s53, v174
	v_fma_f32 v188, v86, s53, v174
	v_fma_f32 v189, v87, s53, v174
	v_fma_f32 v190, v92, s53, v174
	v_fma_f32 v191, v93, s53, v174
	v_fma_f32 v192, v94, s53, v174
	v_fma_f32 v193, v95, s53, v174
	v_exp_f32_e32 v178, v178
	v_exp_f32_e32 v179, v179
	v_exp_f32_e32 v180, v180
	v_exp_f32_e32 v181, v181
	v_exp_f32_e32 v182, v182
	v_exp_f32_e32 v183, v183
	v_exp_f32_e32 v184, v184
	v_exp_f32_e32 v185, v185
	v_exp_f32_e32 v186, v186
	v_exp_f32_e32 v187, v187
	v_exp_f32_e32 v188, v188
	v_exp_f32_e32 v189, v189
	v_exp_f32_e32 v190, v190
	v_exp_f32_e32 v191, v191
	v_exp_f32_e32 v192, v192
	v_exp_f32_e32 v193, v193
	v_add_f32_e32 v178, 1.0, v178
	v_add_f32_e32 v179, 1.0, v179
	v_add_f32_e32 v180, 1.0, v180
	v_add_f32_e32 v181, 1.0, v181
	v_add_f32_e32 v182, 1.0, v182
	v_add_f32_e32 v183, 1.0, v183
	v_add_f32_e32 v184, 1.0, v184
	v_add_f32_e32 v185, 1.0, v185
	v_add_f32_e32 v186, 1.0, v186
	v_add_f32_e32 v187, 1.0, v187
	v_add_f32_e32 v188, 1.0, v188
	v_add_f32_e32 v189, 1.0, v189
	v_add_f32_e32 v190, 1.0, v190
	v_add_f32_e32 v191, 1.0, v191
	v_add_f32_e32 v192, 1.0, v192
	v_add_f32_e32 v193, 1.0, v193
	v_rcp_f32_e32 v178, v178
	v_rcp_f32_e32 v179, v179
	v_rcp_f32_e32 v180, v180
	v_rcp_f32_e32 v181, v181
	v_rcp_f32_e32 v182, v182
	v_rcp_f32_e32 v183, v183
	v_rcp_f32_e32 v184, v184
	v_rcp_f32_e32 v185, v185
	v_rcp_f32_e32 v186, v186
	v_rcp_f32_e32 v187, v187
	v_rcp_f32_e32 v188, v188
	v_rcp_f32_e32 v189, v189
	v_rcp_f32_e32 v190, v190
	v_rcp_f32_e32 v191, v191
	v_rcp_f32_e32 v192, v192
	v_rcp_f32_e32 v193, v193
	v_mul_f32_e32 v178, v175, v178
	v_mul_f32_e32 v179, v175, v179
	v_mul_f32_e32 v180, v175, v180
	v_mul_f32_e32 v181, v175, v181
	v_mul_f32_e32 v182, v175, v182
	v_mul_f32_e32 v183, v175, v183
	v_mul_f32_e32 v184, v175, v184
	v_mul_f32_e32 v185, v175, v185
	v_exp_f32_e32 v104, v178
	v_exp_f32_e32 v105, v179
	v_exp_f32_e32 v106, v180
	v_exp_f32_e32 v107, v181
	v_exp_f32_e32 v108, v182
	v_exp_f32_e32 v109, v183
	v_exp_f32_e32 v110, v184
	v_exp_f32_e32 v111, v185
	s_nop 0
	v_fma_f32 v194, -v104, v104, 1.0
	v_fma_f32 v195, -v105, v105, 1.0
	v_fma_f32 v196, -v106, v106, 1.0
	v_fma_f32 v197, -v107, v107, 1.0
	v_fma_f32 v198, -v108, v108, 1.0
	v_fma_f32 v199, -v109, v109, 1.0
	v_fma_f32 v200, -v110, v110, 1.0
	v_fma_f32 v201, -v111, v111, 1.0
	v_max_f32_e32 v194, 0, v194
	v_max_f32_e32 v195, 0, v195
	v_max_f32_e32 v196, 0, v196
	v_max_f32_e32 v197, 0, v197
	v_max_f32_e32 v198, 0, v198
	v_max_f32_e32 v199, 0, v199
	v_max_f32_e32 v200, 0, v200
	v_max_f32_e32 v201, 0, v201
	v_sqrt_f32_e32 v194, v194
	v_sqrt_f32_e32 v195, v195
	v_sqrt_f32_e32 v196, v196
	v_sqrt_f32_e32 v197, v197
	v_sqrt_f32_e32 v198, v198
	v_sqrt_f32_e32 v199, v199
	v_sqrt_f32_e32 v200, v200
	v_sqrt_f32_e32 v201, v201
	s_waitcnt lgkmcnt(0)
	v_lshlrev_b32_e32 v152, 16, v152
	v_lshlrev_b32_e32 v153, 16, v153
	v_lshlrev_b32_e32 v154, 16, v154
	v_lshlrev_b32_e32 v155, 16, v155
	v_lshlrev_b32_e32 v156, 16, v156
	v_lshlrev_b32_e32 v157, 16, v157
	v_lshlrev_b32_e32 v158, 16, v158
	v_lshlrev_b32_e32 v159, 16, v159
	v_mul_f32_e32 v194, v194, v186
	v_mul_f32_e32 v195, v195, v187
	v_mul_f32_e32 v196, v196, v188
	v_mul_f32_e32 v197, v197, v189
	v_mul_f32_e32 v198, v198, v190
	v_mul_f32_e32 v199, v199, v191
	v_mul_f32_e32 v200, v200, v192
	v_mul_f32_e32 v201, v201, v193
	v_mul_f32_e32 v152, v194, v152
	v_mul_f32_e32 v153, v195, v153
	v_mul_f32_e32 v154, v196, v154
	v_mul_f32_e32 v155, v197, v155
	v_mul_f32_e32 v156, v198, v156
	v_mul_f32_e32 v157, v199, v157
	v_mul_f32_e32 v158, v200, v158
	v_mul_f32_e32 v159, v201, v159
	v_fma_f32 v145, v97, v144, v145
	v_fma_f32 v149, v101, v148, v149
	v_fma_f32 v153, v105, v152, v153
	v_fma_f32 v157, v109, v156, v157
	v_mul_f32_e32 v97, v97, v96
	v_mul_f32_e32 v101, v101, v100
	v_mul_f32_e32 v105, v105, v104
	v_mul_f32_e32 v109, v109, v108
	v_fma_f32 v146, v98, v145, v146
	v_fma_f32 v150, v102, v149, v150
	v_fma_f32 v154, v106, v153, v154
	v_fma_f32 v158, v110, v157, v158
	v_mul_f32_e32 v98, v98, v97
	v_mul_f32_e32 v102, v102, v101
	v_mul_f32_e32 v106, v106, v105
	v_mul_f32_e32 v110, v110, v109
	v_fma_f32 v147, v99, v146, v147
	v_fma_f32 v151, v103, v150, v151
	v_fma_f32 v155, v107, v154, v155
	v_fma_f32 v159, v111, v158, v159
	v_mul_f32_e32 v99, v99, v98
	v_mul_f32_e32 v103, v103, v102
	v_mul_f32_e32 v107, v107, v106
	v_mul_f32_e32 v111, v111, v110
	ds_bpermute_b32 v178, v204, v99
	ds_bpermute_b32 v182, v204, v147
	ds_bpermute_b32 v179, v204, v103
	ds_bpermute_b32 v183, v204, v151
	ds_bpermute_b32 v180, v204, v107
	ds_bpermute_b32 v184, v204, v155
	ds_bpermute_b32 v181, v204, v111
	ds_bpermute_b32 v185, v204, v159
	s_waitcnt lgkmcnt(0)
	v_fma_f32 v186, v182, v99, v147
	v_cndmask_b32_e64 v178, 1.0, v178, s[34:35]
	v_fma_f32 v187, v183, v103, v151
	v_cndmask_b32_e64 v179, 1.0, v179, s[34:35]
	v_fma_f32 v188, v184, v107, v155
	v_cndmask_b32_e64 v180, 1.0, v180, s[34:35]
	v_fma_f32 v189, v185, v111, v159
	v_cndmask_b32_e64 v181, 1.0, v181, s[34:35]
	v_cndmask_b32_e64 v223, v147, v186, s[34:35]
	v_mul_f32_e32 v219, v99, v178
	v_cndmask_b32_e64 v224, v151, v187, s[34:35]
	v_mul_f32_e32 v220, v103, v179
	v_cndmask_b32_e64 v225, v155, v188, s[34:35]
	v_mul_f32_e32 v221, v107, v180
	v_cndmask_b32_e64 v226, v159, v189, s[34:35]
	v_mul_f32_e32 v222, v111, v181
	ds_bpermute_b32 v178, v205, v219
	ds_bpermute_b32 v182, v205, v223
	ds_bpermute_b32 v179, v205, v220
	ds_bpermute_b32 v183, v205, v224
	ds_bpermute_b32 v180, v205, v221
	ds_bpermute_b32 v184, v205, v225
	ds_bpermute_b32 v181, v205, v222
	ds_bpermute_b32 v185, v205, v226
	s_waitcnt lgkmcnt(0)
	v_fma_f32 v186, v182, v219, v223
	v_cndmask_b32_e64 v178, 1.0, v178, s[36:37]
	v_fma_f32 v187, v183, v220, v224
	v_cndmask_b32_e64 v179, 1.0, v179, s[36:37]
	v_fma_f32 v188, v184, v221, v225
	v_cndmask_b32_e64 v180, 1.0, v180, s[36:37]
	v_fma_f32 v189, v185, v222, v226
	v_cndmask_b32_e64 v181, 1.0, v181, s[36:37]
	v_cndmask_b32_e64 v223, v223, v186, s[36:37]
	v_mul_f32_e32 v219, v219, v178
	v_cndmask_b32_e64 v224, v224, v187, s[36:37]
	v_mul_f32_e32 v220, v220, v179
	v_cndmask_b32_e64 v225, v225, v188, s[36:37]
	v_mul_f32_e32 v221, v221, v180
	v_cndmask_b32_e64 v226, v226, v189, s[36:37]
	v_mul_f32_e32 v222, v222, v181
	ds_bpermute_b32 v227, v204, v219
	ds_bpermute_b32 v231, v204, v223
	ds_bpermute_b32 v235, v206, v219
	ds_bpermute_b32 v239, v206, v223
	ds_bpermute_b32 v228, v204, v220
	ds_bpermute_b32 v232, v204, v224
	ds_bpermute_b32 v236, v206, v220
	ds_bpermute_b32 v244, v206, v224
	ds_bpermute_b32 v229, v204, v221
	ds_bpermute_b32 v233, v204, v225
	ds_bpermute_b32 v237, v206, v221
	ds_bpermute_b32 v245, v206, v225
	ds_bpermute_b32 v230, v204, v222
	ds_bpermute_b32 v234, v204, v226
	ds_bpermute_b32 v238, v206, v222
	ds_bpermute_b32 v246, v206, v226
	s_waitcnt lgkmcnt(0)
	v_cndmask_b32_e64 v227, 1.0, v227, s[34:35]
	v_cndmask_b32_e64 v231, 0, v231, s[34:35]
	v_cndmask_b32_e64 v228, 1.0, v228, s[34:35]
	v_cndmask_b32_e64 v232, 0, v232, s[34:35]
	v_cndmask_b32_e64 v229, 1.0, v229, s[34:35]
	v_cndmask_b32_e64 v233, 0, v233, s[34:35]
	v_cndmask_b32_e64 v230, 1.0, v230, s[34:35]
	v_cndmask_b32_e64 v234, 0, v234, s[34:35]
	v_mov_b32_e32 v190, v235
	v_mov_b32_e32 v194, v239
	v_mov_b32_e32 v198, v190
	v_mov_b32_e32 v201, v194
	v_fma_f32 v194, v194, v236, v244
	v_mul_f32_e32 v190, v190, v236
	v_mov_b32_e32 v199, v190
	v_mov_b32_e32 v177, v194
	v_fma_f32 v194, v194, v237, v245
	v_mul_f32_e32 v190, v190, v237
	v_mov_b32_e32 v200, v190
	v_mov_b32_e32 v203, v194
	v_fma_f32 v194, v194, v238, v246
	v_mul_f32_e32 v190, v190, v238
	v_mov_b32_e32 v191, v194
	ds_write_b64 v207, v[190:191] offset:1024
	s_waitcnt vmcnt(0)
	s_waitcnt lgkmcnt(0)
	s_barrier
	s_cmp_gt_u32 s13, 15
	s_cbranch_scc1 .Lmylru_nodma_2
	s_add_i32 s58, s13, 2
	s_cmp_lt_u32 s58, 2
	s_lshl_b32 s50, s58, 7
	s_lshl_b32 s51, s9, 8
	s_add_i32 s51, s51, 0x8000
	s_add_i32 s51, s51, s50
	s_lshl_b32 s59, s9, 11
	s_add_i32 s59, s59, s50
	s_addk_i32 s59, 0xff00
	s_cmp_lt_u32 s58, 2
	s_cselect_b32 s59, s51, s59
	s_lshl_b32 s52, s59, 11
	s_add_u32 s46, s16, s52
	s_addc_u32 s47, s17, 0
	s_lshl_b32 s52, s6, 13
	s_add_i32 s52, s52, 0x10000
	s_mov_b32 m0, s52
	s_add_i32 s52, s52, 0x400
	global_load_lds_dwordx4 v211, s[46:47]
	s_mov_b32 m0, s52
	s_add_i32 s52, s52, 0x400
	global_load_lds_dwordx4 v212, s[46:47]
	s_mov_b32 m0, s52
	s_add_i32 s52, s52, 0x400
	global_load_lds_dwordx4 v213, s[46:47]
	s_mov_b32 m0, s52
	s_add_i32 s52, s52, 0x400
	global_load_lds_dwordx4 v214, s[46:47]
	s_mov_b32 m0, s52
	s_add_i32 s52, s52, 0x400
	global_load_lds_dwordx4 v215, s[46:47]
	s_mov_b32 m0, s52
	s_add_i32 s52, s52, 0x400
	global_load_lds_dwordx4 v216, s[46:47]
	s_mov_b32 m0, s52
	s_add_i32 s52, s52, 0x400
	global_load_lds_dwordx4 v217, s[46:47]
	s_mov_b32 m0, s52
	s_nop 0
	global_load_lds_dwordx4 v218, s[46:47]
.Lmylru_nodma_2:
	ds_read_b64 v[178:179], v208 offset:1024
	ds_read_b64 v[180:181], v208 offset:1536
	s_waitcnt lgkmcnt(0)
	v_fma_f32 v182, v176, v178, v179
	v_cndmask_b32_e64 v183, v176, v182, s[38:39]
	v_fma_f32 v176, v182, v180, v181
	s_add_i32 s13, s13, 1
	s_mov_b32 s60, 8
.Lmylru_loop_0:
	s_add_i32 s54, s13, -2
	s_lshl_b32 s55, s54, 14
	s_lshl_b32 s56, s6, 11
	s_add_i32 s55, s55, s56
	s_add_u32 s44, s22, s55
	s_addc_u32 s45, s23, 0
	v_mov_b32_e32 v163, v162
	ds_read_b128 v[96:99], v163
	ds_read_b128 v[100:103], v163 offset:8192
	ds_read_b128 v[104:107], v163 offset:16384
	ds_read_b128 v[108:111], v163 offset:24576
	v_xor_b32_e32 v164, 0x40, v163
	ds_read_b128 v[112:115], v164
	ds_read_b128 v[116:119], v164 offset:8192
	ds_read_b128 v[120:123], v164 offset:16384
	ds_read_b128 v[124:127], v164 offset:24576
	s_waitcnt lgkmcnt(7)
	v_mfma_f32_16x16x32_bf16 v[64:67], v[96:99], v[0:3], 0
	v_mfma_f32_16x16x32_bf16 v[68:71], v[96:99], v[32:35], 0
	v_xor_b32_e32 v164, 0x80, v163
	ds_read_b128 v[96:99], v164
	s_waitcnt lgkmcnt(7)
	v_mfma_f32_16x16x32_bf16 v[72:75], v[100:103], v[0:3], 0
	v_mfma_f32_16x16x32_bf16 v[76:79], v[100:103], v[32:35], 0
	ds_read_b128 v[100:103], v164 offset:8192
	s_waitcnt lgkmcnt(7)
	v_mfma_f32_16x16x32_bf16 v[80:83], v[104:107], v[0:3], 0
	v_mfma_f32_16x16x32_bf16 v[84:87], v[104:107], v[32:35], 0
	ds_read_b128 v[104:107], v164 offset:16384
	s_waitcnt lgkmcnt(7)
	v_mfma_f32_16x16x32_bf16 v[88:91], v[108:111], v[0:3], 0
	v_mfma_f32_16x16x32_bf16 v[92:95], v[108:111], v[32:35], 0
	ds_read_b128 v[108:111], v164 offset:24576
	s_waitcnt lgkmcnt(7)
	v_mfma_f32_16x16x32_bf16 v[64:67], v[112:115], v[4:7], v[64:67]
	v_mfma_f32_16x16x32_bf16 v[68:71], v[112:115], v[36:39], v[68:71]
	v_xor_b32_e32 v164, 0xc0, v163
	ds_read_b128 v[112:115], v164
	s_waitcnt lgkmcnt(7)
	v_mfma_f32_16x16x32_bf16 v[72:75], v[116:119], v[4:7], v[72:75]
	v_mfma_f32_16x16x32_bf16 v[76:79], v[116:119], v[36:39], v[76:79]
	ds_read_b128 v[116:119], v164 offset:8192
	s_waitcnt lgkmcnt(7)
	v_mfma_f32_16x16x32_bf16 v[80:83], v[120:123], v[4:7], v[80:83]
	v_mfma_f32_16x16x32_bf16 v[84:87], v[120:123], v[36:39], v[84:87]
	ds_read_b128 v[120:123], v164 offset:16384
	s_waitcnt lgkmcnt(7)
	v_mfma_f32_16x16x32_bf16 v[88:91], v[124:127], v[4:7], v[88:91]
	v_mfma_f32_16x16x32_bf16 v[92:95], v[124:127], v[36:39], v[92:95]
	ds_read_b128 v[124:127], v164 offset:24576
	s_waitcnt lgkmcnt(7)
	v_mfma_f32_16x16x32_bf16 v[64:67], v[96:99], v[8:11], v[64:67]
	v_mfma_f32_16x16x32_bf16 v[68:71], v[96:99], v[40:43], v[68:71]
	v_xor_b32_e32 v164, 0x100, v163
	ds_read_b128 v[96:99], v164
	s_waitcnt lgkmcnt(7)
	v_mfma_f32_16x16x32_bf16 v[72:75], v[100:103], v[8:11], v[72:75]
	v_mfma_f32_16x16x32_bf16 v[76:79], v[100:103], v[40:43], v[76:79]
	ds_read_b128 v[100:103], v164 offset:8192
	s_waitcnt lgkmcnt(7)
	v_mfma_f32_16x16x32_bf16 v[80:83], v[104:107], v[8:11], v[80:83]
	v_mfma_f32_16x16x32_bf16 v[84:87], v[104:107], v[40:43], v[84:87]
	ds_read_b128 v[104:107], v164 offset:16384
	s_waitcnt lgkmcnt(7)
	v_mfma_f32_16x16x32_bf16 v[88:91], v[108:111], v[8:11], v[88:91]
	v_mfma_f32_16x16x32_bf16 v[92:95], v[108:111], v[40:43], v[92:95]
	ds_read_b128 v[108:111], v164 offset:24576
	s_waitcnt lgkmcnt(7)
	v_mfma_f32_16x16x32_bf16 v[64:67], v[112:115], v[12:15], v[64:67]
	v_mfma_f32_16x16x32_bf16 v[68:71], v[112:115], v[44:47], v[68:71]
	v_xor_b32_e32 v164, 0x140, v163
	ds_read_b128 v[112:115], v164
	s_waitcnt lgkmcnt(7)
	v_mfma_f32_16x16x32_bf16 v[72:75], v[116:119], v[12:15], v[72:75]
	v_mfma_f32_16x16x32_bf16 v[76:79], v[116:119], v[44:47], v[76:79]
	ds_read_b128 v[116:119], v164 offset:8192
	s_waitcnt lgkmcnt(7)
	v_mfma_f32_16x16x32_bf16 v[80:83], v[120:123], v[12:15], v[80:83]
	v_mfma_f32_16x16x32_bf16 v[84:87], v[120:123], v[44:47], v[84:87]
	ds_read_b128 v[120:123], v164 offset:16384
	s_waitcnt lgkmcnt(7)
	v_mfma_f32_16x16x32_bf16 v[88:91], v[124:127], v[12:15], v[88:91]
	v_mfma_f32_16x16x32_bf16 v[92:95], v[124:127], v[44:47], v[92:95]
	ds_read_b128 v[124:127], v164 offset:24576
	s_waitcnt lgkmcnt(7)
	v_mfma_f32_16x16x32_bf16 v[64:67], v[96:99], v[16:19], v[64:67]
	v_mfma_f32_16x16x32_bf16 v[68:71], v[96:99], v[48:51], v[68:71]
	v_xor_b32_e32 v164, 0x180, v163
	ds_read_b128 v[96:99], v164
	s_waitcnt lgkmcnt(7)
	v_mfma_f32_16x16x32_bf16 v[72:75], v[100:103], v[16:19], v[72:75]
	v_mfma_f32_16x16x32_bf16 v[76:79], v[100:103], v[48:51], v[76:79]
	ds_read_b128 v[100:103], v164 offset:8192
	s_waitcnt lgkmcnt(7)
	v_mfma_f32_16x16x32_bf16 v[80:83], v[104:107], v[16:19], v[80:83]
	v_mfma_f32_16x16x32_bf16 v[84:87], v[104:107], v[48:51], v[84:87]
	ds_read_b128 v[104:107], v164 offset:16384
	s_waitcnt lgkmcnt(7)
	v_mfma_f32_16x16x32_bf16 v[88:91], v[108:111], v[16:19], v[88:91]
	v_mfma_f32_16x16x32_bf16 v[92:95], v[108:111], v[48:51], v[92:95]
	ds_read_b128 v[108:111], v164 offset:24576
	s_waitcnt lgkmcnt(7)
	v_mfma_f32_16x16x32_bf16 v[64:67], v[112:115], v[20:23], v[64:67]
	v_mfma_f32_16x16x32_bf16 v[68:71], v[112:115], v[52:55], v[68:71]
	v_xor_b32_e32 v164, 0x1c0, v163
	ds_read_b128 v[112:115], v164
	s_waitcnt lgkmcnt(7)
	v_mfma_f32_16x16x32_bf16 v[72:75], v[116:119], v[20:23], v[72:75]
	v_mfma_f32_16x16x32_bf16 v[76:79], v[116:119], v[52:55], v[76:79]
	ds_read_b128 v[116:119], v164 offset:8192
	s_waitcnt lgkmcnt(7)
	v_mfma_f32_16x16x32_bf16 v[80:83], v[120:123], v[20:23], v[80:83]
	v_mfma_f32_16x16x32_bf16 v[84:87], v[120:123], v[52:55], v[84:87]
	ds_read_b128 v[120:123], v164 offset:16384
	s_waitcnt lgkmcnt(7)
	v_mfma_f32_16x16x32_bf16 v[88:91], v[124:127], v[20:23], v[88:91]
	v_mfma_f32_16x16x32_bf16 v[92:95], v[124:127], v[52:55], v[92:95]
	ds_read_b128 v[124:127], v164 offset:24576
	s_waitcnt lgkmcnt(7)
	v_mfma_f32_16x16x32_bf16 v[64:67], v[96:99], v[24:27], v[64:67]
	v_mfma_f32_16x16x32_bf16 v[68:71], v[96:99], v[56:59], v[68:71]
	s_waitcnt lgkmcnt(6)
	v_mfma_f32_16x16x32_bf16 v[72:75], v[100:103], v[24:27], v[72:75]
	v_mfma_f32_16x16x32_bf16 v[76:79], v[100:103], v[56:59], v[76:79]
	s_waitcnt lgkmcnt(5)
	v_mfma_f32_16x16x32_bf16 v[80:83], v[104:107], v[24:27], v[80:83]
	v_mfma_f32_16x16x32_bf16 v[84:87], v[104:107], v[56:59], v[84:87]
	s_waitcnt lgkmcnt(4)
	v_mfma_f32_16x16x32_bf16 v[88:91], v[108:111], v[24:27], v[88:91]
	v_mfma_f32_16x16x32_bf16 v[92:95], v[108:111], v[56:59], v[92:95]
	s_waitcnt lgkmcnt(3)
	v_mfma_f32_16x16x32_bf16 v[64:67], v[112:115], v[28:31], v[64:67]
	v_mfma_f32_16x16x32_bf16 v[68:71], v[112:115], v[60:63], v[68:71]
	s_waitcnt lgkmcnt(2)
	v_mfma_f32_16x16x32_bf16 v[72:75], v[116:119], v[28:31], v[72:75]
	v_mfma_f32_16x16x32_bf16 v[76:79], v[116:119], v[60:63], v[76:79]
	s_waitcnt lgkmcnt(1)
	v_mfma_f32_16x16x32_bf16 v[80:83], v[120:123], v[28:31], v[80:83]
	v_mfma_f32_16x16x32_bf16 v[84:87], v[120:123], v[60:63], v[84:87]
	s_waitcnt lgkmcnt(0)
	v_mfma_f32_16x16x32_bf16 v[88:91], v[124:127], v[28:31], v[88:91]
	v_mfma_f32_16x16x32_bf16 v[92:95], v[124:127], v[60:63], v[92:95]
	v_mov_b32_e32 v169, v165
	v_mov_b32_e32 v170, v166
	v_mov_b32_e32 v171, v167
	v_mov_b32_e32 v172, v168
	ds_read_u16 v144, v169
	ds_read_u16 v145, v170
	ds_read_u16 v146, v171
	ds_read_u16 v147, v172
	ds_read_u16 v148, v169 offset:8192
	ds_read_u16 v149, v170 offset:8192
	ds_read_u16 v150, v171 offset:8192
	ds_read_u16 v151, v172 offset:8192
	ds_read_u16 v152, v169 offset:16384
	ds_read_u16 v153, v170 offset:16384
	ds_read_u16 v154, v171 offset:16384
	ds_read_u16 v155, v172 offset:16384
	ds_read_u16 v156, v169 offset:24576
	ds_read_u16 v157, v170 offset:24576
	ds_read_u16 v158, v171 offset:24576
	ds_read_u16 v159, v172 offset:24576
	s_nop 7
	v_fma_f32 v178, v64, s53, v173
	v_fma_f32 v179, v65, s53, v173
	v_fma_f32 v180, v66, s53, v173
	v_fma_f32 v181, v67, s53, v173
	v_fma_f32 v182, v72, s53, v173
	v_fma_f32 v183, v73, s53, v173
	v_fma_f32 v184, v74, s53, v173
	v_fma_f32 v185, v75, s53, v173
	v_fma_f32 v186, v68, s53, v174
	v_fma_f32 v187, v69, s53, v174
	v_fma_f32 v188, v70, s53, v174
	v_fma_f32 v189, v71, s53, v174
	v_fma_f32 v190, v76, s53, v174
	v_fma_f32 v191, v77, s53, v174
	v_fma_f32 v192, v78, s53, v174
	v_fma_f32 v193, v79, s53, v174
	v_exp_f32_e32 v178, v178
	v_exp_f32_e32 v179, v179
	v_exp_f32_e32 v180, v180
	v_exp_f32_e32 v181, v181
	v_exp_f32_e32 v182, v182
	v_exp_f32_e32 v183, v183
	v_exp_f32_e32 v184, v184
	v_exp_f32_e32 v185, v185
	v_exp_f32_e32 v186, v186
	v_exp_f32_e32 v187, v187
	v_exp_f32_e32 v188, v188
	v_exp_f32_e32 v189, v189
	v_exp_f32_e32 v190, v190
	v_exp_f32_e32 v191, v191
	v_exp_f32_e32 v192, v192
	v_exp_f32_e32 v193, v193
	v_add_f32_e32 v178, 1.0, v178
	v_add_f32_e32 v179, 1.0, v179
	v_add_f32_e32 v180, 1.0, v180
	v_add_f32_e32 v181, 1.0, v181
	v_add_f32_e32 v182, 1.0, v182
	v_add_f32_e32 v183, 1.0, v183
	v_add_f32_e32 v184, 1.0, v184
	v_add_f32_e32 v185, 1.0, v185
	v_add_f32_e32 v186, 1.0, v186
	v_add_f32_e32 v187, 1.0, v187
	v_add_f32_e32 v188, 1.0, v188
	v_add_f32_e32 v189, 1.0, v189
	v_add_f32_e32 v190, 1.0, v190
	v_add_f32_e32 v191, 1.0, v191
	v_add_f32_e32 v192, 1.0, v192
	v_add_f32_e32 v193, 1.0, v193
	v_rcp_f32_e32 v178, v178
	v_rcp_f32_e32 v179, v179
	v_rcp_f32_e32 v180, v180
	v_rcp_f32_e32 v181, v181
	v_rcp_f32_e32 v182, v182
	v_rcp_f32_e32 v183, v183
	v_rcp_f32_e32 v184, v184
	v_rcp_f32_e32 v185, v185
	v_rcp_f32_e32 v186, v186
	v_rcp_f32_e32 v187, v187
	v_rcp_f32_e32 v188, v188
	v_rcp_f32_e32 v189, v189
	v_rcp_f32_e32 v190, v190
	v_rcp_f32_e32 v191, v191
	v_rcp_f32_e32 v192, v192
	v_rcp_f32_e32 v193, v193
	v_mul_f32_e32 v178, v175, v178
	v_mul_f32_e32 v179, v175, v179
	v_mul_f32_e32 v180, v175, v180
	v_mul_f32_e32 v181, v175, v181
	v_mul_f32_e32 v182, v175, v182
	v_mul_f32_e32 v183, v175, v183
	v_mul_f32_e32 v184, v175, v184
	v_mul_f32_e32 v185, v175, v185
	v_exp_f32_e32 v96, v178
	v_exp_f32_e32 v97, v179
	v_exp_f32_e32 v98, v180
	v_exp_f32_e32 v99, v181
	v_exp_f32_e32 v100, v182
	v_exp_f32_e32 v101, v183
	v_exp_f32_e32 v102, v184
	v_exp_f32_e32 v103, v185
	s_nop 0
	v_fma_f32 v194, -v96, v96, 1.0
	v_fma_f32 v195, -v97, v97, 1.0
	v_fma_f32 v196, -v98, v98, 1.0
	v_fma_f32 v197, -v99, v99, 1.0
	v_fma_f32 v198, -v100, v100, 1.0
	v_fma_f32 v199, -v101, v101, 1.0
	v_fma_f32 v200, -v102, v102, 1.0
	v_fma_f32 v201, -v103, v103, 1.0
	v_max_f32_e32 v194, 0, v194
	v_max_f32_e32 v195, 0, v195
	v_max_f32_e32 v196, 0, v196
	v_max_f32_e32 v197, 0, v197
	v_max_f32_e32 v198, 0, v198
	v_max_f32_e32 v199, 0, v199
	v_max_f32_e32 v200, 0, v200
	v_max_f32_e32 v201, 0, v201
	v_sqrt_f32_e32 v194, v194
	v_sqrt_f32_e32 v195, v195
	v_sqrt_f32_e32 v196, v196
	v_sqrt_f32_e32 v197, v197
	v_sqrt_f32_e32 v198, v198
	v_sqrt_f32_e32 v199, v199
	v_sqrt_f32_e32 v200, v200
	v_sqrt_f32_e32 v201, v201
	s_waitcnt lgkmcnt(8)
	v_lshlrev_b32_e32 v144, 16, v144
	v_lshlrev_b32_e32 v145, 16, v145
	v_lshlrev_b32_e32 v146, 16, v146
	v_lshlrev_b32_e32 v147, 16, v147
	v_lshlrev_b32_e32 v148, 16, v148
	v_lshlrev_b32_e32 v149, 16, v149
	v_lshlrev_b32_e32 v150, 16, v150
	v_lshlrev_b32_e32 v151, 16, v151
	v_mul_f32_e32 v194, v194, v186
	v_mul_f32_e32 v195, v195, v187
	v_mul_f32_e32 v196, v196, v188
	v_mul_f32_e32 v197, v197, v189
	v_mul_f32_e32 v198, v198, v190
	v_mul_f32_e32 v199, v199, v191
	v_mul_f32_e32 v200, v200, v192
	v_mul_f32_e32 v201, v201, v193
	v_mul_f32_e32 v144, v194, v144
	v_mul_f32_e32 v145, v195, v145
	v_mul_f32_e32 v146, v196, v146
	v_mul_f32_e32 v147, v197, v147
	v_mul_f32_e32 v148, v198, v148
	v_mul_f32_e32 v149, v199, v149
	v_mul_f32_e32 v150, v200, v150
	v_mul_f32_e32 v151, v201, v151
	v_fma_f32 v178, v80, s53, v173
	v_fma_f32 v179, v81, s53, v173
	v_fma_f32 v180, v82, s53, v173
	v_fma_f32 v181, v83, s53, v173
	v_fma_f32 v182, v88, s53, v173
	v_fma_f32 v183, v89, s53, v173
	v_fma_f32 v184, v90, s53, v173
	v_fma_f32 v185, v91, s53, v173
	v_fma_f32 v186, v84, s53, v174
	v_fma_f32 v187, v85, s53, v174
	v_fma_f32 v188, v86, s53, v174
	v_fma_f32 v189, v87, s53, v174
	v_fma_f32 v190, v92, s53, v174
	v_fma_f32 v191, v93, s53, v174
	v_fma_f32 v192, v94, s53, v174
	v_fma_f32 v193, v95, s53, v174
	v_exp_f32_e32 v178, v178
	v_exp_f32_e32 v179, v179
	v_exp_f32_e32 v180, v180
	v_exp_f32_e32 v181, v181
	v_exp_f32_e32 v182, v182
	v_exp_f32_e32 v183, v183
	v_exp_f32_e32 v184, v184
	v_exp_f32_e32 v185, v185
	v_exp_f32_e32 v186, v186
	v_exp_f32_e32 v187, v187
	v_exp_f32_e32 v188, v188
	v_exp_f32_e32 v189, v189
	v_exp_f32_e32 v190, v190
	v_exp_f32_e32 v191, v191
	v_exp_f32_e32 v192, v192
	v_exp_f32_e32 v193, v193
	v_add_f32_e32 v178, 1.0, v178
	v_add_f32_e32 v179, 1.0, v179
	v_add_f32_e32 v180, 1.0, v180
	v_add_f32_e32 v181, 1.0, v181
	v_add_f32_e32 v182, 1.0, v182
	v_add_f32_e32 v183, 1.0, v183
	v_add_f32_e32 v184, 1.0, v184
	v_add_f32_e32 v185, 1.0, v185
	v_add_f32_e32 v186, 1.0, v186
	v_add_f32_e32 v187, 1.0, v187
	v_add_f32_e32 v188, 1.0, v188
	v_add_f32_e32 v189, 1.0, v189
	v_add_f32_e32 v190, 1.0, v190
	v_add_f32_e32 v191, 1.0, v191
	v_add_f32_e32 v192, 1.0, v192
	v_add_f32_e32 v193, 1.0, v193
	v_rcp_f32_e32 v178, v178
	v_rcp_f32_e32 v179, v179
	v_rcp_f32_e32 v180, v180
	v_rcp_f32_e32 v181, v181
	v_rcp_f32_e32 v182, v182
	v_rcp_f32_e32 v183, v183
	v_rcp_f32_e32 v184, v184
	v_rcp_f32_e32 v185, v185
	v_rcp_f32_e32 v186, v186
	v_rcp_f32_e32 v187, v187
	v_rcp_f32_e32 v188, v188
	v_rcp_f32_e32 v189, v189
	v_rcp_f32_e32 v190, v190
	v_rcp_f32_e32 v191, v191
	v_rcp_f32_e32 v192, v192
	v_rcp_f32_e32 v193, v193
	v_mul_f32_e32 v178, v175, v178
	v_mul_f32_e32 v179, v175, v179
	v_mul_f32_e32 v180, v175, v180
	v_mul_f32_e32 v181, v175, v181
	v_mul_f32_e32 v182, v175, v182
	v_mul_f32_e32 v183, v175, v183
	v_mul_f32_e32 v184, v175, v184
	v_mul_f32_e32 v185, v175, v185
	v_exp_f32_e32 v104, v178
	v_exp_f32_e32 v105, v179
	v_exp_f32_e32 v106, v180
	v_exp_f32_e32 v107, v181
	v_exp_f32_e32 v108, v182
	v_exp_f32_e32 v109, v183
	v_exp_f32_e32 v110, v184
	v_exp_f32_e32 v111, v185
	s_nop 0
	v_fma_f32 v194, -v104, v104, 1.0
	v_fma_f32 v195, -v105, v105, 1.0
	v_fma_f32 v196, -v106, v106, 1.0
	v_fma_f32 v197, -v107, v107, 1.0
	v_fma_f32 v198, -v108, v108, 1.0
	v_fma_f32 v199, -v109, v109, 1.0
	v_fma_f32 v200, -v110, v110, 1.0
	v_fma_f32 v201, -v111, v111, 1.0
	v_max_f32_e32 v194, 0, v194
	v_max_f32_e32 v195, 0, v195
	v_max_f32_e32 v196, 0, v196
	v_max_f32_e32 v197, 0, v197
	v_max_f32_e32 v198, 0, v198
	v_max_f32_e32 v199, 0, v199
	v_max_f32_e32 v200, 0, v200
	v_max_f32_e32 v201, 0, v201
	v_sqrt_f32_e32 v194, v194
	v_sqrt_f32_e32 v195, v195
	v_sqrt_f32_e32 v196, v196
	v_sqrt_f32_e32 v197, v197
	v_sqrt_f32_e32 v198, v198
	v_sqrt_f32_e32 v199, v199
	v_sqrt_f32_e32 v200, v200
	v_sqrt_f32_e32 v201, v201
	s_waitcnt lgkmcnt(0)
	v_lshlrev_b32_e32 v152, 16, v152
	v_lshlrev_b32_e32 v153, 16, v153
	v_lshlrev_b32_e32 v154, 16, v154
	v_lshlrev_b32_e32 v155, 16, v155
	v_lshlrev_b32_e32 v156, 16, v156
	v_lshlrev_b32_e32 v157, 16, v157
	v_lshlrev_b32_e32 v158, 16, v158
	v_lshlrev_b32_e32 v159, 16, v159
	v_mul_f32_e32 v194, v194, v186
	v_mul_f32_e32 v195, v195, v187
	v_mul_f32_e32 v196, v196, v188
	v_mul_f32_e32 v197, v197, v189
	v_mul_f32_e32 v198, v198, v190
	v_mul_f32_e32 v199, v199, v191
	v_mul_f32_e32 v200, v200, v192
	v_mul_f32_e32 v201, v201, v193
	v_mul_f32_e32 v152, v194, v152
	v_mul_f32_e32 v153, v195, v153
	v_mul_f32_e32 v154, v196, v154
	v_mul_f32_e32 v155, v197, v155
	v_mul_f32_e32 v156, v198, v156
	v_mul_f32_e32 v157, v199, v157
	v_mul_f32_e32 v158, v200, v158
	v_mul_f32_e32 v159, v201, v159
	v_fma_f32 v145, v97, v144, v145
	v_fma_f32 v149, v101, v148, v149
	v_fma_f32 v153, v105, v152, v153
	v_fma_f32 v157, v109, v156, v157
	v_mul_f32_e32 v97, v97, v96
	v_mul_f32_e32 v101, v101, v100
	v_mul_f32_e32 v105, v105, v104
	v_mul_f32_e32 v109, v109, v108
	v_fma_f32 v146, v98, v145, v146
	v_fma_f32 v150, v102, v149, v150
	v_fma_f32 v154, v106, v153, v154
	v_fma_f32 v158, v110, v157, v158
	v_mul_f32_e32 v98, v98, v97
	v_mul_f32_e32 v102, v102, v101
	v_mul_f32_e32 v106, v106, v105
	v_mul_f32_e32 v110, v110, v109
	v_fma_f32 v147, v99, v146, v147
	v_fma_f32 v151, v103, v150, v151
	v_fma_f32 v155, v107, v154, v155
	v_fma_f32 v159, v111, v158, v159
	v_mul_f32_e32 v99, v99, v98
	v_mul_f32_e32 v103, v103, v102
	v_mul_f32_e32 v107, v107, v106
	v_mul_f32_e32 v111, v111, v110
	ds_bpermute_b32 v178, v204, v99
	ds_bpermute_b32 v182, v204, v147
	ds_bpermute_b32 v179, v204, v103
	ds_bpermute_b32 v183, v204, v151
	ds_bpermute_b32 v180, v204, v107
	ds_bpermute_b32 v184, v204, v155
	ds_bpermute_b32 v181, v204, v111
	ds_bpermute_b32 v185, v204, v159
	s_waitcnt lgkmcnt(0)
	v_fma_f32 v186, v182, v99, v147
	v_cndmask_b32_e64 v178, 1.0, v178, s[34:35]
	v_fma_f32 v187, v183, v103, v151
	v_cndmask_b32_e64 v179, 1.0, v179, s[34:35]
	v_fma_f32 v188, v184, v107, v155
	v_cndmask_b32_e64 v180, 1.0, v180, s[34:35]
	v_fma_f32 v189, v185, v111, v159
	v_cndmask_b32_e64 v181, 1.0, v181, s[34:35]
	v_cndmask_b32_e64 v223, v147, v186, s[34:35]
	v_mul_f32_e32 v219, v99, v178
	v_cndmask_b32_e64 v224, v151, v187, s[34:35]
	v_mul_f32_e32 v220, v103, v179
	v_cndmask_b32_e64 v225, v155, v188, s[34:35]
	v_mul_f32_e32 v221, v107, v180
	v_cndmask_b32_e64 v226, v159, v189, s[34:35]
	v_mul_f32_e32 v222, v111, v181
	ds_bpermute_b32 v178, v205, v219
	ds_bpermute_b32 v182, v205, v223
	ds_bpermute_b32 v179, v205, v220
	ds_bpermute_b32 v183, v205, v224
	ds_bpermute_b32 v180, v205, v221
	ds_bpermute_b32 v184, v205, v225
	ds_bpermute_b32 v181, v205, v222
	ds_bpermute_b32 v185, v205, v226
	s_waitcnt lgkmcnt(0)
	v_fma_f32 v186, v182, v219, v223
	v_cndmask_b32_e64 v178, 1.0, v178, s[36:37]
	v_fma_f32 v187, v183, v220, v224
	v_cndmask_b32_e64 v179, 1.0, v179, s[36:37]
	v_fma_f32 v188, v184, v221, v225
	v_cndmask_b32_e64 v180, 1.0, v180, s[36:37]
	v_fma_f32 v189, v185, v222, v226
	v_cndmask_b32_e64 v181, 1.0, v181, s[36:37]
	v_cndmask_b32_e64 v223, v223, v186, s[36:37]
	v_mul_f32_e32 v219, v219, v178
	v_cndmask_b32_e64 v224, v224, v187, s[36:37]
	v_mul_f32_e32 v220, v220, v179
	v_cndmask_b32_e64 v225, v225, v188, s[36:37]
	v_mul_f32_e32 v221, v221, v180
	v_cndmask_b32_e64 v226, v226, v189, s[36:37]
	v_mul_f32_e32 v222, v222, v181
	ds_bpermute_b32 v227, v204, v219
	ds_bpermute_b32 v231, v204, v223
	ds_bpermute_b32 v235, v206, v219
	ds_bpermute_b32 v239, v206, v223
	ds_bpermute_b32 v228, v204, v220
	ds_bpermute_b32 v232, v204, v224
	ds_bpermute_b32 v236, v206, v220
	ds_bpermute_b32 v244, v206, v224
	ds_bpermute_b32 v229, v204, v221
	ds_bpermute_b32 v233, v204, v225
	ds_bpermute_b32 v237, v206, v221
	ds_bpermute_b32 v245, v206, v225
	ds_bpermute_b32 v230, v204, v222
	ds_bpermute_b32 v234, v204, v226
	ds_bpermute_b32 v238, v206, v222
	ds_bpermute_b32 v246, v206, v226
	s_waitcnt lgkmcnt(0)
	v_cndmask_b32_e64 v227, 1.0, v227, s[34:35]
	v_cndmask_b32_e64 v231, 0, v231, s[34:35]
	v_cndmask_b32_e64 v228, 1.0, v228, s[34:35]
	v_cndmask_b32_e64 v232, 0, v232, s[34:35]
	v_cndmask_b32_e64 v229, 1.0, v229, s[34:35]
	v_cndmask_b32_e64 v233, 0, v233, s[34:35]
	v_cndmask_b32_e64 v230, 1.0, v230, s[34:35]
	v_cndmask_b32_e64 v234, 0, v234, s[34:35]
	v_mov_b32_e32 v190, v235
	v_mov_b32_e32 v194, v239
	v_mov_b32_e32 v198, v190
	v_mov_b32_e32 v201, v194
	v_fma_f32 v194, v194, v236, v244
	v_mul_f32_e32 v190, v190, v236
	v_mov_b32_e32 v199, v190
	v_mov_b32_e32 v177, v194
	v_fma_f32 v194, v194, v237, v245
	v_mul_f32_e32 v190, v190, v237
	v_mov_b32_e32 v200, v190
	v_mov_b32_e32 v203, v194
	v_fma_f32 v194, v194, v238, v246
	v_mul_f32_e32 v190, v190, v238
	v_mov_b32_e32 v191, v194
	ds_write_b64 v207, v[190:191]
	s_cmp_eq_u32 s13, 2
	s_cbranch_scc1 .Lmylru_t0_3
	s_waitcnt vmcnt(8)
	s_branch .Lmylru_t1_3

.Lmylru_t1_3:
	s_waitcnt lgkmcnt(0)
	s_barrier
	s_cmp_gt_u32 s13, 15
	s_cbranch_scc1 .Lmylru_nodma_3
	s_add_i32 s58, s13, 2
	s_cmp_lt_u32 s58, 2
	s_lshl_b32 s50, s58, 7
	s_lshl_b32 s51, s9, 8
	s_add_i32 s51, s51, 0x8000
	s_add_i32 s51, s51, s50
	s_lshl_b32 s59, s9, 11
	s_add_i32 s59, s59, s50
	s_addk_i32 s59, 0xff00
	s_cmp_lt_u32 s58, 2
	s_cselect_b32 s59, s51, s59
	s_lshl_b32 s52, s59, 11
	s_add_u32 s46, s16, s52
	s_addc_u32 s47, s17, 0
	s_lshl_b32 s52, s6, 13
	s_mov_b32 m0, s52
	s_add_i32 s52, s52, 0x400
	global_load_lds_dwordx4 v211, s[46:47]
	s_mov_b32 m0, s52
	s_add_i32 s52, s52, 0x400
	global_load_lds_dwordx4 v212, s[46:47]
	s_mov_b32 m0, s52
	s_add_i32 s52, s52, 0x400
	global_load_lds_dwordx4 v213, s[46:47]
	s_mov_b32 m0, s52
	s_add_i32 s52, s52, 0x400
	global_load_lds_dwordx4 v214, s[46:47]
	s_mov_b32 m0, s52
	s_add_i32 s52, s52, 0x400
	global_load_lds_dwordx4 v215, s[46:47]
	s_mov_b32 m0, s52
	s_add_i32 s52, s52, 0x400
	global_load_lds_dwordx4 v216, s[46:47]
	s_mov_b32 m0, s52
	s_add_i32 s52, s52, 0x400
	global_load_lds_dwordx4 v217, s[46:47]
	s_mov_b32 m0, s52
	s_nop 0
	global_load_lds_dwordx4 v218, s[46:47]
.Lmylru_nodma_3:
	ds_read_b64 v[178:179], v208
	ds_read_b64 v[180:181], v208 offset:512
	s_waitcnt lgkmcnt(0)
	v_fma_f32 v182, v176, v178, v179
	v_cndmask_b32_e64 v183, v176, v182, s[38:39]
	v_fma_f32 v176, v182, v180, v181
	v_mov_b32_e32 v184, v183
	v_fma_f32 v185, v183, v198, v201
	v_fma_f32 v186, v183, v199, v177
	v_fma_f32 v187, v183, v200, v203
	v_fma_f32 v184, v184, v227, v231
	v_fma_f32 v185, v185, v228, v232
	v_fma_f32 v186, v186, v229, v233
	v_fma_f32 v187, v187, v230, v234
	v_fma_f32 v144, v184, v96, v144
	v_fma_f32 v148, v185, v100, v148
	v_fma_f32 v152, v186, v104, v152
	v_fma_f32 v156, v187, v108, v156
	v_fma_f32 v145, v184, v97, v145
	v_fma_f32 v149, v185, v101, v149
	v_fma_f32 v153, v186, v105, v153
	v_fma_f32 v157, v187, v109, v157
	v_fma_f32 v146, v184, v98, v146
	v_fma_f32 v150, v185, v102, v150
	v_fma_f32 v154, v186, v106, v154
	v_fma_f32 v158, v187, v110, v158
	v_fma_f32 v147, v184, v99, v147
	v_fma_f32 v151, v185, v103, v151
	v_fma_f32 v155, v186, v107, v155
	v_fma_f32 v159, v187, v111, v159
	v_cvt_pk_bf16_f32 v178, v144, v145
	v_cvt_pk_bf16_f32 v179, v146, v147
	v_cvt_pk_bf16_f32 v180, v148, v149
	v_cvt_pk_bf16_f32 v181, v150, v151
	v_cvt_pk_bf16_f32 v182, v152, v153
	v_cvt_pk_bf16_f32 v183, v154, v155
	v_cvt_pk_bf16_f32 v184, v156, v157
	v_cvt_pk_bf16_f32 v185, v158, v159
	global_store_dword v209, v178, s[44:45]
	global_store_dword v209, v179, s[44:45] offset:256
	global_store_dword v209, v180, s[44:45] offset:512
	global_store_dword v209, v181, s[44:45] offset:768
	global_store_dword v209, v182, s[44:45] offset:1024
	global_store_dword v209, v183, s[44:45] offset:1280
	global_store_dword v209, v184, s[44:45] offset:1536
	global_store_dword v209, v185, s[44:45] offset:1792
	s_add_i32 s13, s13, 1
	s_add_i32 s54, s13, -2
	s_lshl_b32 s55, s54, 14
	s_lshl_b32 s56, s6, 11
	s_add_i32 s55, s55, s56
	s_add_u32 s44, s22, s55
	s_addc_u32 s45, s23, 0
	v_or_b32_e32 v163, 0x10000, v162
	ds_read_b128 v[96:99], v163
	ds_read_b128 v[100:103], v163 offset:8192
	ds_read_b128 v[104:107], v163 offset:16384
	ds_read_b128 v[108:111], v163 offset:24576
	v_xor_b32_e32 v164, 0x40, v163
	ds_read_b128 v[112:115], v164
	ds_read_b128 v[116:119], v164 offset:8192
	ds_read_b128 v[120:123], v164 offset:16384
	ds_read_b128 v[124:127], v164 offset:24576
	s_waitcnt lgkmcnt(7)
	v_mfma_f32_16x16x32_bf16 v[64:67], v[96:99], v[0:3], 0
	v_mfma_f32_16x16x32_bf16 v[68:71], v[96:99], v[32:35], 0
	v_xor_b32_e32 v164, 0x80, v163
	ds_read_b128 v[96:99], v164
	s_waitcnt lgkmcnt(7)
	v_mfma_f32_16x16x32_bf16 v[72:75], v[100:103], v[0:3], 0
	v_mfma_f32_16x16x32_bf16 v[76:79], v[100:103], v[32:35], 0
	ds_read_b128 v[100:103], v164 offset:8192
	s_waitcnt lgkmcnt(7)
	v_mfma_f32_16x16x32_bf16 v[80:83], v[104:107], v[0:3], 0
	v_mfma_f32_16x16x32_bf16 v[84:87], v[104:107], v[32:35], 0
	ds_read_b128 v[104:107], v164 offset:16384
	s_waitcnt lgkmcnt(7)
	v_mfma_f32_16x16x32_bf16 v[88:91], v[108:111], v[0:3], 0
	v_mfma_f32_16x16x32_bf16 v[92:95], v[108:111], v[32:35], 0
	ds_read_b128 v[108:111], v164 offset:24576
	s_waitcnt lgkmcnt(7)
	v_mfma_f32_16x16x32_bf16 v[64:67], v[112:115], v[4:7], v[64:67]
	v_mfma_f32_16x16x32_bf16 v[68:71], v[112:115], v[36:39], v[68:71]
	v_xor_b32_e32 v164, 0xc0, v163
	ds_read_b128 v[112:115], v164
	s_waitcnt lgkmcnt(7)
	v_mfma_f32_16x16x32_bf16 v[72:75], v[116:119], v[4:7], v[72:75]
	v_mfma_f32_16x16x32_bf16 v[76:79], v[116:119], v[36:39], v[76:79]
	ds_read_b128 v[116:119], v164 offset:8192
	s_waitcnt lgkmcnt(7)
	v_mfma_f32_16x16x32_bf16 v[80:83], v[120:123], v[4:7], v[80:83]
	v_mfma_f32_16x16x32_bf16 v[84:87], v[120:123], v[36:39], v[84:87]
	ds_read_b128 v[120:123], v164 offset:16384
	s_waitcnt lgkmcnt(7)
	v_mfma_f32_16x16x32_bf16 v[88:91], v[124:127], v[4:7], v[88:91]
	v_mfma_f32_16x16x32_bf16 v[92:95], v[124:127], v[36:39], v[92:95]
	ds_read_b128 v[124:127], v164 offset:24576
	s_waitcnt lgkmcnt(7)
	v_mfma_f32_16x16x32_bf16 v[64:67], v[96:99], v[8:11], v[64:67]
	v_mfma_f32_16x16x32_bf16 v[68:71], v[96:99], v[40:43], v[68:71]
	v_xor_b32_e32 v164, 0x100, v163
	ds_read_b128 v[96:99], v164
	s_waitcnt lgkmcnt(7)
	v_mfma_f32_16x16x32_bf16 v[72:75], v[100:103], v[8:11], v[72:75]
	v_mfma_f32_16x16x32_bf16 v[76:79], v[100:103], v[40:43], v[76:79]
	ds_read_b128 v[100:103], v164 offset:8192
	s_waitcnt lgkmcnt(7)
	v_mfma_f32_16x16x32_bf16 v[80:83], v[104:107], v[8:11], v[80:83]
	v_mfma_f32_16x16x32_bf16 v[84:87], v[104:107], v[40:43], v[84:87]
	ds_read_b128 v[104:107], v164 offset:16384
	s_waitcnt lgkmcnt(7)
	v_mfma_f32_16x16x32_bf16 v[88:91], v[108:111], v[8:11], v[88:91]
	v_mfma_f32_16x16x32_bf16 v[92:95], v[108:111], v[40:43], v[92:95]
	ds_read_b128 v[108:111], v164 offset:24576
	s_waitcnt lgkmcnt(7)
	v_mfma_f32_16x16x32_bf16 v[64:67], v[112:115], v[12:15], v[64:67]
	v_mfma_f32_16x16x32_bf16 v[68:71], v[112:115], v[44:47], v[68:71]
	v_xor_b32_e32 v164, 0x140, v163
	ds_read_b128 v[112:115], v164
	s_waitcnt lgkmcnt(7)
	v_mfma_f32_16x16x32_bf16 v[72:75], v[116:119], v[12:15], v[72:75]
	v_mfma_f32_16x16x32_bf16 v[76:79], v[116:119], v[44:47], v[76:79]
	ds_read_b128 v[116:119], v164 offset:8192
	s_waitcnt lgkmcnt(7)
	v_mfma_f32_16x16x32_bf16 v[80:83], v[120:123], v[12:15], v[80:83]
	v_mfma_f32_16x16x32_bf16 v[84:87], v[120:123], v[44:47], v[84:87]
	ds_read_b128 v[120:123], v164 offset:16384
	s_waitcnt lgkmcnt(7)
	v_mfma_f32_16x16x32_bf16 v[88:91], v[124:127], v[12:15], v[88:91]
	v_mfma_f32_16x16x32_bf16 v[92:95], v[124:127], v[44:47], v[92:95]
	ds_read_b128 v[124:127], v164 offset:24576
	s_waitcnt lgkmcnt(7)
	v_mfma_f32_16x16x32_bf16 v[64:67], v[96:99], v[16:19], v[64:67]
	v_mfma_f32_16x16x32_bf16 v[68:71], v[96:99], v[48:51], v[68:71]
	v_xor_b32_e32 v164, 0x180, v163
	ds_read_b128 v[96:99], v164
	s_waitcnt lgkmcnt(7)
	v_mfma_f32_16x16x32_bf16 v[72:75], v[100:103], v[16:19], v[72:75]
	v_mfma_f32_16x16x32_bf16 v[76:79], v[100:103], v[48:51], v[76:79]
	ds_read_b128 v[100:103], v164 offset:8192
	s_waitcnt lgkmcnt(7)
	v_mfma_f32_16x16x32_bf16 v[80:83], v[104:107], v[16:19], v[80:83]
	v_mfma_f32_16x16x32_bf16 v[84:87], v[104:107], v[48:51], v[84:87]
	ds_read_b128 v[104:107], v164 offset:16384
	s_waitcnt lgkmcnt(7)
	v_mfma_f32_16x16x32_bf16 v[88:91], v[108:111], v[16:19], v[88:91]
	v_mfma_f32_16x16x32_bf16 v[92:95], v[108:111], v[48:51], v[92:95]
	ds_read_b128 v[108:111], v164 offset:24576
	s_waitcnt lgkmcnt(7)
	v_mfma_f32_16x16x32_bf16 v[64:67], v[112:115], v[20:23], v[64:67]
	v_mfma_f32_16x16x32_bf16 v[68:71], v[112:115], v[52:55], v[68:71]
	v_xor_b32_e32 v164, 0x1c0, v163
	ds_read_b128 v[112:115], v164
	s_waitcnt lgkmcnt(7)
	v_mfma_f32_16x16x32_bf16 v[72:75], v[116:119], v[20:23], v[72:75]
	v_mfma_f32_16x16x32_bf16 v[76:79], v[116:119], v[52:55], v[76:79]
	ds_read_b128 v[116:119], v164 offset:8192
	s_waitcnt lgkmcnt(7)
	v_mfma_f32_16x16x32_bf16 v[80:83], v[120:123], v[20:23], v[80:83]
	v_mfma_f32_16x16x32_bf16 v[84:87], v[120:123], v[52:55], v[84:87]
	ds_read_b128 v[120:123], v164 offset:16384
	s_waitcnt lgkmcnt(7)
	v_mfma_f32_16x16x32_bf16 v[88:91], v[124:127], v[20:23], v[88:91]
	v_mfma_f32_16x16x32_bf16 v[92:95], v[124:127], v[52:55], v[92:95]
	ds_read_b128 v[124:127], v164 offset:24576
	s_waitcnt lgkmcnt(7)
	v_mfma_f32_16x16x32_bf16 v[64:67], v[96:99], v[24:27], v[64:67]
	v_mfma_f32_16x16x32_bf16 v[68:71], v[96:99], v[56:59], v[68:71]
	s_waitcnt lgkmcnt(6)
	v_mfma_f32_16x16x32_bf16 v[72:75], v[100:103], v[24:27], v[72:75]
	v_mfma_f32_16x16x32_bf16 v[76:79], v[100:103], v[56:59], v[76:79]
	s_waitcnt lgkmcnt(5)
	v_mfma_f32_16x16x32_bf16 v[80:83], v[104:107], v[24:27], v[80:83]
	v_mfma_f32_16x16x32_bf16 v[84:87], v[104:107], v[56:59], v[84:87]
	s_waitcnt lgkmcnt(4)
	v_mfma_f32_16x16x32_bf16 v[88:91], v[108:111], v[24:27], v[88:91]
	v_mfma_f32_16x16x32_bf16 v[92:95], v[108:111], v[56:59], v[92:95]
	s_waitcnt lgkmcnt(3)
	v_mfma_f32_16x16x32_bf16 v[64:67], v[112:115], v[28:31], v[64:67]
	v_mfma_f32_16x16x32_bf16 v[68:71], v[112:115], v[60:63], v[68:71]
	s_waitcnt lgkmcnt(2)
	v_mfma_f32_16x16x32_bf16 v[72:75], v[116:119], v[28:31], v[72:75]
	v_mfma_f32_16x16x32_bf16 v[76:79], v[116:119], v[60:63], v[76:79]
	s_waitcnt lgkmcnt(1)
	v_mfma_f32_16x16x32_bf16 v[80:83], v[120:123], v[28:31], v[80:83]
	v_mfma_f32_16x16x32_bf16 v[84:87], v[120:123], v[60:63], v[84:87]
	s_waitcnt lgkmcnt(0)
	v_mfma_f32_16x16x32_bf16 v[88:91], v[124:127], v[28:31], v[88:91]
	v_mfma_f32_16x16x32_bf16 v[92:95], v[124:127], v[60:63], v[92:95]
	v_or_b32_e32 v169, 0x10000, v165
	v_or_b32_e32 v170, 0x10000, v166
	v_or_b32_e32 v171, 0x10000, v167
	v_or_b32_e32 v172, 0x10000, v168
	ds_read_u16 v144, v169
	ds_read_u16 v145, v170
	ds_read_u16 v146, v171
	ds_read_u16 v147, v172
	ds_read_u16 v148, v169 offset:8192
	ds_read_u16 v149, v170 offset:8192
	ds_read_u16 v150, v171 offset:8192
	ds_read_u16 v151, v172 offset:8192
	ds_read_u16 v152, v169 offset:16384
	ds_read_u16 v153, v170 offset:16384
	ds_read_u16 v154, v171 offset:16384
	ds_read_u16 v155, v172 offset:16384
	ds_read_u16 v156, v169 offset:24576
	ds_read_u16 v157, v170 offset:24576
	ds_read_u16 v158, v171 offset:24576
	ds_read_u16 v159, v172 offset:24576
	s_nop 7
	v_fma_f32 v178, v64, s53, v173
	v_fma_f32 v179, v65, s53, v173
	v_fma_f32 v180, v66, s53, v173
	v_fma_f32 v181, v67, s53, v173
	v_fma_f32 v182, v72, s53, v173
	v_fma_f32 v183, v73, s53, v173
	v_fma_f32 v184, v74, s53, v173
	v_fma_f32 v185, v75, s53, v173
	v_fma_f32 v186, v68, s53, v174
	v_fma_f32 v187, v69, s53, v174
	v_fma_f32 v188, v70, s53, v174
	v_fma_f32 v189, v71, s53, v174
	v_fma_f32 v190, v76, s53, v174
	v_fma_f32 v191, v77, s53, v174
	v_fma_f32 v192, v78, s53, v174
	v_fma_f32 v193, v79, s53, v174
	v_exp_f32_e32 v178, v178
	v_exp_f32_e32 v179, v179
	v_exp_f32_e32 v180, v180
	v_exp_f32_e32 v181, v181
	v_exp_f32_e32 v182, v182
	v_exp_f32_e32 v183, v183
	v_exp_f32_e32 v184, v184
	v_exp_f32_e32 v185, v185
	v_exp_f32_e32 v186, v186
	v_exp_f32_e32 v187, v187
	v_exp_f32_e32 v188, v188
	v_exp_f32_e32 v189, v189
	v_exp_f32_e32 v190, v190
	v_exp_f32_e32 v191, v191
	v_exp_f32_e32 v192, v192
	v_exp_f32_e32 v193, v193
	v_add_f32_e32 v178, 1.0, v178
	v_add_f32_e32 v179, 1.0, v179
	v_add_f32_e32 v180, 1.0, v180
	v_add_f32_e32 v181, 1.0, v181
	v_add_f32_e32 v182, 1.0, v182
	v_add_f32_e32 v183, 1.0, v183
	v_add_f32_e32 v184, 1.0, v184
	v_add_f32_e32 v185, 1.0, v185
	v_add_f32_e32 v186, 1.0, v186
	v_add_f32_e32 v187, 1.0, v187
	v_add_f32_e32 v188, 1.0, v188
	v_add_f32_e32 v189, 1.0, v189
	v_add_f32_e32 v190, 1.0, v190
	v_add_f32_e32 v191, 1.0, v191
	v_add_f32_e32 v192, 1.0, v192
	v_add_f32_e32 v193, 1.0, v193
	v_rcp_f32_e32 v178, v178
	v_rcp_f32_e32 v179, v179
	v_rcp_f32_e32 v180, v180
	v_rcp_f32_e32 v181, v181
	v_rcp_f32_e32 v182, v182
	v_rcp_f32_e32 v183, v183
	v_rcp_f32_e32 v184, v184
	v_rcp_f32_e32 v185, v185
	v_rcp_f32_e32 v186, v186
	v_rcp_f32_e32 v187, v187
	v_rcp_f32_e32 v188, v188
	v_rcp_f32_e32 v189, v189
	v_rcp_f32_e32 v190, v190
	v_rcp_f32_e32 v191, v191
	v_rcp_f32_e32 v192, v192
	v_rcp_f32_e32 v193, v193
	v_mul_f32_e32 v178, v175, v178
	v_mul_f32_e32 v179, v175, v179
	v_mul_f32_e32 v180, v175, v180
	v_mul_f32_e32 v181, v175, v181
	v_mul_f32_e32 v182, v175, v182
	v_mul_f32_e32 v183, v175, v183
	v_mul_f32_e32 v184, v175, v184
	v_mul_f32_e32 v185, v175, v185
	v_exp_f32_e32 v96, v178
	v_exp_f32_e32 v97, v179
	v_exp_f32_e32 v98, v180
	v_exp_f32_e32 v99, v181
	v_exp_f32_e32 v100, v182
	v_exp_f32_e32 v101, v183
	v_exp_f32_e32 v102, v184
	v_exp_f32_e32 v103, v185
	s_nop 0
	v_fma_f32 v194, -v96, v96, 1.0
	v_fma_f32 v195, -v97, v97, 1.0
	v_fma_f32 v196, -v98, v98, 1.0
	v_fma_f32 v197, -v99, v99, 1.0
	v_fma_f32 v198, -v100, v100, 1.0
	v_fma_f32 v199, -v101, v101, 1.0
	v_fma_f32 v200, -v102, v102, 1.0
	v_fma_f32 v201, -v103, v103, 1.0
	v_max_f32_e32 v194, 0, v194
	v_max_f32_e32 v195, 0, v195
	v_max_f32_e32 v196, 0, v196
	v_max_f32_e32 v197, 0, v197
	v_max_f32_e32 v198, 0, v198
	v_max_f32_e32 v199, 0, v199
	v_max_f32_e32 v200, 0, v200
	v_max_f32_e32 v201, 0, v201
	v_sqrt_f32_e32 v194, v194
	v_sqrt_f32_e32 v195, v195
	v_sqrt_f32_e32 v196, v196
	v_sqrt_f32_e32 v197, v197
	v_sqrt_f32_e32 v198, v198
	v_sqrt_f32_e32 v199, v199
	v_sqrt_f32_e32 v200, v200
	v_sqrt_f32_e32 v201, v201
	s_waitcnt lgkmcnt(8)
	v_lshlrev_b32_e32 v144, 16, v144
	v_lshlrev_b32_e32 v145, 16, v145
	v_lshlrev_b32_e32 v146, 16, v146
	v_lshlrev_b32_e32 v147, 16, v147
	v_lshlrev_b32_e32 v148, 16, v148
	v_lshlrev_b32_e32 v149, 16, v149
	v_lshlrev_b32_e32 v150, 16, v150
	v_lshlrev_b32_e32 v151, 16, v151
	v_mul_f32_e32 v194, v194, v186
	v_mul_f32_e32 v195, v195, v187
	v_mul_f32_e32 v196, v196, v188
	v_mul_f32_e32 v197, v197, v189
	v_mul_f32_e32 v198, v198, v190
	v_mul_f32_e32 v199, v199, v191
	v_mul_f32_e32 v200, v200, v192
	v_mul_f32_e32 v201, v201, v193
	v_mul_f32_e32 v144, v194, v144
	v_mul_f32_e32 v145, v195, v145
	v_mul_f32_e32 v146, v196, v146
	v_mul_f32_e32 v147, v197, v147
	v_mul_f32_e32 v148, v198, v148
	v_mul_f32_e32 v149, v199, v149
	v_mul_f32_e32 v150, v200, v150
	v_mul_f32_e32 v151, v201, v151
	v_fma_f32 v178, v80, s53, v173
	v_fma_f32 v179, v81, s53, v173
	v_fma_f32 v180, v82, s53, v173
	v_fma_f32 v181, v83, s53, v173
	v_fma_f32 v182, v88, s53, v173
	v_fma_f32 v183, v89, s53, v173
	v_fma_f32 v184, v90, s53, v173
	v_fma_f32 v185, v91, s53, v173
	v_fma_f32 v186, v84, s53, v174
	v_fma_f32 v187, v85, s53, v174
	v_fma_f32 v188, v86, s53, v174
	v_fma_f32 v189, v87, s53, v174
	v_fma_f32 v190, v92, s53, v174
	v_fma_f32 v191, v93, s53, v174
	v_fma_f32 v192, v94, s53, v174
	v_fma_f32 v193, v95, s53, v174
	v_exp_f32_e32 v178, v178
	v_exp_f32_e32 v179, v179
	v_exp_f32_e32 v180, v180
	v_exp_f32_e32 v181, v181
	v_exp_f32_e32 v182, v182
	v_exp_f32_e32 v183, v183
	v_exp_f32_e32 v184, v184
	v_exp_f32_e32 v185, v185
	v_exp_f32_e32 v186, v186
	v_exp_f32_e32 v187, v187
	v_exp_f32_e32 v188, v188
	v_exp_f32_e32 v189, v189
	v_exp_f32_e32 v190, v190
	v_exp_f32_e32 v191, v191
	v_exp_f32_e32 v192, v192
	v_exp_f32_e32 v193, v193
	v_add_f32_e32 v178, 1.0, v178
	v_add_f32_e32 v179, 1.0, v179
	v_add_f32_e32 v180, 1.0, v180
	v_add_f32_e32 v181, 1.0, v181
	v_add_f32_e32 v182, 1.0, v182
	v_add_f32_e32 v183, 1.0, v183
	v_add_f32_e32 v184, 1.0, v184
	v_add_f32_e32 v185, 1.0, v185
	v_add_f32_e32 v186, 1.0, v186
	v_add_f32_e32 v187, 1.0, v187
	v_add_f32_e32 v188, 1.0, v188
	v_add_f32_e32 v189, 1.0, v189
	v_add_f32_e32 v190, 1.0, v190
	v_add_f32_e32 v191, 1.0, v191
	v_add_f32_e32 v192, 1.0, v192
	v_add_f32_e32 v193, 1.0, v193
	v_rcp_f32_e32 v178, v178
	v_rcp_f32_e32 v179, v179
	v_rcp_f32_e32 v180, v180
	v_rcp_f32_e32 v181, v181
	v_rcp_f32_e32 v182, v182
	v_rcp_f32_e32 v183, v183
	v_rcp_f32_e32 v184, v184
	v_rcp_f32_e32 v185, v185
	v_rcp_f32_e32 v186, v186
	v_rcp_f32_e32 v187, v187
	v_rcp_f32_e32 v188, v188
	v_rcp_f32_e32 v189, v189
	v_rcp_f32_e32 v190, v190
	v_rcp_f32_e32 v191, v191
	v_rcp_f32_e32 v192, v192
	v_rcp_f32_e32 v193, v193
	v_mul_f32_e32 v178, v175, v178
	v_mul_f32_e32 v179, v175, v179
	v_mul_f32_e32 v180, v175, v180
	v_mul_f32_e32 v181, v175, v181
	v_mul_f32_e32 v182, v175, v182
	v_mul_f32_e32 v183, v175, v183
	v_mul_f32_e32 v184, v175, v184
	v_mul_f32_e32 v185, v175, v185
	v_exp_f32_e32 v104, v178
	v_exp_f32_e32 v105, v179
	v_exp_f32_e32 v106, v180
	v_exp_f32_e32 v107, v181
	v_exp_f32_e32 v108, v182
	v_exp_f32_e32 v109, v183
	v_exp_f32_e32 v110, v184
	v_exp_f32_e32 v111, v185
	s_nop 0
	v_fma_f32 v194, -v104, v104, 1.0
	v_fma_f32 v195, -v105, v105, 1.0
	v_fma_f32 v196, -v106, v106, 1.0
	v_fma_f32 v197, -v107, v107, 1.0
	v_fma_f32 v198, -v108, v108, 1.0
	v_fma_f32 v199, -v109, v109, 1.0
	v_fma_f32 v200, -v110, v110, 1.0
	v_fma_f32 v201, -v111, v111, 1.0
	v_max_f32_e32 v194, 0, v194
	v_max_f32_e32 v195, 0, v195
	v_max_f32_e32 v196, 0, v196
	v_max_f32_e32 v197, 0, v197
	v_max_f32_e32 v198, 0, v198
	v_max_f32_e32 v199, 0, v199
	v_max_f32_e32 v200, 0, v200
	v_max_f32_e32 v201, 0, v201
	v_sqrt_f32_e32 v194, v194
	v_sqrt_f32_e32 v195, v195
	v_sqrt_f32_e32 v196, v196
	v_sqrt_f32_e32 v197, v197
	v_sqrt_f32_e32 v198, v198
	v_sqrt_f32_e32 v199, v199
	v_sqrt_f32_e32 v200, v200
	v_sqrt_f32_e32 v201, v201
	s_waitcnt lgkmcnt(0)
	v_lshlrev_b32_e32 v152, 16, v152
	v_lshlrev_b32_e32 v153, 16, v153
	v_lshlrev_b32_e32 v154, 16, v154
	v_lshlrev_b32_e32 v155, 16, v155
	v_lshlrev_b32_e32 v156, 16, v156
	v_lshlrev_b32_e32 v157, 16, v157
	v_lshlrev_b32_e32 v158, 16, v158
	v_lshlrev_b32_e32 v159, 16, v159
	v_mul_f32_e32 v194, v194, v186
	v_mul_f32_e32 v195, v195, v187
	v_mul_f32_e32 v196, v196, v188
	v_mul_f32_e32 v197, v197, v189
	v_mul_f32_e32 v198, v198, v190
	v_mul_f32_e32 v199, v199, v191
	v_mul_f32_e32 v200, v200, v192
	v_mul_f32_e32 v201, v201, v193
	v_mul_f32_e32 v152, v194, v152
	v_mul_f32_e32 v153, v195, v153
	v_mul_f32_e32 v154, v196, v154
	v_mul_f32_e32 v155, v197, v155
	v_mul_f32_e32 v156, v198, v156
	v_mul_f32_e32 v157, v199, v157
	v_mul_f32_e32 v158, v200, v158
	v_mul_f32_e32 v159, v201, v159
	v_fma_f32 v145, v97, v144, v145
	v_fma_f32 v149, v101, v148, v149
	v_fma_f32 v153, v105, v152, v153
	v_fma_f32 v157, v109, v156, v157
	v_mul_f32_e32 v97, v97, v96
	v_mul_f32_e32 v101, v101, v100
	v_mul_f32_e32 v105, v105, v104
	v_mul_f32_e32 v109, v109, v108
	v_fma_f32 v146, v98, v145, v146
	v_fma_f32 v150, v102, v149, v150
	v_fma_f32 v154, v106, v153, v154
	v_fma_f32 v158, v110, v157, v158
	v_mul_f32_e32 v98, v98, v97
	v_mul_f32_e32 v102, v102, v101
	v_mul_f32_e32 v106, v106, v105
	v_mul_f32_e32 v110, v110, v109
	v_fma_f32 v147, v99, v146, v147
	v_fma_f32 v151, v103, v150, v151
	v_fma_f32 v155, v107, v154, v155
	v_fma_f32 v159, v111, v158, v159
	v_mul_f32_e32 v99, v99, v98
	v_mul_f32_e32 v103, v103, v102
	v_mul_f32_e32 v107, v107, v106
	v_mul_f32_e32 v111, v111, v110
	ds_bpermute_b32 v178, v204, v99
	ds_bpermute_b32 v182, v204, v147
	ds_bpermute_b32 v179, v204, v103
	ds_bpermute_b32 v183, v204, v151
	ds_bpermute_b32 v180, v204, v107
	ds_bpermute_b32 v184, v204, v155
	ds_bpermute_b32 v181, v204, v111
	ds_bpermute_b32 v185, v204, v159
	s_waitcnt lgkmcnt(0)
	v_fma_f32 v186, v182, v99, v147
	v_cndmask_b32_e64 v178, 1.0, v178, s[34:35]
	v_fma_f32 v187, v183, v103, v151
	v_cndmask_b32_e64 v179, 1.0, v179, s[34:35]
	v_fma_f32 v188, v184, v107, v155
	v_cndmask_b32_e64 v180, 1.0, v180, s[34:35]
	v_fma_f32 v189, v185, v111, v159
	v_cndmask_b32_e64 v181, 1.0, v181, s[34:35]
	v_cndmask_b32_e64 v223, v147, v186, s[34:35]
	v_mul_f32_e32 v219, v99, v178
	v_cndmask_b32_e64 v224, v151, v187, s[34:35]
	v_mul_f32_e32 v220, v103, v179
	v_cndmask_b32_e64 v225, v155, v188, s[34:35]
	v_mul_f32_e32 v221, v107, v180
	v_cndmask_b32_e64 v226, v159, v189, s[34:35]
	v_mul_f32_e32 v222, v111, v181
	ds_bpermute_b32 v178, v205, v219
	ds_bpermute_b32 v182, v205, v223
	ds_bpermute_b32 v179, v205, v220
	ds_bpermute_b32 v183, v205, v224
	ds_bpermute_b32 v180, v205, v221
	ds_bpermute_b32 v184, v205, v225
	ds_bpermute_b32 v181, v205, v222
	ds_bpermute_b32 v185, v205, v226
	s_waitcnt lgkmcnt(0)
	v_fma_f32 v186, v182, v219, v223
	v_cndmask_b32_e64 v178, 1.0, v178, s[36:37]
	v_fma_f32 v187, v183, v220, v224
	v_cndmask_b32_e64 v179, 1.0, v179, s[36:37]
	v_fma_f32 v188, v184, v221, v225
	v_cndmask_b32_e64 v180, 1.0, v180, s[36:37]
	v_fma_f32 v189, v185, v222, v226
	v_cndmask_b32_e64 v181, 1.0, v181, s[36:37]
	v_cndmask_b32_e64 v223, v223, v186, s[36:37]
	v_mul_f32_e32 v219, v219, v178
	v_cndmask_b32_e64 v224, v224, v187, s[36:37]
	v_mul_f32_e32 v220, v220, v179
	v_cndmask_b32_e64 v225, v225, v188, s[36:37]
	v_mul_f32_e32 v221, v221, v180
	v_cndmask_b32_e64 v226, v226, v189, s[36:37]
	v_mul_f32_e32 v222, v222, v181
	ds_bpermute_b32 v227, v204, v219
	ds_bpermute_b32 v231, v204, v223
	ds_bpermute_b32 v235, v206, v219
	ds_bpermute_b32 v239, v206, v223
	ds_bpermute_b32 v228, v204, v220
	ds_bpermute_b32 v232, v204, v224
	ds_bpermute_b32 v236, v206, v220
	ds_bpermute_b32 v244, v206, v224
	ds_bpermute_b32 v229, v204, v221
	ds_bpermute_b32 v233, v204, v225
	ds_bpermute_b32 v237, v206, v221
	ds_bpermute_b32 v245, v206, v225
	ds_bpermute_b32 v230, v204, v222
	ds_bpermute_b32 v234, v204, v226
	ds_bpermute_b32 v238, v206, v222
	ds_bpermute_b32 v246, v206, v226
	s_waitcnt lgkmcnt(0)
	v_cndmask_b32_e64 v227, 1.0, v227, s[34:35]
	v_cndmask_b32_e64 v231, 0, v231, s[34:35]
	v_cndmask_b32_e64 v228, 1.0, v228, s[34:35]
	v_cndmask_b32_e64 v232, 0, v232, s[34:35]
	v_cndmask_b32_e64 v229, 1.0, v229, s[34:35]
	v_cndmask_b32_e64 v233, 0, v233, s[34:35]
	v_cndmask_b32_e64 v230, 1.0, v230, s[34:35]
	v_cndmask_b32_e64 v234, 0, v234, s[34:35]
	v_mov_b32_e32 v190, v235
	v_mov_b32_e32 v194, v239
	v_mov_b32_e32 v198, v190
	v_mov_b32_e32 v201, v194
	v_fma_f32 v194, v194, v236, v244
	v_mul_f32_e32 v190, v190, v236
	v_mov_b32_e32 v199, v190
	v_mov_b32_e32 v177, v194
	v_fma_f32 v194, v194, v237, v245
	v_mul_f32_e32 v190, v190, v237
	v_mov_b32_e32 v200, v190
	v_mov_b32_e32 v203, v194
	v_fma_f32 v194, v194, v238, v246
	v_mul_f32_e32 v190, v190, v238
	v_mov_b32_e32 v191, v194
	ds_write_b64 v207, v[190:191] offset:1024
	s_cmp_eq_u32 s13, 2
	s_cbranch_scc1 .Lmylru_t0_4
	s_waitcnt vmcnt(8)
	s_branch .Lmylru_t1_4

.Lmylru_t1_4:
	s_waitcnt lgkmcnt(0)
	s_barrier
	s_cmp_gt_u32 s13, 15
	s_cbranch_scc1 .Lmylru_nodma_4
	s_add_i32 s58, s13, 2
	s_cmp_lt_u32 s58, 2
	s_lshl_b32 s50, s58, 7
	s_lshl_b32 s51, s9, 8
	s_add_i32 s51, s51, 0x8000
	s_add_i32 s51, s51, s50
	s_lshl_b32 s59, s9, 11
	s_add_i32 s59, s59, s50
	s_addk_i32 s59, 0xff00
	s_cmp_lt_u32 s58, 2
	s_cselect_b32 s59, s51, s59
	s_lshl_b32 s52, s59, 11
	s_add_u32 s46, s16, s52
	s_addc_u32 s47, s17, 0
	s_lshl_b32 s52, s6, 13
	s_add_i32 s52, s52, 0x10000
	s_mov_b32 m0, s52
	s_add_i32 s52, s52, 0x400
	global_load_lds_dwordx4 v211, s[46:47]
	s_mov_b32 m0, s52
	s_add_i32 s52, s52, 0x400
	global_load_lds_dwordx4 v212, s[46:47]
	s_mov_b32 m0, s52
	s_add_i32 s52, s52, 0x400
	global_load_lds_dwordx4 v213, s[46:47]
	s_mov_b32 m0, s52
	s_add_i32 s52, s52, 0x400
	global_load_lds_dwordx4 v214, s[46:47]
	s_mov_b32 m0, s52
	s_add_i32 s52, s52, 0x400
	global_load_lds_dwordx4 v215, s[46:47]
	s_mov_b32 m0, s52
	s_add_i32 s52, s52, 0x400
	global_load_lds_dwordx4 v216, s[46:47]
	s_mov_b32 m0, s52
	s_add_i32 s52, s52, 0x400
	global_load_lds_dwordx4 v217, s[46:47]
	s_mov_b32 m0, s52
	s_nop 0
	global_load_lds_dwordx4 v218, s[46:47]
.Lmylru_nodma_4:
	ds_read_b64 v[178:179], v208 offset:1024
	ds_read_b64 v[180:181], v208 offset:1536
	s_waitcnt lgkmcnt(0)
	v_fma_f32 v182, v176, v178, v179
	v_cndmask_b32_e64 v183, v176, v182, s[38:39]
	v_fma_f32 v176, v182, v180, v181
	v_mov_b32_e32 v184, v183
	v_fma_f32 v185, v183, v198, v201
	v_fma_f32 v186, v183, v199, v177
	v_fma_f32 v187, v183, v200, v203
	v_fma_f32 v184, v184, v227, v231
	v_fma_f32 v185, v185, v228, v232
	v_fma_f32 v186, v186, v229, v233
	v_fma_f32 v187, v187, v230, v234
	v_fma_f32 v144, v184, v96, v144
	v_fma_f32 v148, v185, v100, v148
	v_fma_f32 v152, v186, v104, v152
	v_fma_f32 v156, v187, v108, v156
	v_fma_f32 v145, v184, v97, v145
	v_fma_f32 v149, v185, v101, v149
	v_fma_f32 v153, v186, v105, v153
	v_fma_f32 v157, v187, v109, v157
	v_fma_f32 v146, v184, v98, v146
	v_fma_f32 v150, v185, v102, v150
	v_fma_f32 v154, v186, v106, v154
	v_fma_f32 v158, v187, v110, v158
	v_fma_f32 v147, v184, v99, v147
	v_fma_f32 v151, v185, v103, v151
	v_fma_f32 v155, v186, v107, v155
	v_fma_f32 v159, v187, v111, v159
	v_cvt_pk_bf16_f32 v178, v144, v145
	v_cvt_pk_bf16_f32 v179, v146, v147
	v_cvt_pk_bf16_f32 v180, v148, v149
	v_cvt_pk_bf16_f32 v181, v150, v151
	v_cvt_pk_bf16_f32 v182, v152, v153
	v_cvt_pk_bf16_f32 v183, v154, v155
	v_cvt_pk_bf16_f32 v184, v156, v157
	v_cvt_pk_bf16_f32 v185, v158, v159
	global_store_dword v209, v178, s[44:45]
	global_store_dword v209, v179, s[44:45] offset:256
	global_store_dword v209, v180, s[44:45] offset:512
	global_store_dword v209, v181, s[44:45] offset:768
	global_store_dword v209, v182, s[44:45] offset:1024
	global_store_dword v209, v183, s[44:45] offset:1280
	global_store_dword v209, v184, s[44:45] offset:1536
	global_store_dword v209, v185, s[44:45] offset:1792
	s_add_i32 s13, s13, 1
	s_add_i32 s60, s60, -1
	s_cmp_lg_u32 s60, 0
	s_cbranch_scc1 .Lmylru_loop_0
	s_lshl_b32 s50, s10, 10
	s_lshl_b32 s51, s11, 6
	s_add_i32 s50, s50, s51
	s_lshl_b32 s51, s8, 4
	s_add_i32 s50, s50, s51
	s_add_i32 s50, s50, 512
	s_lshl_b32 s50, s50, 9
	s_add_u32 s46, s2, s50
	s_addc_u32 s47, s3, 0
	s_add_u32 s46, s46, 0x1000000
	s_addc_u32 s47, s47, 0
	s_add_u32 s48, s46, 0x20000
	s_addc_u32 s49, s47, 0
	v_lshlrev_b32_e32 v178, 9, v160
	v_lshl_add_u32 v178, v161, 4, v178
	global_load_dwordx4 v[0:3], v178, s[46:47]
	global_load_dwordx4 v[4:7], v178, s[46:47] offset:64
	global_load_dwordx4 v[8:11], v178, s[46:47] offset:128
	global_load_dwordx4 v[12:15], v178, s[46:47] offset:192
	global_load_dwordx4 v[16:19], v178, s[46:47] offset:256
	global_load_dwordx4 v[20:23], v178, s[46:47] offset:320
	global_load_dwordx4 v[24:27], v178, s[46:47] offset:384
	global_load_dwordx4 v[28:31], v178, s[46:47] offset:448
	global_load_dwordx4 v[32:35], v178, s[48:49]
	global_load_dwordx4 v[36:39], v178, s[48:49] offset:64
	global_load_dwordx4 v[40:43], v178, s[48:49] offset:128
	global_load_dwordx4 v[44:47], v178, s[48:49] offset:192
	global_load_dwordx4 v[48:51], v178, s[48:49] offset:256
	global_load_dwordx4 v[52:55], v178, s[48:49] offset:320
	global_load_dwordx4 v[56:59], v178, s[48:49] offset:384
	global_load_dwordx4 v[60:63], v178, s[48:49] offset:448
	s_load_dwordx2 s[46:47], s[0:1], 0xc8
	s_load_dwordx2 s[48:49], s[0:1], 0xd8
	s_load_dwordx2 s[40:41], s[0:1], 0xe0
	s_lshl_b32 s50, s10, 8
	s_lshl_b32 s51, s11, 6
	s_add_i32 s50, s50, s51
	s_lshl_b32 s51, s8, 4
	s_add_i32 s50, s50, s51
	v_add_u32_e32 v179, s50, v160
	v_lshlrev_b32_e32 v179, 2, v179
	s_waitcnt lgkmcnt(0)
	global_load_dword v173, v179, s[46:47]
	global_load_dword v174, v179, s[48:49]
	global_load_dword v175, v179, s[40:41]
	v_cmp_gt_u32_e64 s[34:35], 48, v202
	v_cmp_gt_u32_e64 s[36:37], 32, v202
	v_add_u32_e32 v204, 16, v202
	v_add_u32_e32 v205, 32, v202
	v_mov_b32_e32 v206, v160
	s_cmp_eq_u32 s7, 0
	s_cselect_b64 s[38:39], -1, 0
	v_and_b32_e32 v204, 63, v204
	v_lshlrev_b32_e32 v204, 2, v204
	v_and_b32_e32 v205, 63, v205
	v_lshlrev_b32_e32 v205, 2, v205
	v_and_b32_e32 v206, 63, v206
	v_lshlrev_b32_e32 v206, 2, v206
	v_mov_b32_e32 v176, 0
	s_mov_b32 s53, 0xbfb8aa3b
	s_waitcnt vmcnt(0)
	v_mul_f32_e32 v173, s53, v173
	v_mul_f32_e32 v174, s53, v174
	v_mul_f32_e32 v175, s53, v175
	v_exp_f32_e32 v175, v175
	s_nop 0
	v_add_f32_e32 v180, 1.0, v175
	v_log_f32_e32 v180, v180
	v_mov_b32_e32 v181, 0x3eaaaaab
	v_fma_f32 v181, v175, v181, -0.5
	v_fma_f32 v181, v175, v181, 1.0
	v_mul_f32_e32 v181, v175, v181
	v_mul_f32_e32 v181, 0x3fb8aa3b, v181
	v_cmp_gt_f32_e32 vcc, 0x3cf5c28f, v175
	s_nop 1
	v_cndmask_b32_e32 v175, v180, v181, vcc
	v_mul_f32_e32 v175, 0xc1000000, v175
	s_mov_b32 s13, 0
	s_barrier
	s_cmp_lt_u32 s13, 2
	s_sub_i32 s50, 1, s13
	s_lshl_b32 s50, s50, 7
	s_lshl_b32 s51, s9, 8
	s_add_i32 s51, s51, 0x8000
	s_add_i32 s51, s51, s50
	s_sub_i32 s50, 17, s13
	s_lshl_b32 s50, s50, 7
	s_lshl_b32 s59, s9, 11
	s_add_i32 s59, s59, s50
	s_cmp_lt_u32 s13, 2
	s_cselect_b32 s59, s51, s59
	s_lshl_b32 s52, s59, 11
	s_add_u32 s46, s16, s52
	s_addc_u32 s47, s17, 0
	s_lshl_b32 s52, s6, 13
	s_mov_b32 m0, s52
	s_add_i32 s52, s52, 0x400
	global_load_lds_dwordx4 v211, s[46:47]
	s_mov_b32 m0, s52
	s_add_i32 s52, s52, 0x400
	global_load_lds_dwordx4 v212, s[46:47]
	s_mov_b32 m0, s52
	s_add_i32 s52, s52, 0x400
	global_load_lds_dwordx4 v213, s[46:47]
	s_mov_b32 m0, s52
	s_add_i32 s52, s52, 0x400
	global_load_lds_dwordx4 v214, s[46:47]
	s_mov_b32 m0, s52
	s_add_i32 s52, s52, 0x400
	global_load_lds_dwordx4 v215, s[46:47]
	s_mov_b32 m0, s52
	s_add_i32 s52, s52, 0x400
	global_load_lds_dwordx4 v216, s[46:47]
	s_mov_b32 m0, s52
	s_add_i32 s52, s52, 0x400
	global_load_lds_dwordx4 v217, s[46:47]
	s_mov_b32 m0, s52
	s_nop 0
	global_load_lds_dwordx4 v218, s[46:47]
	s_mov_b32 s58, 1
	s_cmp_lt_u32 s58, 2
	s_sub_i32 s50, 1, s58
	s_lshl_b32 s50, s50, 7
	s_lshl_b32 s51, s9, 8
	s_add_i32 s51, s51, 0x8000
	s_add_i32 s51, s51, s50
	s_sub_i32 s50, 17, s58
	s_lshl_b32 s50, s50, 7
	s_lshl_b32 s59, s9, 11
	s_add_i32 s59, s59, s50
	s_cmp_lt_u32 s58, 2
	s_cselect_b32 s59, s51, s59
	s_lshl_b32 s52, s59, 11
	s_add_u32 s46, s16, s52
	s_addc_u32 s47, s17, 0
	s_lshl_b32 s52, s6, 13
	s_add_i32 s52, s52, 0x10000
	s_mov_b32 m0, s52
	s_add_i32 s52, s52, 0x400
	global_load_lds_dwordx4 v211, s[46:47]
	s_mov_b32 m0, s52
	s_add_i32 s52, s52, 0x400
	global_load_lds_dwordx4 v212, s[46:47]
	s_mov_b32 m0, s52
	s_add_i32 s52, s52, 0x400
	global_load_lds_dwordx4 v213, s[46:47]
	s_mov_b32 m0, s52
	s_add_i32 s52, s52, 0x400
	global_load_lds_dwordx4 v214, s[46:47]
	s_mov_b32 m0, s52
	s_add_i32 s52, s52, 0x400
	global_load_lds_dwordx4 v215, s[46:47]
	s_mov_b32 m0, s52
	s_add_i32 s52, s52, 0x400
	global_load_lds_dwordx4 v216, s[46:47]
	s_mov_b32 m0, s52
	s_add_i32 s52, s52, 0x400
	global_load_lds_dwordx4 v217, s[46:47]
	s_mov_b32 m0, s52
	s_nop 0
	global_load_lds_dwordx4 v218, s[46:47]
	s_waitcnt vmcnt(8)
	s_barrier
	v_mov_b32_e32 v163, v162
	ds_read_b128 v[96:99], v163
	ds_read_b128 v[100:103], v163 offset:8192
	ds_read_b128 v[104:107], v163 offset:16384
	ds_read_b128 v[108:111], v163 offset:24576
	v_xor_b32_e32 v164, 0x40, v163
	ds_read_b128 v[112:115], v164
	ds_read_b128 v[116:119], v164 offset:8192
	ds_read_b128 v[120:123], v164 offset:16384
	ds_read_b128 v[124:127], v164 offset:24576
	s_waitcnt lgkmcnt(7)
	v_mfma_f32_16x16x32_bf16 v[64:67], v[96:99], v[0:3], 0
	v_mfma_f32_16x16x32_bf16 v[68:71], v[96:99], v[32:35], 0
	v_xor_b32_e32 v164, 0x80, v163
	ds_read_b128 v[96:99], v164
	s_waitcnt lgkmcnt(7)
	v_mfma_f32_16x16x32_bf16 v[72:75], v[100:103], v[0:3], 0
	v_mfma_f32_16x16x32_bf16 v[76:79], v[100:103], v[32:35], 0
	ds_read_b128 v[100:103], v164 offset:8192
	s_waitcnt lgkmcnt(7)
	v_mfma_f32_16x16x32_bf16 v[80:83], v[104:107], v[0:3], 0
	v_mfma_f32_16x16x32_bf16 v[84:87], v[104:107], v[32:35], 0
	ds_read_b128 v[104:107], v164 offset:16384
	s_waitcnt lgkmcnt(7)
	v_mfma_f32_16x16x32_bf16 v[88:91], v[108:111], v[0:3], 0
	v_mfma_f32_16x16x32_bf16 v[92:95], v[108:111], v[32:35], 0
	ds_read_b128 v[108:111], v164 offset:24576
	s_waitcnt lgkmcnt(7)
	v_mfma_f32_16x16x32_bf16 v[64:67], v[112:115], v[4:7], v[64:67]
	v_mfma_f32_16x16x32_bf16 v[68:71], v[112:115], v[36:39], v[68:71]
	v_xor_b32_e32 v164, 0xc0, v163
	ds_read_b128 v[112:115], v164
	s_waitcnt lgkmcnt(7)
	v_mfma_f32_16x16x32_bf16 v[72:75], v[116:119], v[4:7], v[72:75]
	v_mfma_f32_16x16x32_bf16 v[76:79], v[116:119], v[36:39], v[76:79]
	ds_read_b128 v[116:119], v164 offset:8192
	s_waitcnt lgkmcnt(7)
	v_mfma_f32_16x16x32_bf16 v[80:83], v[120:123], v[4:7], v[80:83]
	v_mfma_f32_16x16x32_bf16 v[84:87], v[120:123], v[36:39], v[84:87]
	ds_read_b128 v[120:123], v164 offset:16384
	s_waitcnt lgkmcnt(7)
	v_mfma_f32_16x16x32_bf16 v[88:91], v[124:127], v[4:7], v[88:91]
	v_mfma_f32_16x16x32_bf16 v[92:95], v[124:127], v[36:39], v[92:95]
	ds_read_b128 v[124:127], v164 offset:24576
	s_waitcnt lgkmcnt(7)
	v_mfma_f32_16x16x32_bf16 v[64:67], v[96:99], v[8:11], v[64:67]
	v_mfma_f32_16x16x32_bf16 v[68:71], v[96:99], v[40:43], v[68:71]
	v_xor_b32_e32 v164, 0x100, v163
	ds_read_b128 v[96:99], v164
	s_waitcnt lgkmcnt(7)
	v_mfma_f32_16x16x32_bf16 v[72:75], v[100:103], v[8:11], v[72:75]
	v_mfma_f32_16x16x32_bf16 v[76:79], v[100:103], v[40:43], v[76:79]
	ds_read_b128 v[100:103], v164 offset:8192
	s_waitcnt lgkmcnt(7)
	v_mfma_f32_16x16x32_bf16 v[80:83], v[104:107], v[8:11], v[80:83]
	v_mfma_f32_16x16x32_bf16 v[84:87], v[104:107], v[40:43], v[84:87]
	ds_read_b128 v[104:107], v164 offset:16384
	s_waitcnt lgkmcnt(7)
	v_mfma_f32_16x16x32_bf16 v[88:91], v[108:111], v[8:11], v[88:91]
	v_mfma_f32_16x16x32_bf16 v[92:95], v[108:111], v[40:43], v[92:95]
	ds_read_b128 v[108:111], v164 offset:24576
	s_waitcnt lgkmcnt(7)
	v_mfma_f32_16x16x32_bf16 v[64:67], v[112:115], v[12:15], v[64:67]
	v_mfma_f32_16x16x32_bf16 v[68:71], v[112:115], v[44:47], v[68:71]
	v_xor_b32_e32 v164, 0x140, v163
	ds_read_b128 v[112:115], v164
	s_waitcnt lgkmcnt(7)
	v_mfma_f32_16x16x32_bf16 v[72:75], v[116:119], v[12:15], v[72:75]
	v_mfma_f32_16x16x32_bf16 v[76:79], v[116:119], v[44:47], v[76:79]
	ds_read_b128 v[116:119], v164 offset:8192
	s_waitcnt lgkmcnt(7)
	v_mfma_f32_16x16x32_bf16 v[80:83], v[120:123], v[12:15], v[80:83]
	v_mfma_f32_16x16x32_bf16 v[84:87], v[120:123], v[44:47], v[84:87]
	ds_read_b128 v[120:123], v164 offset:16384
	s_waitcnt lgkmcnt(7)
	v_mfma_f32_16x16x32_bf16 v[88:91], v[124:127], v[12:15], v[88:91]
	v_mfma_f32_16x16x32_bf16 v[92:95], v[124:127], v[44:47], v[92:95]
	ds_read_b128 v[124:127], v164 offset:24576
	s_waitcnt lgkmcnt(7)
	v_mfma_f32_16x16x32_bf16 v[64:67], v[96:99], v[16:19], v[64:67]
	v_mfma_f32_16x16x32_bf16 v[68:71], v[96:99], v[48:51], v[68:71]
	v_xor_b32_e32 v164, 0x180, v163
	ds_read_b128 v[96:99], v164
	s_waitcnt lgkmcnt(7)
	v_mfma_f32_16x16x32_bf16 v[72:75], v[100:103], v[16:19], v[72:75]
	v_mfma_f32_16x16x32_bf16 v[76:79], v[100:103], v[48:51], v[76:79]
	ds_read_b128 v[100:103], v164 offset:8192
	s_waitcnt lgkmcnt(7)
	v_mfma_f32_16x16x32_bf16 v[80:83], v[104:107], v[16:19], v[80:83]
	v_mfma_f32_16x16x32_bf16 v[84:87], v[104:107], v[48:51], v[84:87]
	ds_read_b128 v[104:107], v164 offset:16384
	s_waitcnt lgkmcnt(7)
	v_mfma_f32_16x16x32_bf16 v[88:91], v[108:111], v[16:19], v[88:91]
	v_mfma_f32_16x16x32_bf16 v[92:95], v[108:111], v[48:51], v[92:95]
	ds_read_b128 v[108:111], v164 offset:24576
	s_waitcnt lgkmcnt(7)
	v_mfma_f32_16x16x32_bf16 v[64:67], v[112:115], v[20:23], v[64:67]
	v_mfma_f32_16x16x32_bf16 v[68:71], v[112:115], v[52:55], v[68:71]
	v_xor_b32_e32 v164, 0x1c0, v163
	ds_read_b128 v[112:115], v164
	s_waitcnt lgkmcnt(7)
	v_mfma_f32_16x16x32_bf16 v[72:75], v[116:119], v[20:23], v[72:75]
	v_mfma_f32_16x16x32_bf16 v[76:79], v[116:119], v[52:55], v[76:79]
	ds_read_b128 v[116:119], v164 offset:8192
	s_waitcnt lgkmcnt(7)
	v_mfma_f32_16x16x32_bf16 v[80:83], v[120:123], v[20:23], v[80:83]
	v_mfma_f32_16x16x32_bf16 v[84:87], v[120:123], v[52:55], v[84:87]
	ds_read_b128 v[120:123], v164 offset:16384
	s_waitcnt lgkmcnt(7)
	v_mfma_f32_16x16x32_bf16 v[88:91], v[124:127], v[20:23], v[88:91]
	v_mfma_f32_16x16x32_bf16 v[92:95], v[124:127], v[52:55], v[92:95]
	ds_read_b128 v[124:127], v164 offset:24576
	s_waitcnt lgkmcnt(7)
	v_mfma_f32_16x16x32_bf16 v[64:67], v[96:99], v[24:27], v[64:67]
	v_mfma_f32_16x16x32_bf16 v[68:71], v[96:99], v[56:59], v[68:71]
	s_waitcnt lgkmcnt(6)
	v_mfma_f32_16x16x32_bf16 v[72:75], v[100:103], v[24:27], v[72:75]
	v_mfma_f32_16x16x32_bf16 v[76:79], v[100:103], v[56:59], v[76:79]
	s_waitcnt lgkmcnt(5)
	v_mfma_f32_16x16x32_bf16 v[80:83], v[104:107], v[24:27], v[80:83]
	v_mfma_f32_16x16x32_bf16 v[84:87], v[104:107], v[56:59], v[84:87]
	s_waitcnt lgkmcnt(4)
	v_mfma_f32_16x16x32_bf16 v[88:91], v[108:111], v[24:27], v[88:91]
	v_mfma_f32_16x16x32_bf16 v[92:95], v[108:111], v[56:59], v[92:95]
	s_waitcnt lgkmcnt(3)
	v_mfma_f32_16x16x32_bf16 v[64:67], v[112:115], v[28:31], v[64:67]
	v_mfma_f32_16x16x32_bf16 v[68:71], v[112:115], v[60:63], v[68:71]
	s_waitcnt lgkmcnt(2)
	v_mfma_f32_16x16x32_bf16 v[72:75], v[116:119], v[28:31], v[72:75]
	v_mfma_f32_16x16x32_bf16 v[76:79], v[116:119], v[60:63], v[76:79]
	s_waitcnt lgkmcnt(1)
	v_mfma_f32_16x16x32_bf16 v[80:83], v[120:123], v[28:31], v[80:83]
	v_mfma_f32_16x16x32_bf16 v[84:87], v[120:123], v[60:63], v[84:87]
	s_waitcnt lgkmcnt(0)
	v_mfma_f32_16x16x32_bf16 v[88:91], v[124:127], v[28:31], v[88:91]
	v_mfma_f32_16x16x32_bf16 v[92:95], v[124:127], v[60:63], v[92:95]
	v_mov_b32_e32 v169, v165
	v_mov_b32_e32 v170, v166
	v_mov_b32_e32 v171, v167
	v_mov_b32_e32 v172, v168
	ds_read_u16 v144, v169
	ds_read_u16 v145, v170
	ds_read_u16 v146, v171
	ds_read_u16 v147, v172
	ds_read_u16 v148, v169 offset:8192
	ds_read_u16 v149, v170 offset:8192
	ds_read_u16 v150, v171 offset:8192
	ds_read_u16 v151, v172 offset:8192
	ds_read_u16 v152, v169 offset:16384
	ds_read_u16 v153, v170 offset:16384
	ds_read_u16 v154, v171 offset:16384
	ds_read_u16 v155, v172 offset:16384
	ds_read_u16 v156, v169 offset:24576
	ds_read_u16 v157, v170 offset:24576
	ds_read_u16 v158, v171 offset:24576
	ds_read_u16 v159, v172 offset:24576
	s_nop 7
	v_fma_f32 v178, v64, s53, v173
	v_fma_f32 v179, v65, s53, v173
	v_fma_f32 v180, v66, s53, v173
	v_fma_f32 v181, v67, s53, v173
	v_fma_f32 v182, v72, s53, v173
	v_fma_f32 v183, v73, s53, v173
	v_fma_f32 v184, v74, s53, v173
	v_fma_f32 v185, v75, s53, v173
	v_fma_f32 v186, v68, s53, v174
	v_fma_f32 v187, v69, s53, v174
	v_fma_f32 v188, v70, s53, v174
	v_fma_f32 v189, v71, s53, v174
	v_fma_f32 v190, v76, s53, v174
	v_fma_f32 v191, v77, s53, v174
	v_fma_f32 v192, v78, s53, v174
	v_fma_f32 v193, v79, s53, v174
	v_exp_f32_e32 v178, v178
	v_exp_f32_e32 v179, v179
	v_exp_f32_e32 v180, v180
	v_exp_f32_e32 v181, v181
	v_exp_f32_e32 v182, v182
	v_exp_f32_e32 v183, v183
	v_exp_f32_e32 v184, v184
	v_exp_f32_e32 v185, v185
	v_exp_f32_e32 v186, v186
	v_exp_f32_e32 v187, v187
	v_exp_f32_e32 v188, v188
	v_exp_f32_e32 v189, v189
	v_exp_f32_e32 v190, v190
	v_exp_f32_e32 v191, v191
	v_exp_f32_e32 v192, v192
	v_exp_f32_e32 v193, v193
	v_add_f32_e32 v178, 1.0, v178
	v_add_f32_e32 v179, 1.0, v179
	v_add_f32_e32 v180, 1.0, v180
	v_add_f32_e32 v181, 1.0, v181
	v_add_f32_e32 v182, 1.0, v182
	v_add_f32_e32 v183, 1.0, v183
	v_add_f32_e32 v184, 1.0, v184
	v_add_f32_e32 v185, 1.0, v185
	v_add_f32_e32 v186, 1.0, v186
	v_add_f32_e32 v187, 1.0, v187
	v_add_f32_e32 v188, 1.0, v188
	v_add_f32_e32 v189, 1.0, v189
	v_add_f32_e32 v190, 1.0, v190
	v_add_f32_e32 v191, 1.0, v191
	v_add_f32_e32 v192, 1.0, v192
	v_add_f32_e32 v193, 1.0, v193
	v_rcp_f32_e32 v178, v178
	v_rcp_f32_e32 v179, v179
	v_rcp_f32_e32 v180, v180
	v_rcp_f32_e32 v181, v181
	v_rcp_f32_e32 v182, v182
	v_rcp_f32_e32 v183, v183
	v_rcp_f32_e32 v184, v184
	v_rcp_f32_e32 v185, v185
	v_rcp_f32_e32 v186, v186
	v_rcp_f32_e32 v187, v187
	v_rcp_f32_e32 v188, v188
	v_rcp_f32_e32 v189, v189
	v_rcp_f32_e32 v190, v190
	v_rcp_f32_e32 v191, v191
	v_rcp_f32_e32 v192, v192
	v_rcp_f32_e32 v193, v193
	v_mul_f32_e32 v178, v175, v178
	v_mul_f32_e32 v179, v175, v179
	v_mul_f32_e32 v180, v175, v180
	v_mul_f32_e32 v181, v175, v181
	v_mul_f32_e32 v182, v175, v182
	v_mul_f32_e32 v183, v175, v183
	v_mul_f32_e32 v184, v175, v184
	v_mul_f32_e32 v185, v175, v185
	v_exp_f32_e32 v96, v178
	v_exp_f32_e32 v97, v179
	v_exp_f32_e32 v98, v180
	v_exp_f32_e32 v99, v181
	v_exp_f32_e32 v100, v182
	v_exp_f32_e32 v101, v183
	v_exp_f32_e32 v102, v184
	v_exp_f32_e32 v103, v185
	s_nop 0
	v_fma_f32 v194, -v96, v96, 1.0
	v_fma_f32 v195, -v97, v97, 1.0
	v_fma_f32 v196, -v98, v98, 1.0
	v_fma_f32 v197, -v99, v99, 1.0
	v_fma_f32 v198, -v100, v100, 1.0
	v_fma_f32 v199, -v101, v101, 1.0
	v_fma_f32 v200, -v102, v102, 1.0
	v_fma_f32 v201, -v103, v103, 1.0
	v_max_f32_e32 v194, 0, v194
	v_max_f32_e32 v195, 0, v195
	v_max_f32_e32 v196, 0, v196
	v_max_f32_e32 v197, 0, v197
	v_max_f32_e32 v198, 0, v198
	v_max_f32_e32 v199, 0, v199
	v_max_f32_e32 v200, 0, v200
	v_max_f32_e32 v201, 0, v201
	v_sqrt_f32_e32 v194, v194
	v_sqrt_f32_e32 v195, v195
	v_sqrt_f32_e32 v196, v196
	v_sqrt_f32_e32 v197, v197
	v_sqrt_f32_e32 v198, v198
	v_sqrt_f32_e32 v199, v199
	v_sqrt_f32_e32 v200, v200
	v_sqrt_f32_e32 v201, v201
	s_waitcnt lgkmcnt(8)
	v_lshlrev_b32_e32 v144, 16, v144
	v_lshlrev_b32_e32 v145, 16, v145
	v_lshlrev_b32_e32 v146, 16, v146
	v_lshlrev_b32_e32 v147, 16, v147
	v_lshlrev_b32_e32 v148, 16, v148
	v_lshlrev_b32_e32 v149, 16, v149
	v_lshlrev_b32_e32 v150, 16, v150
	v_lshlrev_b32_e32 v151, 16, v151
	v_mul_f32_e32 v194, v194, v186
	v_mul_f32_e32 v195, v195, v187
	v_mul_f32_e32 v196, v196, v188
	v_mul_f32_e32 v197, v197, v189
	v_mul_f32_e32 v198, v198, v190
	v_mul_f32_e32 v199, v199, v191
	v_mul_f32_e32 v200, v200, v192
	v_mul_f32_e32 v201, v201, v193
	v_mul_f32_e32 v144, v194, v144
	v_mul_f32_e32 v145, v195, v145
	v_mul_f32_e32 v146, v196, v146
	v_mul_f32_e32 v147, v197, v147
	v_mul_f32_e32 v148, v198, v148
	v_mul_f32_e32 v149, v199, v149
	v_mul_f32_e32 v150, v200, v150
	v_mul_f32_e32 v151, v201, v151
	v_fma_f32 v178, v80, s53, v173
	v_fma_f32 v179, v81, s53, v173
	v_fma_f32 v180, v82, s53, v173
	v_fma_f32 v181, v83, s53, v173
	v_fma_f32 v182, v88, s53, v173
	v_fma_f32 v183, v89, s53, v173
	v_fma_f32 v184, v90, s53, v173
	v_fma_f32 v185, v91, s53, v173
	v_fma_f32 v186, v84, s53, v174
	v_fma_f32 v187, v85, s53, v174
	v_fma_f32 v188, v86, s53, v174
	v_fma_f32 v189, v87, s53, v174
	v_fma_f32 v190, v92, s53, v174
	v_fma_f32 v191, v93, s53, v174
	v_fma_f32 v192, v94, s53, v174
	v_fma_f32 v193, v95, s53, v174
	v_exp_f32_e32 v178, v178
	v_exp_f32_e32 v179, v179
	v_exp_f32_e32 v180, v180
	v_exp_f32_e32 v181, v181
	v_exp_f32_e32 v182, v182
	v_exp_f32_e32 v183, v183
	v_exp_f32_e32 v184, v184
	v_exp_f32_e32 v185, v185
	v_exp_f32_e32 v186, v186
	v_exp_f32_e32 v187, v187
	v_exp_f32_e32 v188, v188
	v_exp_f32_e32 v189, v189
	v_exp_f32_e32 v190, v190
	v_exp_f32_e32 v191, v191
	v_exp_f32_e32 v192, v192
	v_exp_f32_e32 v193, v193
	v_add_f32_e32 v178, 1.0, v178
	v_add_f32_e32 v179, 1.0, v179
	v_add_f32_e32 v180, 1.0, v180
	v_add_f32_e32 v181, 1.0, v181
	v_add_f32_e32 v182, 1.0, v182
	v_add_f32_e32 v183, 1.0, v183
	v_add_f32_e32 v184, 1.0, v184
	v_add_f32_e32 v185, 1.0, v185
	v_add_f32_e32 v186, 1.0, v186
	v_add_f32_e32 v187, 1.0, v187
	v_add_f32_e32 v188, 1.0, v188
	v_add_f32_e32 v189, 1.0, v189
	v_add_f32_e32 v190, 1.0, v190
	v_add_f32_e32 v191, 1.0, v191
	v_add_f32_e32 v192, 1.0, v192
	v_add_f32_e32 v193, 1.0, v193
	v_rcp_f32_e32 v178, v178
	v_rcp_f32_e32 v179, v179
	v_rcp_f32_e32 v180, v180
	v_rcp_f32_e32 v181, v181
	v_rcp_f32_e32 v182, v182
	v_rcp_f32_e32 v183, v183
	v_rcp_f32_e32 v184, v184
	v_rcp_f32_e32 v185, v185
	v_rcp_f32_e32 v186, v186
	v_rcp_f32_e32 v187, v187
	v_rcp_f32_e32 v188, v188
	v_rcp_f32_e32 v189, v189
	v_rcp_f32_e32 v190, v190
	v_rcp_f32_e32 v191, v191
	v_rcp_f32_e32 v192, v192
	v_rcp_f32_e32 v193, v193
	v_mul_f32_e32 v178, v175, v178
	v_mul_f32_e32 v179, v175, v179
	v_mul_f32_e32 v180, v175, v180
	v_mul_f32_e32 v181, v175, v181
	v_mul_f32_e32 v182, v175, v182
	v_mul_f32_e32 v183, v175, v183
	v_mul_f32_e32 v184, v175, v184
	v_mul_f32_e32 v185, v175, v185
	v_exp_f32_e32 v104, v178
	v_exp_f32_e32 v105, v179
	v_exp_f32_e32 v106, v180
	v_exp_f32_e32 v107, v181
	v_exp_f32_e32 v108, v182
	v_exp_f32_e32 v109, v183
	v_exp_f32_e32 v110, v184
	v_exp_f32_e32 v111, v185
	s_nop 0
	v_fma_f32 v194, -v104, v104, 1.0
	v_fma_f32 v195, -v105, v105, 1.0
	v_fma_f32 v196, -v106, v106, 1.0
	v_fma_f32 v197, -v107, v107, 1.0
	v_fma_f32 v198, -v108, v108, 1.0
	v_fma_f32 v199, -v109, v109, 1.0
	v_fma_f32 v200, -v110, v110, 1.0
	v_fma_f32 v201, -v111, v111, 1.0
	v_max_f32_e32 v194, 0, v194
	v_max_f32_e32 v195, 0, v195
	v_max_f32_e32 v196, 0, v196
	v_max_f32_e32 v197, 0, v197
	v_max_f32_e32 v198, 0, v198
	v_max_f32_e32 v199, 0, v199
	v_max_f32_e32 v200, 0, v200
	v_max_f32_e32 v201, 0, v201
	v_sqrt_f32_e32 v194, v194
	v_sqrt_f32_e32 v195, v195
	v_sqrt_f32_e32 v196, v196
	v_sqrt_f32_e32 v197, v197
	v_sqrt_f32_e32 v198, v198
	v_sqrt_f32_e32 v199, v199
	v_sqrt_f32_e32 v200, v200
	v_sqrt_f32_e32 v201, v201
	s_waitcnt lgkmcnt(0)
	v_lshlrev_b32_e32 v152, 16, v152
	v_lshlrev_b32_e32 v153, 16, v153
	v_lshlrev_b32_e32 v154, 16, v154
	v_lshlrev_b32_e32 v155, 16, v155
	v_lshlrev_b32_e32 v156, 16, v156
	v_lshlrev_b32_e32 v157, 16, v157
	v_lshlrev_b32_e32 v158, 16, v158
	v_lshlrev_b32_e32 v159, 16, v159
	v_mul_f32_e32 v194, v194, v186
	v_mul_f32_e32 v195, v195, v187
	v_mul_f32_e32 v196, v196, v188
	v_mul_f32_e32 v197, v197, v189
	v_mul_f32_e32 v198, v198, v190
	v_mul_f32_e32 v199, v199, v191
	v_mul_f32_e32 v200, v200, v192
	v_mul_f32_e32 v201, v201, v193
	v_mul_f32_e32 v152, v194, v152
	v_mul_f32_e32 v153, v195, v153
	v_mul_f32_e32 v154, v196, v154
	v_mul_f32_e32 v155, v197, v155
	v_mul_f32_e32 v156, v198, v156
	v_mul_f32_e32 v157, v199, v157
	v_mul_f32_e32 v158, v200, v158
	v_mul_f32_e32 v159, v201, v159
	v_fma_f32 v146, v98, v147, v146
	v_fma_f32 v150, v102, v151, v150
	v_fma_f32 v154, v106, v155, v154
	v_fma_f32 v158, v110, v159, v158
	v_mul_f32_e32 v98, v98, v99
	v_mul_f32_e32 v102, v102, v103
	v_mul_f32_e32 v106, v106, v107
	v_mul_f32_e32 v110, v110, v111
	v_fma_f32 v145, v97, v146, v145
	v_fma_f32 v149, v101, v150, v149
	v_fma_f32 v153, v105, v154, v153
	v_fma_f32 v157, v109, v158, v157
	v_mul_f32_e32 v97, v97, v98
	v_mul_f32_e32 v101, v101, v102
	v_mul_f32_e32 v105, v105, v106
	v_mul_f32_e32 v109, v109, v110
	v_fma_f32 v144, v96, v145, v144
	v_fma_f32 v148, v100, v149, v148
	v_fma_f32 v152, v104, v153, v152
	v_fma_f32 v156, v108, v157, v156
	v_mul_f32_e32 v96, v96, v97
	v_mul_f32_e32 v100, v100, v101
	v_mul_f32_e32 v104, v104, v105
	v_mul_f32_e32 v108, v108, v109
	ds_bpermute_b32 v178, v204, v96
	ds_bpermute_b32 v182, v204, v144
	ds_bpermute_b32 v179, v204, v100
	ds_bpermute_b32 v183, v204, v148
	ds_bpermute_b32 v180, v204, v104
	ds_bpermute_b32 v184, v204, v152
	ds_bpermute_b32 v181, v204, v108
	ds_bpermute_b32 v185, v204, v156
	s_waitcnt lgkmcnt(0)
	v_fma_f32 v186, v182, v96, v144
	v_cndmask_b32_e64 v178, 1.0, v178, s[34:35]
	v_fma_f32 v187, v183, v100, v148
	v_cndmask_b32_e64 v179, 1.0, v179, s[34:35]
	v_fma_f32 v188, v184, v104, v152
	v_cndmask_b32_e64 v180, 1.0, v180, s[34:35]
	v_fma_f32 v189, v185, v108, v156
	v_cndmask_b32_e64 v181, 1.0, v181, s[34:35]
	v_cndmask_b32_e64 v223, v144, v186, s[34:35]
	v_mul_f32_e32 v219, v96, v178
	v_cndmask_b32_e64 v224, v148, v187, s[34:35]
	v_mul_f32_e32 v220, v100, v179
	v_cndmask_b32_e64 v225, v152, v188, s[34:35]
	v_mul_f32_e32 v221, v104, v180
	v_cndmask_b32_e64 v226, v156, v189, s[34:35]
	v_mul_f32_e32 v222, v108, v181
	ds_bpermute_b32 v178, v205, v219
	ds_bpermute_b32 v182, v205, v223
	ds_bpermute_b32 v179, v205, v220
	ds_bpermute_b32 v183, v205, v224
	ds_bpermute_b32 v180, v205, v221
	ds_bpermute_b32 v184, v205, v225
	ds_bpermute_b32 v181, v205, v222
	ds_bpermute_b32 v185, v205, v226
	s_waitcnt lgkmcnt(0)
	v_fma_f32 v186, v182, v219, v223
	v_cndmask_b32_e64 v178, 1.0, v178, s[36:37]
	v_fma_f32 v187, v183, v220, v224
	v_cndmask_b32_e64 v179, 1.0, v179, s[36:37]
	v_fma_f32 v188, v184, v221, v225
	v_cndmask_b32_e64 v180, 1.0, v180, s[36:37]
	v_fma_f32 v189, v185, v222, v226
	v_cndmask_b32_e64 v181, 1.0, v181, s[36:37]
	v_cndmask_b32_e64 v223, v223, v186, s[36:37]
	v_mul_f32_e32 v219, v219, v178
	v_cndmask_b32_e64 v224, v224, v187, s[36:37]
	v_mul_f32_e32 v220, v220, v179
	v_cndmask_b32_e64 v225, v225, v188, s[36:37]
	v_mul_f32_e32 v221, v221, v180
	v_cndmask_b32_e64 v226, v226, v189, s[36:37]
	v_mul_f32_e32 v222, v222, v181
	ds_bpermute_b32 v227, v204, v219
	ds_bpermute_b32 v231, v204, v223
	ds_bpermute_b32 v235, v206, v219
	ds_bpermute_b32 v239, v206, v223
	ds_bpermute_b32 v228, v204, v220
	ds_bpermute_b32 v232, v204, v224
	ds_bpermute_b32 v236, v206, v220
	ds_bpermute_b32 v244, v206, v224
	ds_bpermute_b32 v229, v204, v221
	ds_bpermute_b32 v233, v204, v225
	ds_bpermute_b32 v237, v206, v221
	ds_bpermute_b32 v245, v206, v225
	ds_bpermute_b32 v230, v204, v222
	ds_bpermute_b32 v234, v204, v226
	ds_bpermute_b32 v238, v206, v222
	ds_bpermute_b32 v246, v206, v226
	s_waitcnt lgkmcnt(0)
	v_cndmask_b32_e64 v227, 1.0, v227, s[34:35]
	v_cndmask_b32_e64 v231, 0, v231, s[34:35]
	v_cndmask_b32_e64 v228, 1.0, v228, s[34:35]
	v_cndmask_b32_e64 v232, 0, v232, s[34:35]
	v_cndmask_b32_e64 v229, 1.0, v229, s[34:35]
	v_cndmask_b32_e64 v233, 0, v233, s[34:35]
	v_cndmask_b32_e64 v230, 1.0, v230, s[34:35]
	v_cndmask_b32_e64 v234, 0, v234, s[34:35]
	v_mov_b32_e32 v190, v238
	v_mov_b32_e32 v194, v246
	v_mov_b32_e32 v198, v190
	v_mov_b32_e32 v201, v194
	v_fma_f32 v194, v194, v237, v245
	v_mul_f32_e32 v190, v190, v237
	v_mov_b32_e32 v199, v190
	v_mov_b32_e32 v177, v194
	v_fma_f32 v194, v194, v236, v244
	v_mul_f32_e32 v190, v190, v236
	v_mov_b32_e32 v200, v190
	v_mov_b32_e32 v203, v194
	v_fma_f32 v194, v194, v235, v239
	v_mul_f32_e32 v190, v190, v235
	v_mov_b32_e32 v191, v194
	ds_write_b64 v207, v[190:191]
	s_waitcnt vmcnt(0)
	s_waitcnt lgkmcnt(0)
	s_barrier
	s_cmp_gt_u32 s13, 15
	s_cbranch_scc1 .Lmylru_nodma_5
	s_add_i32 s58, s13, 2
	s_cmp_lt_u32 s58, 2
	s_sub_i32 s50, 1, s58
	s_lshl_b32 s50, s50, 7
	s_lshl_b32 s51, s9, 8
	s_add_i32 s51, s51, 0x8000
	s_add_i32 s51, s51, s50
	s_sub_i32 s50, 17, s58
	s_lshl_b32 s50, s50, 7
	s_lshl_b32 s59, s9, 11
	s_add_i32 s59, s59, s50
	s_cmp_lt_u32 s58, 2
	s_cselect_b32 s59, s51, s59
	s_lshl_b32 s52, s59, 11
	s_add_u32 s46, s16, s52
	s_addc_u32 s47, s17, 0
	s_lshl_b32 s52, s6, 13
	s_mov_b32 m0, s52
	s_add_i32 s52, s52, 0x400
	global_load_lds_dwordx4 v211, s[46:47]
	s_mov_b32 m0, s52
	s_add_i32 s52, s52, 0x400
	global_load_lds_dwordx4 v212, s[46:47]
	s_mov_b32 m0, s52
	s_add_i32 s52, s52, 0x400
	global_load_lds_dwordx4 v213, s[46:47]
	s_mov_b32 m0, s52
	s_add_i32 s52, s52, 0x400
	global_load_lds_dwordx4 v214, s[46:47]
	s_mov_b32 m0, s52
	s_add_i32 s52, s52, 0x400
	global_load_lds_dwordx4 v215, s[46:47]
	s_mov_b32 m0, s52
	s_add_i32 s52, s52, 0x400
	global_load_lds_dwordx4 v216, s[46:47]
	s_mov_b32 m0, s52
	s_add_i32 s52, s52, 0x400
	global_load_lds_dwordx4 v217, s[46:47]
	s_mov_b32 m0, s52
	s_nop 0
	global_load_lds_dwordx4 v218, s[46:47]
.Lmylru_nodma_5:
	ds_read_b64 v[178:179], v208 offset:512
	ds_read_b64 v[180:181], v208
	s_waitcnt lgkmcnt(0)
	v_fma_f32 v182, v176, v178, v179
	v_cndmask_b32_e64 v183, v176, v182, s[38:39]
	v_fma_f32 v176, v182, v180, v181
	s_add_i32 s13, s13, 1
	v_or_b32_e32 v163, 0x10000, v162
	ds_read_b128 v[96:99], v163
	ds_read_b128 v[100:103], v163 offset:8192
	ds_read_b128 v[104:107], v163 offset:16384
	ds_read_b128 v[108:111], v163 offset:24576
	v_xor_b32_e32 v164, 0x40, v163
	ds_read_b128 v[112:115], v164
	ds_read_b128 v[116:119], v164 offset:8192
	ds_read_b128 v[120:123], v164 offset:16384
	ds_read_b128 v[124:127], v164 offset:24576
	s_waitcnt lgkmcnt(7)
	v_mfma_f32_16x16x32_bf16 v[64:67], v[96:99], v[0:3], 0
	v_mfma_f32_16x16x32_bf16 v[68:71], v[96:99], v[32:35], 0
	v_xor_b32_e32 v164, 0x80, v163
	ds_read_b128 v[96:99], v164
	s_waitcnt lgkmcnt(7)
	v_mfma_f32_16x16x32_bf16 v[72:75], v[100:103], v[0:3], 0
	v_mfma_f32_16x16x32_bf16 v[76:79], v[100:103], v[32:35], 0
	ds_read_b128 v[100:103], v164 offset:8192
	s_waitcnt lgkmcnt(7)
	v_mfma_f32_16x16x32_bf16 v[80:83], v[104:107], v[0:3], 0
	v_mfma_f32_16x16x32_bf16 v[84:87], v[104:107], v[32:35], 0
	ds_read_b128 v[104:107], v164 offset:16384
	s_waitcnt lgkmcnt(7)
	v_mfma_f32_16x16x32_bf16 v[88:91], v[108:111], v[0:3], 0
	v_mfma_f32_16x16x32_bf16 v[92:95], v[108:111], v[32:35], 0
	ds_read_b128 v[108:111], v164 offset:24576
	s_waitcnt lgkmcnt(7)
	v_mfma_f32_16x16x32_bf16 v[64:67], v[112:115], v[4:7], v[64:67]
	v_mfma_f32_16x16x32_bf16 v[68:71], v[112:115], v[36:39], v[68:71]
	v_xor_b32_e32 v164, 0xc0, v163
	ds_read_b128 v[112:115], v164
	s_waitcnt lgkmcnt(7)
	v_mfma_f32_16x16x32_bf16 v[72:75], v[116:119], v[4:7], v[72:75]
	v_mfma_f32_16x16x32_bf16 v[76:79], v[116:119], v[36:39], v[76:79]
	ds_read_b128 v[116:119], v164 offset:8192
	s_waitcnt lgkmcnt(7)
	v_mfma_f32_16x16x32_bf16 v[80:83], v[120:123], v[4:7], v[80:83]
	v_mfma_f32_16x16x32_bf16 v[84:87], v[120:123], v[36:39], v[84:87]
	ds_read_b128 v[120:123], v164 offset:16384
	s_waitcnt lgkmcnt(7)
	v_mfma_f32_16x16x32_bf16 v[88:91], v[124:127], v[4:7], v[88:91]
	v_mfma_f32_16x16x32_bf16 v[92:95], v[124:127], v[36:39], v[92:95]
	ds_read_b128 v[124:127], v164 offset:24576
	s_waitcnt lgkmcnt(7)
	v_mfma_f32_16x16x32_bf16 v[64:67], v[96:99], v[8:11], v[64:67]
	v_mfma_f32_16x16x32_bf16 v[68:71], v[96:99], v[40:43], v[68:71]
	v_xor_b32_e32 v164, 0x100, v163
	ds_read_b128 v[96:99], v164
	s_waitcnt lgkmcnt(7)
	v_mfma_f32_16x16x32_bf16 v[72:75], v[100:103], v[8:11], v[72:75]
	v_mfma_f32_16x16x32_bf16 v[76:79], v[100:103], v[40:43], v[76:79]
	ds_read_b128 v[100:103], v164 offset:8192
	s_waitcnt lgkmcnt(7)
	v_mfma_f32_16x16x32_bf16 v[80:83], v[104:107], v[8:11], v[80:83]
	v_mfma_f32_16x16x32_bf16 v[84:87], v[104:107], v[40:43], v[84:87]
	ds_read_b128 v[104:107], v164 offset:16384
	s_waitcnt lgkmcnt(7)
	v_mfma_f32_16x16x32_bf16 v[88:91], v[108:111], v[8:11], v[88:91]
	v_mfma_f32_16x16x32_bf16 v[92:95], v[108:111], v[40:43], v[92:95]
	ds_read_b128 v[108:111], v164 offset:24576
	s_waitcnt lgkmcnt(7)
	v_mfma_f32_16x16x32_bf16 v[64:67], v[112:115], v[12:15], v[64:67]
	v_mfma_f32_16x16x32_bf16 v[68:71], v[112:115], v[44:47], v[68:71]
	v_xor_b32_e32 v164, 0x140, v163
	ds_read_b128 v[112:115], v164
	s_waitcnt lgkmcnt(7)
	v_mfma_f32_16x16x32_bf16 v[72:75], v[116:119], v[12:15], v[72:75]
	v_mfma_f32_16x16x32_bf16 v[76:79], v[116:119], v[44:47], v[76:79]
	ds_read_b128 v[116:119], v164 offset:8192
	s_waitcnt lgkmcnt(7)
	v_mfma_f32_16x16x32_bf16 v[80:83], v[120:123], v[12:15], v[80:83]
	v_mfma_f32_16x16x32_bf16 v[84:87], v[120:123], v[44:47], v[84:87]
	ds_read_b128 v[120:123], v164 offset:16384
	s_waitcnt lgkmcnt(7)
	v_mfma_f32_16x16x32_bf16 v[88:91], v[124:127], v[12:15], v[88:91]
	v_mfma_f32_16x16x32_bf16 v[92:95], v[124:127], v[44:47], v[92:95]
	ds_read_b128 v[124:127], v164 offset:24576
	s_waitcnt lgkmcnt(7)
	v_mfma_f32_16x16x32_bf16 v[64:67], v[96:99], v[16:19], v[64:67]
	v_mfma_f32_16x16x32_bf16 v[68:71], v[96:99], v[48:51], v[68:71]
	v_xor_b32_e32 v164, 0x180, v163
	ds_read_b128 v[96:99], v164
	s_waitcnt lgkmcnt(7)
	v_mfma_f32_16x16x32_bf16 v[72:75], v[100:103], v[16:19], v[72:75]
	v_mfma_f32_16x16x32_bf16 v[76:79], v[100:103], v[48:51], v[76:79]
	ds_read_b128 v[100:103], v164 offset:8192
	s_waitcnt lgkmcnt(7)
	v_mfma_f32_16x16x32_bf16 v[80:83], v[104:107], v[16:19], v[80:83]
	v_mfma_f32_16x16x32_bf16 v[84:87], v[104:107], v[48:51], v[84:87]
	ds_read_b128 v[104:107], v164 offset:16384
	s_waitcnt lgkmcnt(7)
	v_mfma_f32_16x16x32_bf16 v[88:91], v[108:111], v[16:19], v[88:91]
	v_mfma_f32_16x16x32_bf16 v[92:95], v[108:111], v[48:51], v[92:95]
	ds_read_b128 v[108:111], v164 offset:24576
	s_waitcnt lgkmcnt(7)
	v_mfma_f32_16x16x32_bf16 v[64:67], v[112:115], v[20:23], v[64:67]
	v_mfma_f32_16x16x32_bf16 v[68:71], v[112:115], v[52:55], v[68:71]
	v_xor_b32_e32 v164, 0x1c0, v163
	ds_read_b128 v[112:115], v164
	s_waitcnt lgkmcnt(7)
	v_mfma_f32_16x16x32_bf16 v[72:75], v[116:119], v[20:23], v[72:75]
	v_mfma_f32_16x16x32_bf16 v[76:79], v[116:119], v[52:55], v[76:79]
	ds_read_b128 v[116:119], v164 offset:8192
	s_waitcnt lgkmcnt(7)
	v_mfma_f32_16x16x32_bf16 v[80:83], v[120:123], v[20:23], v[80:83]
	v_mfma_f32_16x16x32_bf16 v[84:87], v[120:123], v[52:55], v[84:87]
	ds_read_b128 v[120:123], v164 offset:16384
	s_waitcnt lgkmcnt(7)
	v_mfma_f32_16x16x32_bf16 v[88:91], v[124:127], v[20:23], v[88:91]
	v_mfma_f32_16x16x32_bf16 v[92:95], v[124:127], v[52:55], v[92:95]
	ds_read_b128 v[124:127], v164 offset:24576
	s_waitcnt lgkmcnt(7)
	v_mfma_f32_16x16x32_bf16 v[64:67], v[96:99], v[24:27], v[64:67]
	v_mfma_f32_16x16x32_bf16 v[68:71], v[96:99], v[56:59], v[68:71]
	s_waitcnt lgkmcnt(6)
	v_mfma_f32_16x16x32_bf16 v[72:75], v[100:103], v[24:27], v[72:75]
	v_mfma_f32_16x16x32_bf16 v[76:79], v[100:103], v[56:59], v[76:79]
	s_waitcnt lgkmcnt(5)
	v_mfma_f32_16x16x32_bf16 v[80:83], v[104:107], v[24:27], v[80:83]
	v_mfma_f32_16x16x32_bf16 v[84:87], v[104:107], v[56:59], v[84:87]
	s_waitcnt lgkmcnt(4)
	v_mfma_f32_16x16x32_bf16 v[88:91], v[108:111], v[24:27], v[88:91]
	v_mfma_f32_16x16x32_bf16 v[92:95], v[108:111], v[56:59], v[92:95]
	s_waitcnt lgkmcnt(3)
	v_mfma_f32_16x16x32_bf16 v[64:67], v[112:115], v[28:31], v[64:67]
	v_mfma_f32_16x16x32_bf16 v[68:71], v[112:115], v[60:63], v[68:71]
	s_waitcnt lgkmcnt(2)
	v_mfma_f32_16x16x32_bf16 v[72:75], v[116:119], v[28:31], v[72:75]
	v_mfma_f32_16x16x32_bf16 v[76:79], v[116:119], v[60:63], v[76:79]
	s_waitcnt lgkmcnt(1)
	v_mfma_f32_16x16x32_bf16 v[80:83], v[120:123], v[28:31], v[80:83]
	v_mfma_f32_16x16x32_bf16 v[84:87], v[120:123], v[60:63], v[84:87]
	s_waitcnt lgkmcnt(0)
	v_mfma_f32_16x16x32_bf16 v[88:91], v[124:127], v[28:31], v[88:91]
	v_mfma_f32_16x16x32_bf16 v[92:95], v[124:127], v[60:63], v[92:95]
	v_or_b32_e32 v169, 0x10000, v165
	v_or_b32_e32 v170, 0x10000, v166
	v_or_b32_e32 v171, 0x10000, v167
	v_or_b32_e32 v172, 0x10000, v168
	ds_read_u16 v144, v169
	ds_read_u16 v145, v170
	ds_read_u16 v146, v171
	ds_read_u16 v147, v172
	ds_read_u16 v148, v169 offset:8192
	ds_read_u16 v149, v170 offset:8192
	ds_read_u16 v150, v171 offset:8192
	ds_read_u16 v151, v172 offset:8192
	ds_read_u16 v152, v169 offset:16384
	ds_read_u16 v153, v170 offset:16384
	ds_read_u16 v154, v171 offset:16384
	ds_read_u16 v155, v172 offset:16384
	ds_read_u16 v156, v169 offset:24576
	ds_read_u16 v157, v170 offset:24576
	ds_read_u16 v158, v171 offset:24576
	ds_read_u16 v159, v172 offset:24576
	s_nop 7
	v_fma_f32 v178, v64, s53, v173
	v_fma_f32 v179, v65, s53, v173
	v_fma_f32 v180, v66, s53, v173
	v_fma_f32 v181, v67, s53, v173
	v_fma_f32 v182, v72, s53, v173
	v_fma_f32 v183, v73, s53, v173
	v_fma_f32 v184, v74, s53, v173
	v_fma_f32 v185, v75, s53, v173
	v_fma_f32 v186, v68, s53, v174
	v_fma_f32 v187, v69, s53, v174
	v_fma_f32 v188, v70, s53, v174
	v_fma_f32 v189, v71, s53, v174
	v_fma_f32 v190, v76, s53, v174
	v_fma_f32 v191, v77, s53, v174
	v_fma_f32 v192, v78, s53, v174
	v_fma_f32 v193, v79, s53, v174
	v_exp_f32_e32 v178, v178
	v_exp_f32_e32 v179, v179
	v_exp_f32_e32 v180, v180
	v_exp_f32_e32 v181, v181
	v_exp_f32_e32 v182, v182
	v_exp_f32_e32 v183, v183
	v_exp_f32_e32 v184, v184
	v_exp_f32_e32 v185, v185
	v_exp_f32_e32 v186, v186
	v_exp_f32_e32 v187, v187
	v_exp_f32_e32 v188, v188
	v_exp_f32_e32 v189, v189
	v_exp_f32_e32 v190, v190
	v_exp_f32_e32 v191, v191
	v_exp_f32_e32 v192, v192
	v_exp_f32_e32 v193, v193
	v_add_f32_e32 v178, 1.0, v178
	v_add_f32_e32 v179, 1.0, v179
	v_add_f32_e32 v180, 1.0, v180
	v_add_f32_e32 v181, 1.0, v181
	v_add_f32_e32 v182, 1.0, v182
	v_add_f32_e32 v183, 1.0, v183
	v_add_f32_e32 v184, 1.0, v184
	v_add_f32_e32 v185, 1.0, v185
	v_add_f32_e32 v186, 1.0, v186
	v_add_f32_e32 v187, 1.0, v187
	v_add_f32_e32 v188, 1.0, v188
	v_add_f32_e32 v189, 1.0, v189
	v_add_f32_e32 v190, 1.0, v190
	v_add_f32_e32 v191, 1.0, v191
	v_add_f32_e32 v192, 1.0, v192
	v_add_f32_e32 v193, 1.0, v193
	v_rcp_f32_e32 v178, v178
	v_rcp_f32_e32 v179, v179
	v_rcp_f32_e32 v180, v180
	v_rcp_f32_e32 v181, v181
	v_rcp_f32_e32 v182, v182
	v_rcp_f32_e32 v183, v183
	v_rcp_f32_e32 v184, v184
	v_rcp_f32_e32 v185, v185
	v_rcp_f32_e32 v186, v186
	v_rcp_f32_e32 v187, v187
	v_rcp_f32_e32 v188, v188
	v_rcp_f32_e32 v189, v189
	v_rcp_f32_e32 v190, v190
	v_rcp_f32_e32 v191, v191
	v_rcp_f32_e32 v192, v192
	v_rcp_f32_e32 v193, v193
	v_mul_f32_e32 v178, v175, v178
	v_mul_f32_e32 v179, v175, v179
	v_mul_f32_e32 v180, v175, v180
	v_mul_f32_e32 v181, v175, v181
	v_mul_f32_e32 v182, v175, v182
	v_mul_f32_e32 v183, v175, v183
	v_mul_f32_e32 v184, v175, v184
	v_mul_f32_e32 v185, v175, v185
	v_exp_f32_e32 v96, v178
	v_exp_f32_e32 v97, v179
	v_exp_f32_e32 v98, v180
	v_exp_f32_e32 v99, v181
	v_exp_f32_e32 v100, v182
	v_exp_f32_e32 v101, v183
	v_exp_f32_e32 v102, v184
	v_exp_f32_e32 v103, v185
	s_nop 0
	v_fma_f32 v194, -v96, v96, 1.0
	v_fma_f32 v195, -v97, v97, 1.0
	v_fma_f32 v196, -v98, v98, 1.0
	v_fma_f32 v197, -v99, v99, 1.0
	v_fma_f32 v198, -v100, v100, 1.0
	v_fma_f32 v199, -v101, v101, 1.0
	v_fma_f32 v200, -v102, v102, 1.0
	v_fma_f32 v201, -v103, v103, 1.0
	v_max_f32_e32 v194, 0, v194
	v_max_f32_e32 v195, 0, v195
	v_max_f32_e32 v196, 0, v196
	v_max_f32_e32 v197, 0, v197
	v_max_f32_e32 v198, 0, v198
	v_max_f32_e32 v199, 0, v199
	v_max_f32_e32 v200, 0, v200
	v_max_f32_e32 v201, 0, v201
	v_sqrt_f32_e32 v194, v194
	v_sqrt_f32_e32 v195, v195
	v_sqrt_f32_e32 v196, v196
	v_sqrt_f32_e32 v197, v197
	v_sqrt_f32_e32 v198, v198
	v_sqrt_f32_e32 v199, v199
	v_sqrt_f32_e32 v200, v200
	v_sqrt_f32_e32 v201, v201
	s_waitcnt lgkmcnt(8)
	v_lshlrev_b32_e32 v144, 16, v144
	v_lshlrev_b32_e32 v145, 16, v145
	v_lshlrev_b32_e32 v146, 16, v146
	v_lshlrev_b32_e32 v147, 16, v147
	v_lshlrev_b32_e32 v148, 16, v148
	v_lshlrev_b32_e32 v149, 16, v149
	v_lshlrev_b32_e32 v150, 16, v150
	v_lshlrev_b32_e32 v151, 16, v151
	v_mul_f32_e32 v194, v194, v186
	v_mul_f32_e32 v195, v195, v187
	v_mul_f32_e32 v196, v196, v188
	v_mul_f32_e32 v197, v197, v189
	v_mul_f32_e32 v198, v198, v190
	v_mul_f32_e32 v199, v199, v191
	v_mul_f32_e32 v200, v200, v192
	v_mul_f32_e32 v201, v201, v193
	v_mul_f32_e32 v144, v194, v144
	v_mul_f32_e32 v145, v195, v145
	v_mul_f32_e32 v146, v196, v146
	v_mul_f32_e32 v147, v197, v147
	v_mul_f32_e32 v148, v198, v148
	v_mul_f32_e32 v149, v199, v149
	v_mul_f32_e32 v150, v200, v150
	v_mul_f32_e32 v151, v201, v151
	v_fma_f32 v178, v80, s53, v173
	v_fma_f32 v179, v81, s53, v173
	v_fma_f32 v180, v82, s53, v173
	v_fma_f32 v181, v83, s53, v173
	v_fma_f32 v182, v88, s53, v173
	v_fma_f32 v183, v89, s53, v173
	v_fma_f32 v184, v90, s53, v173
	v_fma_f32 v185, v91, s53, v173
	v_fma_f32 v186, v84, s53, v174
	v_fma_f32 v187, v85, s53, v174
	v_fma_f32 v188, v86, s53, v174
	v_fma_f32 v189, v87, s53, v174
	v_fma_f32 v190, v92, s53, v174
	v_fma_f32 v191, v93, s53, v174
	v_fma_f32 v192, v94, s53, v174
	v_fma_f32 v193, v95, s53, v174
	v_exp_f32_e32 v178, v178
	v_exp_f32_e32 v179, v179
	v_exp_f32_e32 v180, v180
	v_exp_f32_e32 v181, v181
	v_exp_f32_e32 v182, v182
	v_exp_f32_e32 v183, v183
	v_exp_f32_e32 v184, v184
	v_exp_f32_e32 v185, v185
	v_exp_f32_e32 v186, v186
	v_exp_f32_e32 v187, v187
	v_exp_f32_e32 v188, v188
	v_exp_f32_e32 v189, v189
	v_exp_f32_e32 v190, v190
	v_exp_f32_e32 v191, v191
	v_exp_f32_e32 v192, v192
	v_exp_f32_e32 v193, v193
	v_add_f32_e32 v178, 1.0, v178
	v_add_f32_e32 v179, 1.0, v179
	v_add_f32_e32 v180, 1.0, v180
	v_add_f32_e32 v181, 1.0, v181
	v_add_f32_e32 v182, 1.0, v182
	v_add_f32_e32 v183, 1.0, v183
	v_add_f32_e32 v184, 1.0, v184
	v_add_f32_e32 v185, 1.0, v185
	v_add_f32_e32 v186, 1.0, v186
	v_add_f32_e32 v187, 1.0, v187
	v_add_f32_e32 v188, 1.0, v188
	v_add_f32_e32 v189, 1.0, v189
	v_add_f32_e32 v190, 1.0, v190
	v_add_f32_e32 v191, 1.0, v191
	v_add_f32_e32 v192, 1.0, v192
	v_add_f32_e32 v193, 1.0, v193
	v_rcp_f32_e32 v178, v178
	v_rcp_f32_e32 v179, v179
	v_rcp_f32_e32 v180, v180
	v_rcp_f32_e32 v181, v181
	v_rcp_f32_e32 v182, v182
	v_rcp_f32_e32 v183, v183
	v_rcp_f32_e32 v184, v184
	v_rcp_f32_e32 v185, v185
	v_rcp_f32_e32 v186, v186
	v_rcp_f32_e32 v187, v187
	v_rcp_f32_e32 v188, v188
	v_rcp_f32_e32 v189, v189
	v_rcp_f32_e32 v190, v190
	v_rcp_f32_e32 v191, v191
	v_rcp_f32_e32 v192, v192
	v_rcp_f32_e32 v193, v193
	v_mul_f32_e32 v178, v175, v178
	v_mul_f32_e32 v179, v175, v179
	v_mul_f32_e32 v180, v175, v180
	v_mul_f32_e32 v181, v175, v181
	v_mul_f32_e32 v182, v175, v182
	v_mul_f32_e32 v183, v175, v183
	v_mul_f32_e32 v184, v175, v184
	v_mul_f32_e32 v185, v175, v185
	v_exp_f32_e32 v104, v178
	v_exp_f32_e32 v105, v179
	v_exp_f32_e32 v106, v180
	v_exp_f32_e32 v107, v181
	v_exp_f32_e32 v108, v182
	v_exp_f32_e32 v109, v183
	v_exp_f32_e32 v110, v184
	v_exp_f32_e32 v111, v185
	s_nop 0
	v_fma_f32 v194, -v104, v104, 1.0
	v_fma_f32 v195, -v105, v105, 1.0
	v_fma_f32 v196, -v106, v106, 1.0
	v_fma_f32 v197, -v107, v107, 1.0
	v_fma_f32 v198, -v108, v108, 1.0
	v_fma_f32 v199, -v109, v109, 1.0
	v_fma_f32 v200, -v110, v110, 1.0
	v_fma_f32 v201, -v111, v111, 1.0
	v_max_f32_e32 v194, 0, v194
	v_max_f32_e32 v195, 0, v195
	v_max_f32_e32 v196, 0, v196
	v_max_f32_e32 v197, 0, v197
	v_max_f32_e32 v198, 0, v198
	v_max_f32_e32 v199, 0, v199
	v_max_f32_e32 v200, 0, v200
	v_max_f32_e32 v201, 0, v201
	v_sqrt_f32_e32 v194, v194
	v_sqrt_f32_e32 v195, v195
	v_sqrt_f32_e32 v196, v196
	v_sqrt_f32_e32 v197, v197
	v_sqrt_f32_e32 v198, v198
	v_sqrt_f32_e32 v199, v199
	v_sqrt_f32_e32 v200, v200
	v_sqrt_f32_e32 v201, v201
	s_waitcnt lgkmcnt(0)
	v_lshlrev_b32_e32 v152, 16, v152
	v_lshlrev_b32_e32 v153, 16, v153
	v_lshlrev_b32_e32 v154, 16, v154
	v_lshlrev_b32_e32 v155, 16, v155
	v_lshlrev_b32_e32 v156, 16, v156
	v_lshlrev_b32_e32 v157, 16, v157
	v_lshlrev_b32_e32 v158, 16, v158
	v_lshlrev_b32_e32 v159, 16, v159
	v_mul_f32_e32 v194, v194, v186
	v_mul_f32_e32 v195, v195, v187
	v_mul_f32_e32 v196, v196, v188
	v_mul_f32_e32 v197, v197, v189
	v_mul_f32_e32 v198, v198, v190
	v_mul_f32_e32 v199, v199, v191
	v_mul_f32_e32 v200, v200, v192
	v_mul_f32_e32 v201, v201, v193
	v_mul_f32_e32 v152, v194, v152
	v_mul_f32_e32 v153, v195, v153
	v_mul_f32_e32 v154, v196, v154
	v_mul_f32_e32 v155, v197, v155
	v_mul_f32_e32 v156, v198, v156
	v_mul_f32_e32 v157, v199, v157
	v_mul_f32_e32 v158, v200, v158
	v_mul_f32_e32 v159, v201, v159
	v_fma_f32 v146, v98, v147, v146
	v_fma_f32 v150, v102, v151, v150
	v_fma_f32 v154, v106, v155, v154
	v_fma_f32 v158, v110, v159, v158
	v_mul_f32_e32 v98, v98, v99
	v_mul_f32_e32 v102, v102, v103
	v_mul_f32_e32 v106, v106, v107
	v_mul_f32_e32 v110, v110, v111
	v_fma_f32 v145, v97, v146, v145
	v_fma_f32 v149, v101, v150, v149
	v_fma_f32 v153, v105, v154, v153
	v_fma_f32 v157, v109, v158, v157
	v_mul_f32_e32 v97, v97, v98
	v_mul_f32_e32 v101, v101, v102
	v_mul_f32_e32 v105, v105, v106
	v_mul_f32_e32 v109, v109, v110
	v_fma_f32 v144, v96, v145, v144
	v_fma_f32 v148, v100, v149, v148
	v_fma_f32 v152, v104, v153, v152
	v_fma_f32 v156, v108, v157, v156
	v_mul_f32_e32 v96, v96, v97
	v_mul_f32_e32 v100, v100, v101
	v_mul_f32_e32 v104, v104, v105
	v_mul_f32_e32 v108, v108, v109
	ds_bpermute_b32 v178, v204, v96
	ds_bpermute_b32 v182, v204, v144
	ds_bpermute_b32 v179, v204, v100
	ds_bpermute_b32 v183, v204, v148
	ds_bpermute_b32 v180, v204, v104
	ds_bpermute_b32 v184, v204, v152
	ds_bpermute_b32 v181, v204, v108
	ds_bpermute_b32 v185, v204, v156
	s_waitcnt lgkmcnt(0)
	v_fma_f32 v186, v182, v96, v144
	v_cndmask_b32_e64 v178, 1.0, v178, s[34:35]
	v_fma_f32 v187, v183, v100, v148
	v_cndmask_b32_e64 v179, 1.0, v179, s[34:35]
	v_fma_f32 v188, v184, v104, v152
	v_cndmask_b32_e64 v180, 1.0, v180, s[34:35]
	v_fma_f32 v189, v185, v108, v156
	v_cndmask_b32_e64 v181, 1.0, v181, s[34:35]
	v_cndmask_b32_e64 v223, v144, v186, s[34:35]
	v_mul_f32_e32 v219, v96, v178
	v_cndmask_b32_e64 v224, v148, v187, s[34:35]
	v_mul_f32_e32 v220, v100, v179
	v_cndmask_b32_e64 v225, v152, v188, s[34:35]
	v_mul_f32_e32 v221, v104, v180
	v_cndmask_b32_e64 v226, v156, v189, s[34:35]
	v_mul_f32_e32 v222, v108, v181
	ds_bpermute_b32 v178, v205, v219
	ds_bpermute_b32 v182, v205, v223
	ds_bpermute_b32 v179, v205, v220
	ds_bpermute_b32 v183, v205, v224
	ds_bpermute_b32 v180, v205, v221
	ds_bpermute_b32 v184, v205, v225
	ds_bpermute_b32 v181, v205, v222
	ds_bpermute_b32 v185, v205, v226
	s_waitcnt lgkmcnt(0)
	v_fma_f32 v186, v182, v219, v223
	v_cndmask_b32_e64 v178, 1.0, v178, s[36:37]
	v_fma_f32 v187, v183, v220, v224
	v_cndmask_b32_e64 v179, 1.0, v179, s[36:37]
	v_fma_f32 v188, v184, v221, v225
	v_cndmask_b32_e64 v180, 1.0, v180, s[36:37]
	v_fma_f32 v189, v185, v222, v226
	v_cndmask_b32_e64 v181, 1.0, v181, s[36:37]
	v_cndmask_b32_e64 v223, v223, v186, s[36:37]
	v_mul_f32_e32 v219, v219, v178
	v_cndmask_b32_e64 v224, v224, v187, s[36:37]
	v_mul_f32_e32 v220, v220, v179
	v_cndmask_b32_e64 v225, v225, v188, s[36:37]
	v_mul_f32_e32 v221, v221, v180
	v_cndmask_b32_e64 v226, v226, v189, s[36:37]
	v_mul_f32_e32 v222, v222, v181
	ds_bpermute_b32 v227, v204, v219
	ds_bpermute_b32 v231, v204, v223
	ds_bpermute_b32 v235, v206, v219
	ds_bpermute_b32 v239, v206, v223
	ds_bpermute_b32 v228, v204, v220
	ds_bpermute_b32 v232, v204, v224
	ds_bpermute_b32 v236, v206, v220
	ds_bpermute_b32 v244, v206, v224
	ds_bpermute_b32 v229, v204, v221
	ds_bpermute_b32 v233, v204, v225
	ds_bpermute_b32 v237, v206, v221
	ds_bpermute_b32 v245, v206, v225
	ds_bpermute_b32 v230, v204, v222
	ds_bpermute_b32 v234, v204, v226
	ds_bpermute_b32 v238, v206, v222
	ds_bpermute_b32 v246, v206, v226
	s_waitcnt lgkmcnt(0)
	v_cndmask_b32_e64 v227, 1.0, v227, s[34:35]
	v_cndmask_b32_e64 v231, 0, v231, s[34:35]
	v_cndmask_b32_e64 v228, 1.0, v228, s[34:35]
	v_cndmask_b32_e64 v232, 0, v232, s[34:35]
	v_cndmask_b32_e64 v229, 1.0, v229, s[34:35]
	v_cndmask_b32_e64 v233, 0, v233, s[34:35]
	v_cndmask_b32_e64 v230, 1.0, v230, s[34:35]
	v_cndmask_b32_e64 v234, 0, v234, s[34:35]
	v_mov_b32_e32 v190, v238
	v_mov_b32_e32 v194, v246
	v_mov_b32_e32 v198, v190
	v_mov_b32_e32 v201, v194
	v_fma_f32 v194, v194, v237, v245
	v_mul_f32_e32 v190, v190, v237
	v_mov_b32_e32 v199, v190
	v_mov_b32_e32 v177, v194
	v_fma_f32 v194, v194, v236, v244
	v_mul_f32_e32 v190, v190, v236
	v_mov_b32_e32 v200, v190
	v_mov_b32_e32 v203, v194
	v_fma_f32 v194, v194, v235, v239
	v_mul_f32_e32 v190, v190, v235
	v_mov_b32_e32 v191, v194
	ds_write_b64 v207, v[190:191] offset:1024
	s_waitcnt vmcnt(0)
	s_waitcnt lgkmcnt(0)
	s_barrier
	s_cmp_gt_u32 s13, 15
	s_cbranch_scc1 .Lmylru_nodma_6
	s_add_i32 s58, s13, 2
	s_cmp_lt_u32 s58, 2
	s_sub_i32 s50, 1, s58
	s_lshl_b32 s50, s50, 7
	s_lshl_b32 s51, s9, 8
	s_add_i32 s51, s51, 0x8000
	s_add_i32 s51, s51, s50
	s_sub_i32 s50, 17, s58
	s_lshl_b32 s50, s50, 7
	s_lshl_b32 s59, s9, 11
	s_add_i32 s59, s59, s50
	s_cmp_lt_u32 s58, 2
	s_cselect_b32 s59, s51, s59
	s_lshl_b32 s52, s59, 11
	s_add_u32 s46, s16, s52
	s_addc_u32 s47, s17, 0
	s_lshl_b32 s52, s6, 13
	s_add_i32 s52, s52, 0x10000
	s_mov_b32 m0, s52
	s_add_i32 s52, s52, 0x400
	global_load_lds_dwordx4 v211, s[46:47]
	s_mov_b32 m0, s52
	s_add_i32 s52, s52, 0x400
	global_load_lds_dwordx4 v212, s[46:47]
	s_mov_b32 m0, s52
	s_add_i32 s52, s52, 0x400
	global_load_lds_dwordx4 v213, s[46:47]
	s_mov_b32 m0, s52
	s_add_i32 s52, s52, 0x400
	global_load_lds_dwordx4 v214, s[46:47]
	s_mov_b32 m0, s52
	s_add_i32 s52, s52, 0x400
	global_load_lds_dwordx4 v215, s[46:47]
	s_mov_b32 m0, s52
	s_add_i32 s52, s52, 0x400
	global_load_lds_dwordx4 v216, s[46:47]
	s_mov_b32 m0, s52
	s_add_i32 s52, s52, 0x400
	global_load_lds_dwordx4 v217, s[46:47]
	s_mov_b32 m0, s52
	s_nop 0
	global_load_lds_dwordx4 v218, s[46:47]
.Lmylru_nodma_6:
	ds_read_b64 v[178:179], v208 offset:1536
	ds_read_b64 v[180:181], v208 offset:1024
	s_waitcnt lgkmcnt(0)
	v_fma_f32 v182, v176, v178, v179
	v_cndmask_b32_e64 v183, v176, v182, s[38:39]
	v_fma_f32 v176, v182, v180, v181
	s_add_i32 s13, s13, 1
	s_mov_b32 s60, 8
.Lmylru_loop_1:
	s_sub_i32 s54, 17, s13
	s_lshl_b32 s55, s54, 14
	s_lshl_b32 s56, s6, 11
	s_add_i32 s55, s55, s56
	s_add_u32 s44, s22, s55
	s_addc_u32 s45, s23, 0
	s_cmp_lt_u32 s13, 2
	s_sub_i32 s50, 1, s13
	s_lshl_b32 s50, s50, 7
	s_lshl_b32 s51, s9, 8
	s_add_i32 s51, s51, 0x8000
	s_add_i32 s51, s51, s50
	s_sub_i32 s50, 17, s13
	s_lshl_b32 s50, s50, 7
	s_lshl_b32 s57, s9, 11
	s_add_i32 s57, s57, s50
	s_cmp_lt_u32 s13, 2
	s_cselect_b32 s57, s51, s57
	s_lshl_b32 s57, s57, 11
	s_add_u32 s40, s18, s57
	s_addc_u32 s41, s19, 0
	s_add_u32 s42, s20, s57
	s_addc_u32 s43, s21, 0
	global_load_dword v247, v209, s[44:45]
	global_load_dword v248, v209, s[44:45] offset:256
	global_load_dword v249, v209, s[44:45] offset:512
	global_load_dword v250, v209, s[44:45] offset:768
	global_load_dword v251, v209, s[44:45] offset:1024
	global_load_dword v252, v209, s[44:45] offset:1280
	global_load_dword v253, v209, s[44:45] offset:1536
	global_load_dword v254, v209, s[44:45] offset:1792
	v_add_u32_e32 v182, 0x0, v210
	v_add_u32_e32 v183, 0x1000, v182
	global_load_ushort v128, v182, s[40:41]
	global_load_ushort v129, v182, s[40:41] offset:2048
	global_load_ushort v130, v183, s[40:41]
	global_load_ushort v131, v183, s[40:41] offset:2048
	v_add_u32_e32 v182, 0x8000, v210
	v_add_u32_e32 v183, 0x1000, v182
	global_load_ushort v132, v182, s[40:41]
	global_load_ushort v133, v182, s[40:41] offset:2048
	global_load_ushort v134, v183, s[40:41]
	global_load_ushort v135, v183, s[40:41] offset:2048
	v_add_u32_e32 v182, 0x10000, v210
	v_add_u32_e32 v183, 0x1000, v182
	global_load_ushort v136, v182, s[40:41]
	global_load_ushort v137, v182, s[40:41] offset:2048
	global_load_ushort v138, v183, s[40:41]
	global_load_ushort v139, v183, s[40:41] offset:2048
	v_add_u32_e32 v182, 0x18000, v210
	v_add_u32_e32 v183, 0x1000, v182
	global_load_ushort v140, v182, s[40:41]
	global_load_ushort v141, v182, s[40:41] offset:2048
	global_load_ushort v142, v183, s[40:41]
	global_load_ushort v143, v183, s[40:41] offset:2048
	v_mov_b32_e32 v163, v162
	ds_read_b128 v[96:99], v163
	ds_read_b128 v[100:103], v163 offset:8192
	ds_read_b128 v[104:107], v163 offset:16384
	ds_read_b128 v[108:111], v163 offset:24576
	v_xor_b32_e32 v164, 0x40, v163
	ds_read_b128 v[112:115], v164
	ds_read_b128 v[116:119], v164 offset:8192
	ds_read_b128 v[120:123], v164 offset:16384
	ds_read_b128 v[124:127], v164 offset:24576
	s_waitcnt lgkmcnt(7)
	v_mfma_f32_16x16x32_bf16 v[64:67], v[96:99], v[0:3], 0
	v_mfma_f32_16x16x32_bf16 v[68:71], v[96:99], v[32:35], 0
	v_xor_b32_e32 v164, 0x80, v163
	ds_read_b128 v[96:99], v164
	s_waitcnt lgkmcnt(7)
	v_mfma_f32_16x16x32_bf16 v[72:75], v[100:103], v[0:3], 0
	v_mfma_f32_16x16x32_bf16 v[76:79], v[100:103], v[32:35], 0
	ds_read_b128 v[100:103], v164 offset:8192
	s_waitcnt lgkmcnt(7)
	v_mfma_f32_16x16x32_bf16 v[80:83], v[104:107], v[0:3], 0
	v_mfma_f32_16x16x32_bf16 v[84:87], v[104:107], v[32:35], 0
	ds_read_b128 v[104:107], v164 offset:16384
	s_waitcnt lgkmcnt(7)
	v_mfma_f32_16x16x32_bf16 v[88:91], v[108:111], v[0:3], 0
	v_mfma_f32_16x16x32_bf16 v[92:95], v[108:111], v[32:35], 0
	ds_read_b128 v[108:111], v164 offset:24576
	s_waitcnt lgkmcnt(7)
	v_mfma_f32_16x16x32_bf16 v[64:67], v[112:115], v[4:7], v[64:67]
	v_mfma_f32_16x16x32_bf16 v[68:71], v[112:115], v[36:39], v[68:71]
	v_xor_b32_e32 v164, 0xc0, v163
	ds_read_b128 v[112:115], v164
	s_waitcnt lgkmcnt(7)
	v_mfma_f32_16x16x32_bf16 v[72:75], v[116:119], v[4:7], v[72:75]
	v_mfma_f32_16x16x32_bf16 v[76:79], v[116:119], v[36:39], v[76:79]
	ds_read_b128 v[116:119], v164 offset:8192
	s_waitcnt lgkmcnt(7)
	v_mfma_f32_16x16x32_bf16 v[80:83], v[120:123], v[4:7], v[80:83]
	v_mfma_f32_16x16x32_bf16 v[84:87], v[120:123], v[36:39], v[84:87]
	ds_read_b128 v[120:123], v164 offset:16384
	s_waitcnt lgkmcnt(7)
	v_mfma_f32_16x16x32_bf16 v[88:91], v[124:127], v[4:7], v[88:91]
	v_mfma_f32_16x16x32_bf16 v[92:95], v[124:127], v[36:39], v[92:95]
	ds_read_b128 v[124:127], v164 offset:24576
	s_waitcnt lgkmcnt(7)
	v_mfma_f32_16x16x32_bf16 v[64:67], v[96:99], v[8:11], v[64:67]
	v_mfma_f32_16x16x32_bf16 v[68:71], v[96:99], v[40:43], v[68:71]
	v_xor_b32_e32 v164, 0x100, v163
	ds_read_b128 v[96:99], v164
	s_waitcnt lgkmcnt(7)
	v_mfma_f32_16x16x32_bf16 v[72:75], v[100:103], v[8:11], v[72:75]
	v_mfma_f32_16x16x32_bf16 v[76:79], v[100:103], v[40:43], v[76:79]
	ds_read_b128 v[100:103], v164 offset:8192
	s_waitcnt lgkmcnt(7)
	v_mfma_f32_16x16x32_bf16 v[80:83], v[104:107], v[8:11], v[80:83]
	v_mfma_f32_16x16x32_bf16 v[84:87], v[104:107], v[40:43], v[84:87]
	ds_read_b128 v[104:107], v164 offset:16384
	s_waitcnt lgkmcnt(7)
	v_mfma_f32_16x16x32_bf16 v[88:91], v[108:111], v[8:11], v[88:91]
	v_mfma_f32_16x16x32_bf16 v[92:95], v[108:111], v[40:43], v[92:95]
	ds_read_b128 v[108:111], v164 offset:24576
	s_waitcnt lgkmcnt(7)
	v_mfma_f32_16x16x32_bf16 v[64:67], v[112:115], v[12:15], v[64:67]
	v_mfma_f32_16x16x32_bf16 v[68:71], v[112:115], v[44:47], v[68:71]
	v_xor_b32_e32 v164, 0x140, v163
	ds_read_b128 v[112:115], v164
	s_waitcnt lgkmcnt(7)
	v_mfma_f32_16x16x32_bf16 v[72:75], v[116:119], v[12:15], v[72:75]
	v_mfma_f32_16x16x32_bf16 v[76:79], v[116:119], v[44:47], v[76:79]
	ds_read_b128 v[116:119], v164 offset:8192
	s_waitcnt lgkmcnt(7)
	v_mfma_f32_16x16x32_bf16 v[80:83], v[120:123], v[12:15], v[80:83]
	v_mfma_f32_16x16x32_bf16 v[84:87], v[120:123], v[44:47], v[84:87]
	ds_read_b128 v[120:123], v164 offset:16384
	s_waitcnt lgkmcnt(7)
	v_mfma_f32_16x16x32_bf16 v[88:91], v[124:127], v[12:15], v[88:91]
	v_mfma_f32_16x16x32_bf16 v[92:95], v[124:127], v[44:47], v[92:95]
	ds_read_b128 v[124:127], v164 offset:24576
	s_waitcnt lgkmcnt(7)
	v_mfma_f32_16x16x32_bf16 v[64:67], v[96:99], v[16:19], v[64:67]
	v_mfma_f32_16x16x32_bf16 v[68:71], v[96:99], v[48:51], v[68:71]
	v_xor_b32_e32 v164, 0x180, v163
	ds_read_b128 v[96:99], v164
	s_waitcnt lgkmcnt(7)
	v_mfma_f32_16x16x32_bf16 v[72:75], v[100:103], v[16:19], v[72:75]
	v_mfma_f32_16x16x32_bf16 v[76:79], v[100:103], v[48:51], v[76:79]
	ds_read_b128 v[100:103], v164 offset:8192
	s_waitcnt lgkmcnt(7)
	v_mfma_f32_16x16x32_bf16 v[80:83], v[104:107], v[16:19], v[80:83]
	v_mfma_f32_16x16x32_bf16 v[84:87], v[104:107], v[48:51], v[84:87]
	ds_read_b128 v[104:107], v164 offset:16384
	s_waitcnt lgkmcnt(7)
	v_mfma_f32_16x16x32_bf16 v[88:91], v[108:111], v[16:19], v[88:91]
	v_mfma_f32_16x16x32_bf16 v[92:95], v[108:111], v[48:51], v[92:95]
	ds_read_b128 v[108:111], v164 offset:24576
	s_waitcnt lgkmcnt(7)
	v_mfma_f32_16x16x32_bf16 v[64:67], v[112:115], v[20:23], v[64:67]
	v_mfma_f32_16x16x32_bf16 v[68:71], v[112:115], v[52:55], v[68:71]
	v_xor_b32_e32 v164, 0x1c0, v163
	ds_read_b128 v[112:115], v164
	s_waitcnt lgkmcnt(7)
	v_mfma_f32_16x16x32_bf16 v[72:75], v[116:119], v[20:23], v[72:75]
	v_mfma_f32_16x16x32_bf16 v[76:79], v[116:119], v[52:55], v[76:79]
	ds_read_b128 v[116:119], v164 offset:8192
	s_waitcnt lgkmcnt(7)
	v_mfma_f32_16x16x32_bf16 v[80:83], v[120:123], v[20:23], v[80:83]
	v_mfma_f32_16x16x32_bf16 v[84:87], v[120:123], v[52:55], v[84:87]
	ds_read_b128 v[120:123], v164 offset:16384
	s_waitcnt lgkmcnt(7)
	v_mfma_f32_16x16x32_bf16 v[88:91], v[124:127], v[20:23], v[88:91]
	v_mfma_f32_16x16x32_bf16 v[92:95], v[124:127], v[52:55], v[92:95]
	ds_read_b128 v[124:127], v164 offset:24576
	s_waitcnt lgkmcnt(7)
	v_mfma_f32_16x16x32_bf16 v[64:67], v[96:99], v[24:27], v[64:67]
	v_mfma_f32_16x16x32_bf16 v[68:71], v[96:99], v[56:59], v[68:71]
	s_waitcnt lgkmcnt(6)
	v_mfma_f32_16x16x32_bf16 v[72:75], v[100:103], v[24:27], v[72:75]
	v_mfma_f32_16x16x32_bf16 v[76:79], v[100:103], v[56:59], v[76:79]
	s_waitcnt lgkmcnt(5)
	v_mfma_f32_16x16x32_bf16 v[80:83], v[104:107], v[24:27], v[80:83]
	v_mfma_f32_16x16x32_bf16 v[84:87], v[104:107], v[56:59], v[84:87]
	s_waitcnt lgkmcnt(4)
	v_mfma_f32_16x16x32_bf16 v[88:91], v[108:111], v[24:27], v[88:91]
	v_mfma_f32_16x16x32_bf16 v[92:95], v[108:111], v[56:59], v[92:95]
	s_waitcnt lgkmcnt(3)
	v_mfma_f32_16x16x32_bf16 v[64:67], v[112:115], v[28:31], v[64:67]
	v_mfma_f32_16x16x32_bf16 v[68:71], v[112:115], v[60:63], v[68:71]
	s_waitcnt lgkmcnt(2)
	v_mfma_f32_16x16x32_bf16 v[72:75], v[116:119], v[28:31], v[72:75]
	v_mfma_f32_16x16x32_bf16 v[76:79], v[116:119], v[60:63], v[76:79]
	s_waitcnt lgkmcnt(1)
	v_mfma_f32_16x16x32_bf16 v[80:83], v[120:123], v[28:31], v[80:83]
	v_mfma_f32_16x16x32_bf16 v[84:87], v[120:123], v[60:63], v[84:87]
	s_waitcnt lgkmcnt(0)
	v_mfma_f32_16x16x32_bf16 v[88:91], v[124:127], v[28:31], v[88:91]
	v_mfma_f32_16x16x32_bf16 v[92:95], v[124:127], v[60:63], v[92:95]
	v_mov_b32_e32 v169, v165
	v_mov_b32_e32 v170, v166
	v_mov_b32_e32 v171, v167
	v_mov_b32_e32 v172, v168
	ds_read_u16 v144, v169
	ds_read_u16 v145, v170
	ds_read_u16 v146, v171
	ds_read_u16 v147, v172
	ds_read_u16 v148, v169 offset:8192
	ds_read_u16 v149, v170 offset:8192
	ds_read_u16 v150, v171 offset:8192
	ds_read_u16 v151, v172 offset:8192
	ds_read_u16 v152, v169 offset:16384
	ds_read_u16 v153, v170 offset:16384
	ds_read_u16 v154, v171 offset:16384
	ds_read_u16 v155, v172 offset:16384
	ds_read_u16 v156, v169 offset:24576
	ds_read_u16 v157, v170 offset:24576
	ds_read_u16 v158, v171 offset:24576
	ds_read_u16 v159, v172 offset:24576
	s_nop 7
	v_fma_f32 v178, v64, s53, v173
	v_fma_f32 v179, v65, s53, v173
	v_fma_f32 v180, v66, s53, v173
	v_fma_f32 v181, v67, s53, v173
	v_fma_f32 v182, v72, s53, v173
	v_fma_f32 v183, v73, s53, v173
	v_fma_f32 v184, v74, s53, v173
	v_fma_f32 v185, v75, s53, v173
	v_fma_f32 v186, v68, s53, v174
	v_fma_f32 v187, v69, s53, v174
	v_fma_f32 v188, v70, s53, v174
	v_fma_f32 v189, v71, s53, v174
	v_fma_f32 v190, v76, s53, v174
	v_fma_f32 v191, v77, s53, v174
	v_fma_f32 v192, v78, s53, v174
	v_fma_f32 v193, v79, s53, v174
	v_exp_f32_e32 v178, v178
	v_exp_f32_e32 v179, v179
	v_exp_f32_e32 v180, v180
	v_exp_f32_e32 v181, v181
	v_exp_f32_e32 v182, v182
	v_exp_f32_e32 v183, v183
	v_exp_f32_e32 v184, v184
	v_exp_f32_e32 v185, v185
	v_exp_f32_e32 v186, v186
	v_exp_f32_e32 v187, v187
	v_exp_f32_e32 v188, v188
	v_exp_f32_e32 v189, v189
	v_exp_f32_e32 v190, v190
	v_exp_f32_e32 v191, v191
	v_exp_f32_e32 v192, v192
	v_exp_f32_e32 v193, v193
	v_add_f32_e32 v178, 1.0, v178
	v_add_f32_e32 v179, 1.0, v179
	v_add_f32_e32 v180, 1.0, v180
	v_add_f32_e32 v181, 1.0, v181
	v_add_f32_e32 v182, 1.0, v182
	v_add_f32_e32 v183, 1.0, v183
	v_add_f32_e32 v184, 1.0, v184
	v_add_f32_e32 v185, 1.0, v185
	v_add_f32_e32 v186, 1.0, v186
	v_add_f32_e32 v187, 1.0, v187
	v_add_f32_e32 v188, 1.0, v188
	v_add_f32_e32 v189, 1.0, v189
	v_add_f32_e32 v190, 1.0, v190
	v_add_f32_e32 v191, 1.0, v191
	v_add_f32_e32 v192, 1.0, v192
	v_add_f32_e32 v193, 1.0, v193
	v_rcp_f32_e32 v178, v178
	v_rcp_f32_e32 v179, v179
	v_rcp_f32_e32 v180, v180
	v_rcp_f32_e32 v181, v181
	v_rcp_f32_e32 v182, v182
	v_rcp_f32_e32 v183, v183
	v_rcp_f32_e32 v184, v184
	v_rcp_f32_e32 v185, v185
	v_rcp_f32_e32 v186, v186
	v_rcp_f32_e32 v187, v187
	v_rcp_f32_e32 v188, v188
	v_rcp_f32_e32 v189, v189
	v_rcp_f32_e32 v190, v190
	v_rcp_f32_e32 v191, v191
	v_rcp_f32_e32 v192, v192
	v_rcp_f32_e32 v193, v193
	v_mul_f32_e32 v178, v175, v178
	v_mul_f32_e32 v179, v175, v179
	v_mul_f32_e32 v180, v175, v180
	v_mul_f32_e32 v181, v175, v181
	v_mul_f32_e32 v182, v175, v182
	v_mul_f32_e32 v183, v175, v183
	v_mul_f32_e32 v184, v175, v184
	v_mul_f32_e32 v185, v175, v185
	v_exp_f32_e32 v96, v178
	v_exp_f32_e32 v97, v179
	v_exp_f32_e32 v98, v180
	v_exp_f32_e32 v99, v181
	v_exp_f32_e32 v100, v182
	v_exp_f32_e32 v101, v183
	v_exp_f32_e32 v102, v184
	v_exp_f32_e32 v103, v185
	s_nop 0
	v_fma_f32 v194, -v96, v96, 1.0
	v_fma_f32 v195, -v97, v97, 1.0
	v_fma_f32 v196, -v98, v98, 1.0
	v_fma_f32 v197, -v99, v99, 1.0
	v_fma_f32 v198, -v100, v100, 1.0
	v_fma_f32 v199, -v101, v101, 1.0
	v_fma_f32 v200, -v102, v102, 1.0
	v_fma_f32 v201, -v103, v103, 1.0
	v_max_f32_e32 v194, 0, v194
	v_max_f32_e32 v195, 0, v195
	v_max_f32_e32 v196, 0, v196
	v_max_f32_e32 v197, 0, v197
	v_max_f32_e32 v198, 0, v198
	v_max_f32_e32 v199, 0, v199
	v_max_f32_e32 v200, 0, v200
	v_max_f32_e32 v201, 0, v201
	v_sqrt_f32_e32 v194, v194
	v_sqrt_f32_e32 v195, v195
	v_sqrt_f32_e32 v196, v196
	v_sqrt_f32_e32 v197, v197
	v_sqrt_f32_e32 v198, v198
	v_sqrt_f32_e32 v199, v199
	v_sqrt_f32_e32 v200, v200
	v_sqrt_f32_e32 v201, v201
	s_waitcnt lgkmcnt(8)
	v_lshlrev_b32_e32 v144, 16, v144
	v_lshlrev_b32_e32 v145, 16, v145
	v_lshlrev_b32_e32 v146, 16, v146
	v_lshlrev_b32_e32 v147, 16, v147
	v_lshlrev_b32_e32 v148, 16, v148
	v_lshlrev_b32_e32 v149, 16, v149
	v_lshlrev_b32_e32 v150, 16, v150
	v_lshlrev_b32_e32 v151, 16, v151
	v_mul_f32_e32 v194, v194, v186
	v_mul_f32_e32 v195, v195, v187
	v_mul_f32_e32 v196, v196, v188
	v_mul_f32_e32 v197, v197, v189
	v_mul_f32_e32 v198, v198, v190
	v_mul_f32_e32 v199, v199, v191
	v_mul_f32_e32 v200, v200, v192
	v_mul_f32_e32 v201, v201, v193
	v_mul_f32_e32 v144, v194, v144
	v_mul_f32_e32 v145, v195, v145
	v_mul_f32_e32 v146, v196, v146
	v_mul_f32_e32 v147, v197, v147
	v_mul_f32_e32 v148, v198, v148
	v_mul_f32_e32 v149, v199, v149
	v_mul_f32_e32 v150, v200, v150
	v_mul_f32_e32 v151, v201, v151
	v_fma_f32 v178, v80, s53, v173
	v_fma_f32 v179, v81, s53, v173
	v_fma_f32 v180, v82, s53, v173
	v_fma_f32 v181, v83, s53, v173
	v_fma_f32 v182, v88, s53, v173
	v_fma_f32 v183, v89, s53, v173
	v_fma_f32 v184, v90, s53, v173
	v_fma_f32 v185, v91, s53, v173
	v_fma_f32 v186, v84, s53, v174
	v_fma_f32 v187, v85, s53, v174
	v_fma_f32 v188, v86, s53, v174
	v_fma_f32 v189, v87, s53, v174
	v_fma_f32 v190, v92, s53, v174
	v_fma_f32 v191, v93, s53, v174
	v_fma_f32 v192, v94, s53, v174
	v_fma_f32 v193, v95, s53, v174
	v_exp_f32_e32 v178, v178
	v_exp_f32_e32 v179, v179
	v_exp_f32_e32 v180, v180
	v_exp_f32_e32 v181, v181
	v_exp_f32_e32 v182, v182
	v_exp_f32_e32 v183, v183
	v_exp_f32_e32 v184, v184
	v_exp_f32_e32 v185, v185
	v_exp_f32_e32 v186, v186
	v_exp_f32_e32 v187, v187
	v_exp_f32_e32 v188, v188
	v_exp_f32_e32 v189, v189
	v_exp_f32_e32 v190, v190
	v_exp_f32_e32 v191, v191
	v_exp_f32_e32 v192, v192
	v_exp_f32_e32 v193, v193
	v_add_f32_e32 v178, 1.0, v178
	v_add_f32_e32 v179, 1.0, v179
	v_add_f32_e32 v180, 1.0, v180
	v_add_f32_e32 v181, 1.0, v181
	v_add_f32_e32 v182, 1.0, v182
	v_add_f32_e32 v183, 1.0, v183
	v_add_f32_e32 v184, 1.0, v184
	v_add_f32_e32 v185, 1.0, v185
	v_add_f32_e32 v186, 1.0, v186
	v_add_f32_e32 v187, 1.0, v187
	v_add_f32_e32 v188, 1.0, v188
	v_add_f32_e32 v189, 1.0, v189
	v_add_f32_e32 v190, 1.0, v190
	v_add_f32_e32 v191, 1.0, v191
	v_add_f32_e32 v192, 1.0, v192
	v_add_f32_e32 v193, 1.0, v193
	v_rcp_f32_e32 v178, v178
	v_rcp_f32_e32 v179, v179
	v_rcp_f32_e32 v180, v180
	v_rcp_f32_e32 v181, v181
	v_rcp_f32_e32 v182, v182
	v_rcp_f32_e32 v183, v183
	v_rcp_f32_e32 v184, v184
	v_rcp_f32_e32 v185, v185
	v_rcp_f32_e32 v186, v186
	v_rcp_f32_e32 v187, v187
	v_rcp_f32_e32 v188, v188
	v_rcp_f32_e32 v189, v189
	v_rcp_f32_e32 v190, v190
	v_rcp_f32_e32 v191, v191
	v_rcp_f32_e32 v192, v192
	v_rcp_f32_e32 v193, v193
	v_mul_f32_e32 v178, v175, v178
	v_mul_f32_e32 v179, v175, v179
	v_mul_f32_e32 v180, v175, v180
	v_mul_f32_e32 v181, v175, v181
	v_mul_f32_e32 v182, v175, v182
	v_mul_f32_e32 v183, v175, v183
	v_mul_f32_e32 v184, v175, v184
	v_mul_f32_e32 v185, v175, v185
	v_exp_f32_e32 v104, v178
	v_exp_f32_e32 v105, v179
	v_exp_f32_e32 v106, v180
	v_exp_f32_e32 v107, v181
	v_exp_f32_e32 v108, v182
	v_exp_f32_e32 v109, v183
	v_exp_f32_e32 v110, v184
	v_exp_f32_e32 v111, v185
	s_nop 0
	v_fma_f32 v194, -v104, v104, 1.0
	v_fma_f32 v195, -v105, v105, 1.0
	v_fma_f32 v196, -v106, v106, 1.0
	v_fma_f32 v197, -v107, v107, 1.0
	v_fma_f32 v198, -v108, v108, 1.0
	v_fma_f32 v199, -v109, v109, 1.0
	v_fma_f32 v200, -v110, v110, 1.0
	v_fma_f32 v201, -v111, v111, 1.0
	v_max_f32_e32 v194, 0, v194
	v_max_f32_e32 v195, 0, v195
	v_max_f32_e32 v196, 0, v196
	v_max_f32_e32 v197, 0, v197
	v_max_f32_e32 v198, 0, v198
	v_max_f32_e32 v199, 0, v199
	v_max_f32_e32 v200, 0, v200
	v_max_f32_e32 v201, 0, v201
	v_sqrt_f32_e32 v194, v194
	v_sqrt_f32_e32 v195, v195
	v_sqrt_f32_e32 v196, v196
	v_sqrt_f32_e32 v197, v197
	v_sqrt_f32_e32 v198, v198
	v_sqrt_f32_e32 v199, v199
	v_sqrt_f32_e32 v200, v200
	v_sqrt_f32_e32 v201, v201
	s_waitcnt lgkmcnt(0)
	v_lshlrev_b32_e32 v152, 16, v152
	v_lshlrev_b32_e32 v153, 16, v153
	v_lshlrev_b32_e32 v154, 16, v154
	v_lshlrev_b32_e32 v155, 16, v155
	v_lshlrev_b32_e32 v156, 16, v156
	v_lshlrev_b32_e32 v157, 16, v157
	v_lshlrev_b32_e32 v158, 16, v158
	v_lshlrev_b32_e32 v159, 16, v159
	v_mul_f32_e32 v194, v194, v186
	v_mul_f32_e32 v195, v195, v187
	v_mul_f32_e32 v196, v196, v188
	v_mul_f32_e32 v197, v197, v189
	v_mul_f32_e32 v198, v198, v190
	v_mul_f32_e32 v199, v199, v191
	v_mul_f32_e32 v200, v200, v192
	v_mul_f32_e32 v201, v201, v193
	v_mul_f32_e32 v152, v194, v152
	v_mul_f32_e32 v153, v195, v153
	v_mul_f32_e32 v154, v196, v154
	v_mul_f32_e32 v155, v197, v155
	v_mul_f32_e32 v156, v198, v156
	v_mul_f32_e32 v157, v199, v157
	v_mul_f32_e32 v158, v200, v158
	v_mul_f32_e32 v159, v201, v159
	v_fma_f32 v146, v98, v147, v146
	v_fma_f32 v150, v102, v151, v150
	v_fma_f32 v154, v106, v155, v154
	v_fma_f32 v158, v110, v159, v158
	v_mul_f32_e32 v98, v98, v99
	v_mul_f32_e32 v102, v102, v103
	v_mul_f32_e32 v106, v106, v107
	v_mul_f32_e32 v110, v110, v111
	v_fma_f32 v145, v97, v146, v145
	v_fma_f32 v149, v101, v150, v149
	v_fma_f32 v153, v105, v154, v153
	v_fma_f32 v157, v109, v158, v157
	v_mul_f32_e32 v97, v97, v98
	v_mul_f32_e32 v101, v101, v102
	v_mul_f32_e32 v105, v105, v106
	v_mul_f32_e32 v109, v109, v110
	v_fma_f32 v144, v96, v145, v144
	v_fma_f32 v148, v100, v149, v148
	v_fma_f32 v152, v104, v153, v152
	v_fma_f32 v156, v108, v157, v156
	v_mul_f32_e32 v96, v96, v97
	v_mul_f32_e32 v100, v100, v101
	v_mul_f32_e32 v104, v104, v105
	v_mul_f32_e32 v108, v108, v109
	ds_bpermute_b32 v178, v204, v96
	ds_bpermute_b32 v182, v204, v144
	ds_bpermute_b32 v179, v204, v100
	ds_bpermute_b32 v183, v204, v148
	ds_bpermute_b32 v180, v204, v104
	ds_bpermute_b32 v184, v204, v152
	ds_bpermute_b32 v181, v204, v108
	ds_bpermute_b32 v185, v204, v156
	s_waitcnt lgkmcnt(0)
	v_fma_f32 v186, v182, v96, v144
	v_cndmask_b32_e64 v178, 1.0, v178, s[34:35]
	v_fma_f32 v187, v183, v100, v148
	v_cndmask_b32_e64 v179, 1.0, v179, s[34:35]
	v_fma_f32 v188, v184, v104, v152
	v_cndmask_b32_e64 v180, 1.0, v180, s[34:35]
	v_fma_f32 v189, v185, v108, v156
	v_cndmask_b32_e64 v181, 1.0, v181, s[34:35]
	v_cndmask_b32_e64 v223, v144, v186, s[34:35]
	v_mul_f32_e32 v219, v96, v178
	v_cndmask_b32_e64 v224, v148, v187, s[34:35]
	v_mul_f32_e32 v220, v100, v179
	v_cndmask_b32_e64 v225, v152, v188, s[34:35]
	v_mul_f32_e32 v221, v104, v180
	v_cndmask_b32_e64 v226, v156, v189, s[34:35]
	v_mul_f32_e32 v222, v108, v181
	ds_bpermute_b32 v178, v205, v219
	ds_bpermute_b32 v182, v205, v223
	ds_bpermute_b32 v179, v205, v220
	ds_bpermute_b32 v183, v205, v224
	ds_bpermute_b32 v180, v205, v221
	ds_bpermute_b32 v184, v205, v225
	ds_bpermute_b32 v181, v205, v222
	ds_bpermute_b32 v185, v205, v226
	s_waitcnt lgkmcnt(0)
	v_fma_f32 v186, v182, v219, v223
	v_cndmask_b32_e64 v178, 1.0, v178, s[36:37]
	v_fma_f32 v187, v183, v220, v224
	v_cndmask_b32_e64 v179, 1.0, v179, s[36:37]
	v_fma_f32 v188, v184, v221, v225
	v_cndmask_b32_e64 v180, 1.0, v180, s[36:37]
	v_fma_f32 v189, v185, v222, v226
	v_cndmask_b32_e64 v181, 1.0, v181, s[36:37]
	v_cndmask_b32_e64 v223, v223, v186, s[36:37]
	v_mul_f32_e32 v219, v219, v178
	v_cndmask_b32_e64 v224, v224, v187, s[36:37]
	v_mul_f32_e32 v220, v220, v179
	v_cndmask_b32_e64 v225, v225, v188, s[36:37]
	v_mul_f32_e32 v221, v221, v180
	v_cndmask_b32_e64 v226, v226, v189, s[36:37]
	v_mul_f32_e32 v222, v222, v181
	ds_bpermute_b32 v227, v204, v219
	ds_bpermute_b32 v231, v204, v223
	ds_bpermute_b32 v235, v206, v219
	ds_bpermute_b32 v239, v206, v223
	ds_bpermute_b32 v228, v204, v220
	ds_bpermute_b32 v232, v204, v224
	ds_bpermute_b32 v236, v206, v220
	ds_bpermute_b32 v244, v206, v224
	ds_bpermute_b32 v229, v204, v221
	ds_bpermute_b32 v233, v204, v225
	ds_bpermute_b32 v237, v206, v221
	ds_bpermute_b32 v245, v206, v225
	ds_bpermute_b32 v230, v204, v222
	ds_bpermute_b32 v234, v204, v226
	ds_bpermute_b32 v238, v206, v222
	ds_bpermute_b32 v246, v206, v226
	s_waitcnt lgkmcnt(0)
	v_cndmask_b32_e64 v227, 1.0, v227, s[34:35]
	v_cndmask_b32_e64 v231, 0, v231, s[34:35]
	v_cndmask_b32_e64 v228, 1.0, v228, s[34:35]
	v_cndmask_b32_e64 v232, 0, v232, s[34:35]
	v_cndmask_b32_e64 v229, 1.0, v229, s[34:35]
	v_cndmask_b32_e64 v233, 0, v233, s[34:35]
	v_cndmask_b32_e64 v230, 1.0, v230, s[34:35]
	v_cndmask_b32_e64 v234, 0, v234, s[34:35]
	v_mov_b32_e32 v190, v238
	v_mov_b32_e32 v194, v246
	v_mov_b32_e32 v198, v190
	v_mov_b32_e32 v201, v194
	v_fma_f32 v194, v194, v237, v245
	v_mul_f32_e32 v190, v190, v237
	v_mov_b32_e32 v199, v190
	v_mov_b32_e32 v177, v194
	v_fma_f32 v194, v194, v236, v244
	v_mul_f32_e32 v190, v190, v236
	v_mov_b32_e32 v200, v190
	v_mov_b32_e32 v203, v194
	v_fma_f32 v194, v194, v235, v239
	v_mul_f32_e32 v190, v190, v235
	v_mov_b32_e32 v191, v194
	ds_write_b64 v207, v[190:191]
	s_cmp_eq_u32 s13, 2
	s_cbranch_scc1 .Lmylru_t0_7
	s_waitcnt vmcnt(40)
	s_branch .Lmylru_t1_7
.Lmylru_t0_7:
	s_waitcnt vmcnt(24)
.Lmylru_t1_7:
	s_waitcnt lgkmcnt(0)
	s_barrier
	s_cmp_gt_u32 s13, 15
	s_cbranch_scc1 .Lmylru_nodma_7
	s_add_i32 s58, s13, 2
	s_cmp_lt_u32 s58, 2
	s_sub_i32 s50, 1, s58
	s_lshl_b32 s50, s50, 7
	s_lshl_b32 s51, s9, 8
	s_add_i32 s51, s51, 0x8000
	s_add_i32 s51, s51, s50
	s_sub_i32 s50, 17, s58
	s_lshl_b32 s50, s50, 7
	s_lshl_b32 s59, s9, 11
	s_add_i32 s59, s59, s50
	s_cmp_lt_u32 s58, 2
	s_cselect_b32 s59, s51, s59
	s_lshl_b32 s52, s59, 11
	s_add_u32 s46, s16, s52
	s_addc_u32 s47, s17, 0
	s_lshl_b32 s52, s6, 13
	s_mov_b32 m0, s52
	s_add_i32 s52, s52, 0x400
	global_load_lds_dwordx4 v211, s[46:47]
	s_mov_b32 m0, s52
	s_add_i32 s52, s52, 0x400
	global_load_lds_dwordx4 v212, s[46:47]
	s_mov_b32 m0, s52
	s_add_i32 s52, s52, 0x400
	global_load_lds_dwordx4 v213, s[46:47]
	s_mov_b32 m0, s52
	s_add_i32 s52, s52, 0x400
	global_load_lds_dwordx4 v214, s[46:47]
	s_mov_b32 m0, s52
	s_add_i32 s52, s52, 0x400
	global_load_lds_dwordx4 v215, s[46:47]
	s_mov_b32 m0, s52
	s_add_i32 s52, s52, 0x400
	global_load_lds_dwordx4 v216, s[46:47]
	s_mov_b32 m0, s52
	s_add_i32 s52, s52, 0x400
	global_load_lds_dwordx4 v217, s[46:47]
	s_mov_b32 m0, s52
	s_nop 0
	global_load_lds_dwordx4 v218, s[46:47]
.Lmylru_nodma_7:
	ds_read_b64 v[178:179], v208 offset:512
	ds_read_b64 v[180:181], v208
	s_waitcnt lgkmcnt(0)
	v_fma_f32 v182, v176, v178, v179
	v_cndmask_b32_e64 v183, v176, v182, s[38:39]
	v_fma_f32 v176, v182, v180, v181
	v_fma_f32 v184, v183, v200, v203
	v_fma_f32 v185, v183, v199, v177
	v_fma_f32 v186, v183, v198, v201
	v_mov_b32_e32 v187, v183
	v_fma_f32 v184, v184, v227, v231
	v_fma_f32 v185, v185, v228, v232
	v_fma_f32 v186, v186, v229, v233
	v_fma_f32 v187, v187, v230, v234
	v_fma_f32 v144, v184, v96, v144
	v_fma_f32 v148, v185, v100, v148
	v_fma_f32 v152, v186, v104, v152
	v_fma_f32 v156, v187, v108, v156
	v_fma_f32 v145, v184, v97, v145
	v_fma_f32 v149, v185, v101, v149
	v_fma_f32 v153, v186, v105, v153
	v_fma_f32 v157, v187, v109, v157
	v_fma_f32 v146, v184, v98, v146
	v_fma_f32 v150, v185, v102, v150
	v_fma_f32 v154, v186, v106, v154
	v_fma_f32 v158, v187, v110, v158
	v_fma_f32 v147, v184, v99, v147
	v_fma_f32 v151, v185, v103, v151
	v_fma_f32 v155, v186, v107, v155
	v_fma_f32 v159, v187, v111, v159
	s_cmp_gt_u32 s13, 15
	s_cbranch_scc1 .Lmylru_w0_7
	s_waitcnt vmcnt(8)
	s_branch .Lmylru_w1_7

.Lmylru_w1_7:
	v_lshlrev_b32_e32 v178, 16, v247
	v_add_f32_e32 v144, v144, v178
	v_lshlrev_b32_e32 v128, 16, v128
	v_mul_f32_e32 v144, v144, v128
	v_cvt_pk_bf16_f32 v144, v144, v144
	v_and_b32_e32 v179, 0xffff0000, v247
	v_add_f32_e32 v145, v145, v179
	v_lshlrev_b32_e32 v129, 16, v129
	v_mul_f32_e32 v145, v145, v129
	v_cvt_pk_bf16_f32 v145, v145, v145
	v_lshlrev_b32_e32 v180, 16, v248
	v_add_f32_e32 v146, v146, v180
	v_lshlrev_b32_e32 v130, 16, v130
	v_mul_f32_e32 v146, v146, v130
	v_cvt_pk_bf16_f32 v146, v146, v146
	v_and_b32_e32 v181, 0xffff0000, v248
	v_add_f32_e32 v147, v147, v181
	v_lshlrev_b32_e32 v131, 16, v131
	v_mul_f32_e32 v147, v147, v131
	v_cvt_pk_bf16_f32 v147, v147, v147
	v_lshlrev_b32_e32 v178, 16, v249
	v_add_f32_e32 v148, v148, v178
	v_lshlrev_b32_e32 v132, 16, v132
	v_mul_f32_e32 v148, v148, v132
	v_cvt_pk_bf16_f32 v148, v148, v148
	v_and_b32_e32 v179, 0xffff0000, v249
	v_add_f32_e32 v149, v149, v179
	v_lshlrev_b32_e32 v133, 16, v133
	v_mul_f32_e32 v149, v149, v133
	v_cvt_pk_bf16_f32 v149, v149, v149
	v_lshlrev_b32_e32 v180, 16, v250
	v_add_f32_e32 v150, v150, v180
	v_lshlrev_b32_e32 v134, 16, v134
	v_mul_f32_e32 v150, v150, v134
	v_cvt_pk_bf16_f32 v150, v150, v150
	v_and_b32_e32 v181, 0xffff0000, v250
	v_add_f32_e32 v151, v151, v181
	v_lshlrev_b32_e32 v135, 16, v135
	v_mul_f32_e32 v151, v151, v135
	v_cvt_pk_bf16_f32 v151, v151, v151
	v_lshlrev_b32_e32 v178, 16, v251
	v_add_f32_e32 v152, v152, v178
	v_lshlrev_b32_e32 v136, 16, v136
	v_mul_f32_e32 v152, v152, v136
	v_cvt_pk_bf16_f32 v152, v152, v152
	v_and_b32_e32 v179, 0xffff0000, v251
	v_add_f32_e32 v153, v153, v179
	v_lshlrev_b32_e32 v137, 16, v137
	v_mul_f32_e32 v153, v153, v137
	v_cvt_pk_bf16_f32 v153, v153, v153
	v_lshlrev_b32_e32 v180, 16, v252
	v_add_f32_e32 v154, v154, v180
	v_lshlrev_b32_e32 v138, 16, v138
	v_mul_f32_e32 v154, v154, v138
	v_cvt_pk_bf16_f32 v154, v154, v154
	v_and_b32_e32 v181, 0xffff0000, v252
	v_add_f32_e32 v155, v155, v181
	v_lshlrev_b32_e32 v139, 16, v139
	v_mul_f32_e32 v155, v155, v139
	v_cvt_pk_bf16_f32 v155, v155, v155
	v_lshlrev_b32_e32 v178, 16, v253
	v_add_f32_e32 v156, v156, v178
	v_lshlrev_b32_e32 v140, 16, v140
	v_mul_f32_e32 v156, v156, v140
	v_cvt_pk_bf16_f32 v156, v156, v156
	v_and_b32_e32 v179, 0xffff0000, v253
	v_add_f32_e32 v157, v157, v179
	v_lshlrev_b32_e32 v141, 16, v141
	v_mul_f32_e32 v157, v157, v141
	v_cvt_pk_bf16_f32 v157, v157, v157
	v_lshlrev_b32_e32 v180, 16, v254
	v_add_f32_e32 v158, v158, v180
	v_lshlrev_b32_e32 v142, 16, v142
	v_mul_f32_e32 v158, v158, v142
	v_cvt_pk_bf16_f32 v158, v158, v158
	v_and_b32_e32 v181, 0xffff0000, v254
	v_add_f32_e32 v159, v159, v181
	v_lshlrev_b32_e32 v143, 16, v143
	v_mul_f32_e32 v159, v159, v143
	v_cvt_pk_bf16_f32 v159, v159, v159
	v_add_u32_e32 v182, 0x0, v210
	v_add_u32_e32 v183, 0x1000, v182
	global_store_short v182, v144, s[42:43]
	global_store_short v182, v145, s[42:43] offset:2048
	global_store_short v183, v146, s[42:43]
	global_store_short v183, v147, s[42:43] offset:2048
	v_add_u32_e32 v182, 0x8000, v210
	v_add_u32_e32 v183, 0x1000, v182
	global_store_short v182, v148, s[42:43]
	global_store_short v182, v149, s[42:43] offset:2048
	global_store_short v183, v150, s[42:43]
	global_store_short v183, v151, s[42:43] offset:2048
	v_add_u32_e32 v182, 0x10000, v210
	v_add_u32_e32 v183, 0x1000, v182
	global_store_short v182, v152, s[42:43]
	global_store_short v182, v153, s[42:43] offset:2048
	global_store_short v183, v154, s[42:43]
	global_store_short v183, v155, s[42:43] offset:2048
	v_add_u32_e32 v182, 0x18000, v210
	v_add_u32_e32 v183, 0x1000, v182
	global_store_short v182, v156, s[42:43]
	global_store_short v182, v157, s[42:43] offset:2048
	global_store_short v183, v158, s[42:43]
	global_store_short v183, v159, s[42:43] offset:2048
	s_add_i32 s13, s13, 1
	s_sub_i32 s54, 17, s13
	s_lshl_b32 s55, s54, 14
	s_lshl_b32 s56, s6, 11
	s_add_i32 s55, s55, s56
	s_add_u32 s44, s22, s55
	s_addc_u32 s45, s23, 0
	s_cmp_lt_u32 s13, 2
	s_sub_i32 s50, 1, s13
	s_lshl_b32 s50, s50, 7
	s_lshl_b32 s51, s9, 8
	s_add_i32 s51, s51, 0x8000
	s_add_i32 s51, s51, s50
	s_sub_i32 s50, 17, s13
	s_lshl_b32 s50, s50, 7
	s_lshl_b32 s57, s9, 11
	s_add_i32 s57, s57, s50
	s_cmp_lt_u32 s13, 2
	s_cselect_b32 s57, s51, s57
	s_lshl_b32 s57, s57, 11
	s_add_u32 s40, s18, s57
	s_addc_u32 s41, s19, 0
	s_add_u32 s42, s20, s57
	s_addc_u32 s43, s21, 0
	global_load_dword v247, v209, s[44:45]
	global_load_dword v248, v209, s[44:45] offset:256
	global_load_dword v249, v209, s[44:45] offset:512
	global_load_dword v250, v209, s[44:45] offset:768
	global_load_dword v251, v209, s[44:45] offset:1024
	global_load_dword v252, v209, s[44:45] offset:1280
	global_load_dword v253, v209, s[44:45] offset:1536
	global_load_dword v254, v209, s[44:45] offset:1792
	v_add_u32_e32 v182, 0x0, v210
	v_add_u32_e32 v183, 0x1000, v182
	global_load_ushort v128, v182, s[40:41]
	global_load_ushort v129, v182, s[40:41] offset:2048
	global_load_ushort v130, v183, s[40:41]
	global_load_ushort v131, v183, s[40:41] offset:2048
	v_add_u32_e32 v182, 0x8000, v210
	v_add_u32_e32 v183, 0x1000, v182
	global_load_ushort v132, v182, s[40:41]
	global_load_ushort v133, v182, s[40:41] offset:2048
	global_load_ushort v134, v183, s[40:41]
	global_load_ushort v135, v183, s[40:41] offset:2048
	v_add_u32_e32 v182, 0x10000, v210
	v_add_u32_e32 v183, 0x1000, v182
	global_load_ushort v136, v182, s[40:41]
	global_load_ushort v137, v182, s[40:41] offset:2048
	global_load_ushort v138, v183, s[40:41]
	global_load_ushort v139, v183, s[40:41] offset:2048
	v_add_u32_e32 v182, 0x18000, v210
	v_add_u32_e32 v183, 0x1000, v182
	global_load_ushort v140, v182, s[40:41]
	global_load_ushort v141, v182, s[40:41] offset:2048
	global_load_ushort v142, v183, s[40:41]
	global_load_ushort v143, v183, s[40:41] offset:2048
	v_or_b32_e32 v163, 0x10000, v162
	ds_read_b128 v[96:99], v163
	ds_read_b128 v[100:103], v163 offset:8192
	ds_read_b128 v[104:107], v163 offset:16384
	ds_read_b128 v[108:111], v163 offset:24576
	v_xor_b32_e32 v164, 0x40, v163
	ds_read_b128 v[112:115], v164
	ds_read_b128 v[116:119], v164 offset:8192
	ds_read_b128 v[120:123], v164 offset:16384
	ds_read_b128 v[124:127], v164 offset:24576
	s_waitcnt lgkmcnt(7)
	v_mfma_f32_16x16x32_bf16 v[64:67], v[96:99], v[0:3], 0
	v_mfma_f32_16x16x32_bf16 v[68:71], v[96:99], v[32:35], 0
	v_xor_b32_e32 v164, 0x80, v163
	ds_read_b128 v[96:99], v164
	s_waitcnt lgkmcnt(7)
	v_mfma_f32_16x16x32_bf16 v[72:75], v[100:103], v[0:3], 0
	v_mfma_f32_16x16x32_bf16 v[76:79], v[100:103], v[32:35], 0
	ds_read_b128 v[100:103], v164 offset:8192
	s_waitcnt lgkmcnt(7)
	v_mfma_f32_16x16x32_bf16 v[80:83], v[104:107], v[0:3], 0
	v_mfma_f32_16x16x32_bf16 v[84:87], v[104:107], v[32:35], 0
	ds_read_b128 v[104:107], v164 offset:16384
	s_waitcnt lgkmcnt(7)
	v_mfma_f32_16x16x32_bf16 v[88:91], v[108:111], v[0:3], 0
	v_mfma_f32_16x16x32_bf16 v[92:95], v[108:111], v[32:35], 0
	ds_read_b128 v[108:111], v164 offset:24576
	s_waitcnt lgkmcnt(7)
	v_mfma_f32_16x16x32_bf16 v[64:67], v[112:115], v[4:7], v[64:67]
	v_mfma_f32_16x16x32_bf16 v[68:71], v[112:115], v[36:39], v[68:71]
	v_xor_b32_e32 v164, 0xc0, v163
	ds_read_b128 v[112:115], v164
	s_waitcnt lgkmcnt(7)
	v_mfma_f32_16x16x32_bf16 v[72:75], v[116:119], v[4:7], v[72:75]
	v_mfma_f32_16x16x32_bf16 v[76:79], v[116:119], v[36:39], v[76:79]
	ds_read_b128 v[116:119], v164 offset:8192
	s_waitcnt lgkmcnt(7)
	v_mfma_f32_16x16x32_bf16 v[80:83], v[120:123], v[4:7], v[80:83]
	v_mfma_f32_16x16x32_bf16 v[84:87], v[120:123], v[36:39], v[84:87]
	ds_read_b128 v[120:123], v164 offset:16384
	s_waitcnt lgkmcnt(7)
	v_mfma_f32_16x16x32_bf16 v[88:91], v[124:127], v[4:7], v[88:91]
	v_mfma_f32_16x16x32_bf16 v[92:95], v[124:127], v[36:39], v[92:95]
	ds_read_b128 v[124:127], v164 offset:24576
	s_waitcnt lgkmcnt(7)
	v_mfma_f32_16x16x32_bf16 v[64:67], v[96:99], v[8:11], v[64:67]
	v_mfma_f32_16x16x32_bf16 v[68:71], v[96:99], v[40:43], v[68:71]
	v_xor_b32_e32 v164, 0x100, v163
	ds_read_b128 v[96:99], v164
	s_waitcnt lgkmcnt(7)
	v_mfma_f32_16x16x32_bf16 v[72:75], v[100:103], v[8:11], v[72:75]
	v_mfma_f32_16x16x32_bf16 v[76:79], v[100:103], v[40:43], v[76:79]
	ds_read_b128 v[100:103], v164 offset:8192
	s_waitcnt lgkmcnt(7)
	v_mfma_f32_16x16x32_bf16 v[80:83], v[104:107], v[8:11], v[80:83]
	v_mfma_f32_16x16x32_bf16 v[84:87], v[104:107], v[40:43], v[84:87]
	ds_read_b128 v[104:107], v164 offset:16384
	s_waitcnt lgkmcnt(7)
	v_mfma_f32_16x16x32_bf16 v[88:91], v[108:111], v[8:11], v[88:91]
	v_mfma_f32_16x16x32_bf16 v[92:95], v[108:111], v[40:43], v[92:95]
	ds_read_b128 v[108:111], v164 offset:24576
	s_waitcnt lgkmcnt(7)
	v_mfma_f32_16x16x32_bf16 v[64:67], v[112:115], v[12:15], v[64:67]
	v_mfma_f32_16x16x32_bf16 v[68:71], v[112:115], v[44:47], v[68:71]
	v_xor_b32_e32 v164, 0x140, v163
	ds_read_b128 v[112:115], v164
	s_waitcnt lgkmcnt(7)
	v_mfma_f32_16x16x32_bf16 v[72:75], v[116:119], v[12:15], v[72:75]
	v_mfma_f32_16x16x32_bf16 v[76:79], v[116:119], v[44:47], v[76:79]
	ds_read_b128 v[116:119], v164 offset:8192
	s_waitcnt lgkmcnt(7)
	v_mfma_f32_16x16x32_bf16 v[80:83], v[120:123], v[12:15], v[80:83]
	v_mfma_f32_16x16x32_bf16 v[84:87], v[120:123], v[44:47], v[84:87]
	ds_read_b128 v[120:123], v164 offset:16384
	s_waitcnt lgkmcnt(7)
	v_mfma_f32_16x16x32_bf16 v[88:91], v[124:127], v[12:15], v[88:91]
	v_mfma_f32_16x16x32_bf16 v[92:95], v[124:127], v[44:47], v[92:95]
	ds_read_b128 v[124:127], v164 offset:24576
	s_waitcnt lgkmcnt(7)
	v_mfma_f32_16x16x32_bf16 v[64:67], v[96:99], v[16:19], v[64:67]
	v_mfma_f32_16x16x32_bf16 v[68:71], v[96:99], v[48:51], v[68:71]
	v_xor_b32_e32 v164, 0x180, v163
	ds_read_b128 v[96:99], v164
	s_waitcnt lgkmcnt(7)
	v_mfma_f32_16x16x32_bf16 v[72:75], v[100:103], v[16:19], v[72:75]
	v_mfma_f32_16x16x32_bf16 v[76:79], v[100:103], v[48:51], v[76:79]
	ds_read_b128 v[100:103], v164 offset:8192
	s_waitcnt lgkmcnt(7)
	v_mfma_f32_16x16x32_bf16 v[80:83], v[104:107], v[16:19], v[80:83]
	v_mfma_f32_16x16x32_bf16 v[84:87], v[104:107], v[48:51], v[84:87]
	ds_read_b128 v[104:107], v164 offset:16384
	s_waitcnt lgkmcnt(7)
	v_mfma_f32_16x16x32_bf16 v[88:91], v[108:111], v[16:19], v[88:91]
	v_mfma_f32_16x16x32_bf16 v[92:95], v[108:111], v[48:51], v[92:95]
	ds_read_b128 v[108:111], v164 offset:24576
	s_waitcnt lgkmcnt(7)
	v_mfma_f32_16x16x32_bf16 v[64:67], v[112:115], v[20:23], v[64:67]
	v_mfma_f32_16x16x32_bf16 v[68:71], v[112:115], v[52:55], v[68:71]
	v_xor_b32_e32 v164, 0x1c0, v163
	ds_read_b128 v[112:115], v164
	s_waitcnt lgkmcnt(7)
	v_mfma_f32_16x16x32_bf16 v[72:75], v[116:119], v[20:23], v[72:75]
	v_mfma_f32_16x16x32_bf16 v[76:79], v[116:119], v[52:55], v[76:79]
	ds_read_b128 v[116:119], v164 offset:8192
	s_waitcnt lgkmcnt(7)
	v_mfma_f32_16x16x32_bf16 v[80:83], v[120:123], v[20:23], v[80:83]
	v_mfma_f32_16x16x32_bf16 v[84:87], v[120:123], v[52:55], v[84:87]
	ds_read_b128 v[120:123], v164 offset:16384
	s_waitcnt lgkmcnt(7)
	v_mfma_f32_16x16x32_bf16 v[88:91], v[124:127], v[20:23], v[88:91]
	v_mfma_f32_16x16x32_bf16 v[92:95], v[124:127], v[52:55], v[92:95]
	ds_read_b128 v[124:127], v164 offset:24576
	s_waitcnt lgkmcnt(7)
	v_mfma_f32_16x16x32_bf16 v[64:67], v[96:99], v[24:27], v[64:67]
	v_mfma_f32_16x16x32_bf16 v[68:71], v[96:99], v[56:59], v[68:71]
	s_waitcnt lgkmcnt(6)
	v_mfma_f32_16x16x32_bf16 v[72:75], v[100:103], v[24:27], v[72:75]
	v_mfma_f32_16x16x32_bf16 v[76:79], v[100:103], v[56:59], v[76:79]
	s_waitcnt lgkmcnt(5)
	v_mfma_f32_16x16x32_bf16 v[80:83], v[104:107], v[24:27], v[80:83]
	v_mfma_f32_16x16x32_bf16 v[84:87], v[104:107], v[56:59], v[84:87]
	s_waitcnt lgkmcnt(4)
	v_mfma_f32_16x16x32_bf16 v[88:91], v[108:111], v[24:27], v[88:91]
	v_mfma_f32_16x16x32_bf16 v[92:95], v[108:111], v[56:59], v[92:95]
	s_waitcnt lgkmcnt(3)
	v_mfma_f32_16x16x32_bf16 v[64:67], v[112:115], v[28:31], v[64:67]
	v_mfma_f32_16x16x32_bf16 v[68:71], v[112:115], v[60:63], v[68:71]
	s_waitcnt lgkmcnt(2)
	v_mfma_f32_16x16x32_bf16 v[72:75], v[116:119], v[28:31], v[72:75]
	v_mfma_f32_16x16x32_bf16 v[76:79], v[116:119], v[60:63], v[76:79]
	s_waitcnt lgkmcnt(1)
	v_mfma_f32_16x16x32_bf16 v[80:83], v[120:123], v[28:31], v[80:83]
	v_mfma_f32_16x16x32_bf16 v[84:87], v[120:123], v[60:63], v[84:87]
	s_waitcnt lgkmcnt(0)
	v_mfma_f32_16x16x32_bf16 v[88:91], v[124:127], v[28:31], v[88:91]
	v_mfma_f32_16x16x32_bf16 v[92:95], v[124:127], v[60:63], v[92:95]
	v_or_b32_e32 v169, 0x10000, v165
	v_or_b32_e32 v170, 0x10000, v166
	v_or_b32_e32 v171, 0x10000, v167
	v_or_b32_e32 v172, 0x10000, v168
	ds_read_u16 v144, v169
	ds_read_u16 v145, v170
	ds_read_u16 v146, v171
	ds_read_u16 v147, v172
	ds_read_u16 v148, v169 offset:8192
	ds_read_u16 v149, v170 offset:8192
	ds_read_u16 v150, v171 offset:8192
	ds_read_u16 v151, v172 offset:8192
	ds_read_u16 v152, v169 offset:16384
	ds_read_u16 v153, v170 offset:16384
	ds_read_u16 v154, v171 offset:16384
	ds_read_u16 v155, v172 offset:16384
	ds_read_u16 v156, v169 offset:24576
	ds_read_u16 v157, v170 offset:24576
	ds_read_u16 v158, v171 offset:24576
	ds_read_u16 v159, v172 offset:24576
	s_nop 7
	v_fma_f32 v178, v64, s53, v173
	v_fma_f32 v179, v65, s53, v173
	v_fma_f32 v180, v66, s53, v173
	v_fma_f32 v181, v67, s53, v173
	v_fma_f32 v182, v72, s53, v173
	v_fma_f32 v183, v73, s53, v173
	v_fma_f32 v184, v74, s53, v173
	v_fma_f32 v185, v75, s53, v173
	v_fma_f32 v186, v68, s53, v174
	v_fma_f32 v187, v69, s53, v174
	v_fma_f32 v188, v70, s53, v174
	v_fma_f32 v189, v71, s53, v174
	v_fma_f32 v190, v76, s53, v174
	v_fma_f32 v191, v77, s53, v174
	v_fma_f32 v192, v78, s53, v174
	v_fma_f32 v193, v79, s53, v174
	v_exp_f32_e32 v178, v178
	v_exp_f32_e32 v179, v179
	v_exp_f32_e32 v180, v180
	v_exp_f32_e32 v181, v181
	v_exp_f32_e32 v182, v182
	v_exp_f32_e32 v183, v183
	v_exp_f32_e32 v184, v184
	v_exp_f32_e32 v185, v185
	v_exp_f32_e32 v186, v186
	v_exp_f32_e32 v187, v187
	v_exp_f32_e32 v188, v188
	v_exp_f32_e32 v189, v189
	v_exp_f32_e32 v190, v190
	v_exp_f32_e32 v191, v191
	v_exp_f32_e32 v192, v192
	v_exp_f32_e32 v193, v193
	v_add_f32_e32 v178, 1.0, v178
	v_add_f32_e32 v179, 1.0, v179
	v_add_f32_e32 v180, 1.0, v180
	v_add_f32_e32 v181, 1.0, v181
	v_add_f32_e32 v182, 1.0, v182
	v_add_f32_e32 v183, 1.0, v183
	v_add_f32_e32 v184, 1.0, v184
	v_add_f32_e32 v185, 1.0, v185
	v_add_f32_e32 v186, 1.0, v186
	v_add_f32_e32 v187, 1.0, v187
	v_add_f32_e32 v188, 1.0, v188
	v_add_f32_e32 v189, 1.0, v189
	v_add_f32_e32 v190, 1.0, v190
	v_add_f32_e32 v191, 1.0, v191
	v_add_f32_e32 v192, 1.0, v192
	v_add_f32_e32 v193, 1.0, v193
	v_rcp_f32_e32 v178, v178
	v_rcp_f32_e32 v179, v179
	v_rcp_f32_e32 v180, v180
	v_rcp_f32_e32 v181, v181
	v_rcp_f32_e32 v182, v182
	v_rcp_f32_e32 v183, v183
	v_rcp_f32_e32 v184, v184
	v_rcp_f32_e32 v185, v185
	v_rcp_f32_e32 v186, v186
	v_rcp_f32_e32 v187, v187
	v_rcp_f32_e32 v188, v188
	v_rcp_f32_e32 v189, v189
	v_rcp_f32_e32 v190, v190
	v_rcp_f32_e32 v191, v191
	v_rcp_f32_e32 v192, v192
	v_rcp_f32_e32 v193, v193
	v_mul_f32_e32 v178, v175, v178
	v_mul_f32_e32 v179, v175, v179
	v_mul_f32_e32 v180, v175, v180
	v_mul_f32_e32 v181, v175, v181
	v_mul_f32_e32 v182, v175, v182
	v_mul_f32_e32 v183, v175, v183
	v_mul_f32_e32 v184, v175, v184
	v_mul_f32_e32 v185, v175, v185
	v_exp_f32_e32 v96, v178
	v_exp_f32_e32 v97, v179
	v_exp_f32_e32 v98, v180
	v_exp_f32_e32 v99, v181
	v_exp_f32_e32 v100, v182
	v_exp_f32_e32 v101, v183
	v_exp_f32_e32 v102, v184
	v_exp_f32_e32 v103, v185
	s_nop 0
	v_fma_f32 v194, -v96, v96, 1.0
	v_fma_f32 v195, -v97, v97, 1.0
	v_fma_f32 v196, -v98, v98, 1.0
	v_fma_f32 v197, -v99, v99, 1.0
	v_fma_f32 v198, -v100, v100, 1.0
	v_fma_f32 v199, -v101, v101, 1.0
	v_fma_f32 v200, -v102, v102, 1.0
	v_fma_f32 v201, -v103, v103, 1.0
	v_max_f32_e32 v194, 0, v194
	v_max_f32_e32 v195, 0, v195
	v_max_f32_e32 v196, 0, v196
	v_max_f32_e32 v197, 0, v197
	v_max_f32_e32 v198, 0, v198
	v_max_f32_e32 v199, 0, v199
	v_max_f32_e32 v200, 0, v200
	v_max_f32_e32 v201, 0, v201
	v_sqrt_f32_e32 v194, v194
	v_sqrt_f32_e32 v195, v195
	v_sqrt_f32_e32 v196, v196
	v_sqrt_f32_e32 v197, v197
	v_sqrt_f32_e32 v198, v198
	v_sqrt_f32_e32 v199, v199
	v_sqrt_f32_e32 v200, v200
	v_sqrt_f32_e32 v201, v201
	s_waitcnt lgkmcnt(8)
	v_lshlrev_b32_e32 v144, 16, v144
	v_lshlrev_b32_e32 v145, 16, v145
	v_lshlrev_b32_e32 v146, 16, v146
	v_lshlrev_b32_e32 v147, 16, v147
	v_lshlrev_b32_e32 v148, 16, v148
	v_lshlrev_b32_e32 v149, 16, v149
	v_lshlrev_b32_e32 v150, 16, v150
	v_lshlrev_b32_e32 v151, 16, v151
	v_mul_f32_e32 v194, v194, v186
	v_mul_f32_e32 v195, v195, v187
	v_mul_f32_e32 v196, v196, v188
	v_mul_f32_e32 v197, v197, v189
	v_mul_f32_e32 v198, v198, v190
	v_mul_f32_e32 v199, v199, v191
	v_mul_f32_e32 v200, v200, v192
	v_mul_f32_e32 v201, v201, v193
	v_mul_f32_e32 v144, v194, v144
	v_mul_f32_e32 v145, v195, v145
	v_mul_f32_e32 v146, v196, v146
	v_mul_f32_e32 v147, v197, v147
	v_mul_f32_e32 v148, v198, v148
	v_mul_f32_e32 v149, v199, v149
	v_mul_f32_e32 v150, v200, v150
	v_mul_f32_e32 v151, v201, v151
	v_fma_f32 v178, v80, s53, v173
	v_fma_f32 v179, v81, s53, v173
	v_fma_f32 v180, v82, s53, v173
	v_fma_f32 v181, v83, s53, v173
	v_fma_f32 v182, v88, s53, v173
	v_fma_f32 v183, v89, s53, v173
	v_fma_f32 v184, v90, s53, v173
	v_fma_f32 v185, v91, s53, v173
	v_fma_f32 v186, v84, s53, v174
	v_fma_f32 v187, v85, s53, v174
	v_fma_f32 v188, v86, s53, v174
	v_fma_f32 v189, v87, s53, v174
	v_fma_f32 v190, v92, s53, v174
	v_fma_f32 v191, v93, s53, v174
	v_fma_f32 v192, v94, s53, v174
	v_fma_f32 v193, v95, s53, v174
	v_exp_f32_e32 v178, v178
	v_exp_f32_e32 v179, v179
	v_exp_f32_e32 v180, v180
	v_exp_f32_e32 v181, v181
	v_exp_f32_e32 v182, v182
	v_exp_f32_e32 v183, v183
	v_exp_f32_e32 v184, v184
	v_exp_f32_e32 v185, v185
	v_exp_f32_e32 v186, v186
	v_exp_f32_e32 v187, v187
	v_exp_f32_e32 v188, v188
	v_exp_f32_e32 v189, v189
	v_exp_f32_e32 v190, v190
	v_exp_f32_e32 v191, v191
	v_exp_f32_e32 v192, v192
	v_exp_f32_e32 v193, v193
	v_add_f32_e32 v178, 1.0, v178
	v_add_f32_e32 v179, 1.0, v179
	v_add_f32_e32 v180, 1.0, v180
	v_add_f32_e32 v181, 1.0, v181
	v_add_f32_e32 v182, 1.0, v182
	v_add_f32_e32 v183, 1.0, v183
	v_add_f32_e32 v184, 1.0, v184
	v_add_f32_e32 v185, 1.0, v185
	v_add_f32_e32 v186, 1.0, v186
	v_add_f32_e32 v187, 1.0, v187
	v_add_f32_e32 v188, 1.0, v188
	v_add_f32_e32 v189, 1.0, v189
	v_add_f32_e32 v190, 1.0, v190
	v_add_f32_e32 v191, 1.0, v191
	v_add_f32_e32 v192, 1.0, v192
	v_add_f32_e32 v193, 1.0, v193
	v_rcp_f32_e32 v178, v178
	v_rcp_f32_e32 v179, v179
	v_rcp_f32_e32 v180, v180
	v_rcp_f32_e32 v181, v181
	v_rcp_f32_e32 v182, v182
	v_rcp_f32_e32 v183, v183
	v_rcp_f32_e32 v184, v184
	v_rcp_f32_e32 v185, v185
	v_rcp_f32_e32 v186, v186
	v_rcp_f32_e32 v187, v187
	v_rcp_f32_e32 v188, v188
	v_rcp_f32_e32 v189, v189
	v_rcp_f32_e32 v190, v190
	v_rcp_f32_e32 v191, v191
	v_rcp_f32_e32 v192, v192
	v_rcp_f32_e32 v193, v193
	v_mul_f32_e32 v178, v175, v178
	v_mul_f32_e32 v179, v175, v179
	v_mul_f32_e32 v180, v175, v180
	v_mul_f32_e32 v181, v175, v181
	v_mul_f32_e32 v182, v175, v182
	v_mul_f32_e32 v183, v175, v183
	v_mul_f32_e32 v184, v175, v184
	v_mul_f32_e32 v185, v175, v185
	v_exp_f32_e32 v104, v178
	v_exp_f32_e32 v105, v179
	v_exp_f32_e32 v106, v180
	v_exp_f32_e32 v107, v181
	v_exp_f32_e32 v108, v182
	v_exp_f32_e32 v109, v183
	v_exp_f32_e32 v110, v184
	v_exp_f32_e32 v111, v185
	s_nop 0
	v_fma_f32 v194, -v104, v104, 1.0
	v_fma_f32 v195, -v105, v105, 1.0
	v_fma_f32 v196, -v106, v106, 1.0
	v_fma_f32 v197, -v107, v107, 1.0
	v_fma_f32 v198, -v108, v108, 1.0
	v_fma_f32 v199, -v109, v109, 1.0
	v_fma_f32 v200, -v110, v110, 1.0
	v_fma_f32 v201, -v111, v111, 1.0
	v_max_f32_e32 v194, 0, v194
	v_max_f32_e32 v195, 0, v195
	v_max_f32_e32 v196, 0, v196
	v_max_f32_e32 v197, 0, v197
	v_max_f32_e32 v198, 0, v198
	v_max_f32_e32 v199, 0, v199
	v_max_f32_e32 v200, 0, v200
	v_max_f32_e32 v201, 0, v201
	v_sqrt_f32_e32 v194, v194
	v_sqrt_f32_e32 v195, v195
	v_sqrt_f32_e32 v196, v196
	v_sqrt_f32_e32 v197, v197
	v_sqrt_f32_e32 v198, v198
	v_sqrt_f32_e32 v199, v199
	v_sqrt_f32_e32 v200, v200
	v_sqrt_f32_e32 v201, v201
	s_waitcnt lgkmcnt(0)
	v_lshlrev_b32_e32 v152, 16, v152
	v_lshlrev_b32_e32 v153, 16, v153
	v_lshlrev_b32_e32 v154, 16, v154
	v_lshlrev_b32_e32 v155, 16, v155
	v_lshlrev_b32_e32 v156, 16, v156
	v_lshlrev_b32_e32 v157, 16, v157
	v_lshlrev_b32_e32 v158, 16, v158
	v_lshlrev_b32_e32 v159, 16, v159
	v_mul_f32_e32 v194, v194, v186
	v_mul_f32_e32 v195, v195, v187
	v_mul_f32_e32 v196, v196, v188
	v_mul_f32_e32 v197, v197, v189
	v_mul_f32_e32 v198, v198, v190
	v_mul_f32_e32 v199, v199, v191
	v_mul_f32_e32 v200, v200, v192
	v_mul_f32_e32 v201, v201, v193
	v_mul_f32_e32 v152, v194, v152
	v_mul_f32_e32 v153, v195, v153
	v_mul_f32_e32 v154, v196, v154
	v_mul_f32_e32 v155, v197, v155
	v_mul_f32_e32 v156, v198, v156
	v_mul_f32_e32 v157, v199, v157
	v_mul_f32_e32 v158, v200, v158
	v_mul_f32_e32 v159, v201, v159
	v_fma_f32 v146, v98, v147, v146
	v_fma_f32 v150, v102, v151, v150
	v_fma_f32 v154, v106, v155, v154
	v_fma_f32 v158, v110, v159, v158
	v_mul_f32_e32 v98, v98, v99
	v_mul_f32_e32 v102, v102, v103
	v_mul_f32_e32 v106, v106, v107
	v_mul_f32_e32 v110, v110, v111
	v_fma_f32 v145, v97, v146, v145
	v_fma_f32 v149, v101, v150, v149
	v_fma_f32 v153, v105, v154, v153
	v_fma_f32 v157, v109, v158, v157
	v_mul_f32_e32 v97, v97, v98
	v_mul_f32_e32 v101, v101, v102
	v_mul_f32_e32 v105, v105, v106
	v_mul_f32_e32 v109, v109, v110
	v_fma_f32 v144, v96, v145, v144
	v_fma_f32 v148, v100, v149, v148
	v_fma_f32 v152, v104, v153, v152
	v_fma_f32 v156, v108, v157, v156
	v_mul_f32_e32 v96, v96, v97
	v_mul_f32_e32 v100, v100, v101
	v_mul_f32_e32 v104, v104, v105
	v_mul_f32_e32 v108, v108, v109
	ds_bpermute_b32 v178, v204, v96
	ds_bpermute_b32 v182, v204, v144
	ds_bpermute_b32 v179, v204, v100
	ds_bpermute_b32 v183, v204, v148
	ds_bpermute_b32 v180, v204, v104
	ds_bpermute_b32 v184, v204, v152
	ds_bpermute_b32 v181, v204, v108
	ds_bpermute_b32 v185, v204, v156
	s_waitcnt lgkmcnt(0)
	v_fma_f32 v186, v182, v96, v144
	v_cndmask_b32_e64 v178, 1.0, v178, s[34:35]
	v_fma_f32 v187, v183, v100, v148
	v_cndmask_b32_e64 v179, 1.0, v179, s[34:35]
	v_fma_f32 v188, v184, v104, v152
	v_cndmask_b32_e64 v180, 1.0, v180, s[34:35]
	v_fma_f32 v189, v185, v108, v156
	v_cndmask_b32_e64 v181, 1.0, v181, s[34:35]
	v_cndmask_b32_e64 v223, v144, v186, s[34:35]
	v_mul_f32_e32 v219, v96, v178
	v_cndmask_b32_e64 v224, v148, v187, s[34:35]
	v_mul_f32_e32 v220, v100, v179
	v_cndmask_b32_e64 v225, v152, v188, s[34:35]
	v_mul_f32_e32 v221, v104, v180
	v_cndmask_b32_e64 v226, v156, v189, s[34:35]
	v_mul_f32_e32 v222, v108, v181
	ds_bpermute_b32 v178, v205, v219
	ds_bpermute_b32 v182, v205, v223
	ds_bpermute_b32 v179, v205, v220
	ds_bpermute_b32 v183, v205, v224
	ds_bpermute_b32 v180, v205, v221
	ds_bpermute_b32 v184, v205, v225
	ds_bpermute_b32 v181, v205, v222
	ds_bpermute_b32 v185, v205, v226
	s_waitcnt lgkmcnt(0)
	v_fma_f32 v186, v182, v219, v223
	v_cndmask_b32_e64 v178, 1.0, v178, s[36:37]
	v_fma_f32 v187, v183, v220, v224
	v_cndmask_b32_e64 v179, 1.0, v179, s[36:37]
	v_fma_f32 v188, v184, v221, v225
	v_cndmask_b32_e64 v180, 1.0, v180, s[36:37]
	v_fma_f32 v189, v185, v222, v226
	v_cndmask_b32_e64 v181, 1.0, v181, s[36:37]
	v_cndmask_b32_e64 v223, v223, v186, s[36:37]
	v_mul_f32_e32 v219, v219, v178
	v_cndmask_b32_e64 v224, v224, v187, s[36:37]
	v_mul_f32_e32 v220, v220, v179
	v_cndmask_b32_e64 v225, v225, v188, s[36:37]
	v_mul_f32_e32 v221, v221, v180
	v_cndmask_b32_e64 v226, v226, v189, s[36:37]
	v_mul_f32_e32 v222, v222, v181
	ds_bpermute_b32 v227, v204, v219
	ds_bpermute_b32 v231, v204, v223
	ds_bpermute_b32 v235, v206, v219
	ds_bpermute_b32 v239, v206, v223
	ds_bpermute_b32 v228, v204, v220
	ds_bpermute_b32 v232, v204, v224
	ds_bpermute_b32 v236, v206, v220
	ds_bpermute_b32 v244, v206, v224
	ds_bpermute_b32 v229, v204, v221
	ds_bpermute_b32 v233, v204, v225
	ds_bpermute_b32 v237, v206, v221
	ds_bpermute_b32 v245, v206, v225
	ds_bpermute_b32 v230, v204, v222
	ds_bpermute_b32 v234, v204, v226
	ds_bpermute_b32 v238, v206, v222
	ds_bpermute_b32 v246, v206, v226
	s_waitcnt lgkmcnt(0)
	v_cndmask_b32_e64 v227, 1.0, v227, s[34:35]
	v_cndmask_b32_e64 v231, 0, v231, s[34:35]
	v_cndmask_b32_e64 v228, 1.0, v228, s[34:35]
	v_cndmask_b32_e64 v232, 0, v232, s[34:35]
	v_cndmask_b32_e64 v229, 1.0, v229, s[34:35]
	v_cndmask_b32_e64 v233, 0, v233, s[34:35]
	v_cndmask_b32_e64 v230, 1.0, v230, s[34:35]
	v_cndmask_b32_e64 v234, 0, v234, s[34:35]
	v_mov_b32_e32 v190, v238
	v_mov_b32_e32 v194, v246
	v_mov_b32_e32 v198, v190
	v_mov_b32_e32 v201, v194
	v_fma_f32 v194, v194, v237, v245
	v_mul_f32_e32 v190, v190, v237
	v_mov_b32_e32 v199, v190
	v_mov_b32_e32 v177, v194
	v_fma_f32 v194, v194, v236, v244
	v_mul_f32_e32 v190, v190, v236
	v_mov_b32_e32 v200, v190
	v_mov_b32_e32 v203, v194
	v_fma_f32 v194, v194, v235, v239
	v_mul_f32_e32 v190, v190, v235
	v_mov_b32_e32 v191, v194
	ds_write_b64 v207, v[190:191] offset:1024
	s_cmp_eq_u32 s13, 2
	s_cbranch_scc1 .Lmylru_t0_8
	s_waitcnt vmcnt(40)
	s_branch .Lmylru_t1_8

.Lmylru_t1_8:
	s_waitcnt lgkmcnt(0)
	s_barrier
	s_cmp_gt_u32 s13, 15
	s_cbranch_scc1 .Lmylru_nodma_8
	s_add_i32 s58, s13, 2
	s_cmp_lt_u32 s58, 2
	s_sub_i32 s50, 1, s58
	s_lshl_b32 s50, s50, 7
	s_lshl_b32 s51, s9, 8
	s_add_i32 s51, s51, 0x8000
	s_add_i32 s51, s51, s50
	s_sub_i32 s50, 17, s58
	s_lshl_b32 s50, s50, 7
	s_lshl_b32 s59, s9, 11
	s_add_i32 s59, s59, s50
	s_cmp_lt_u32 s58, 2
	s_cselect_b32 s59, s51, s59
	s_lshl_b32 s52, s59, 11
	s_add_u32 s46, s16, s52
	s_addc_u32 s47, s17, 0
	s_lshl_b32 s52, s6, 13
	s_add_i32 s52, s52, 0x10000
	s_mov_b32 m0, s52
	s_add_i32 s52, s52, 0x400
	global_load_lds_dwordx4 v211, s[46:47]
	s_mov_b32 m0, s52
	s_add_i32 s52, s52, 0x400
	global_load_lds_dwordx4 v212, s[46:47]
	s_mov_b32 m0, s52
	s_add_i32 s52, s52, 0x400
	global_load_lds_dwordx4 v213, s[46:47]
	s_mov_b32 m0, s52
	s_add_i32 s52, s52, 0x400
	global_load_lds_dwordx4 v214, s[46:47]
	s_mov_b32 m0, s52
	s_add_i32 s52, s52, 0x400
	global_load_lds_dwordx4 v215, s[46:47]
	s_mov_b32 m0, s52
	s_add_i32 s52, s52, 0x400
	global_load_lds_dwordx4 v216, s[46:47]
	s_mov_b32 m0, s52
	s_add_i32 s52, s52, 0x400
	global_load_lds_dwordx4 v217, s[46:47]
	s_mov_b32 m0, s52
	s_nop 0
	global_load_lds_dwordx4 v218, s[46:47]
.Lmylru_nodma_8:
	ds_read_b64 v[178:179], v208 offset:1536
	ds_read_b64 v[180:181], v208 offset:1024
	s_waitcnt lgkmcnt(0)
	v_fma_f32 v182, v176, v178, v179
	v_cndmask_b32_e64 v183, v176, v182, s[38:39]
	v_fma_f32 v176, v182, v180, v181
	v_fma_f32 v184, v183, v200, v203
	v_fma_f32 v185, v183, v199, v177
	v_fma_f32 v186, v183, v198, v201
	v_mov_b32_e32 v187, v183
	v_fma_f32 v184, v184, v227, v231
	v_fma_f32 v185, v185, v228, v232
	v_fma_f32 v186, v186, v229, v233
	v_fma_f32 v187, v187, v230, v234
	v_fma_f32 v144, v184, v96, v144
	v_fma_f32 v148, v185, v100, v148
	v_fma_f32 v152, v186, v104, v152
	v_fma_f32 v156, v187, v108, v156
	v_fma_f32 v145, v184, v97, v145
	v_fma_f32 v149, v185, v101, v149
	v_fma_f32 v153, v186, v105, v153
	v_fma_f32 v157, v187, v109, v157
	v_fma_f32 v146, v184, v98, v146
	v_fma_f32 v150, v185, v102, v150
	v_fma_f32 v154, v186, v106, v154
	v_fma_f32 v158, v187, v110, v158
	v_fma_f32 v147, v184, v99, v147
	v_fma_f32 v151, v185, v103, v151
	v_fma_f32 v155, v186, v107, v155
	v_fma_f32 v159, v187, v111, v159
	s_cmp_gt_u32 s13, 15
	s_cbranch_scc1 .Lmylru_w0_8
	s_waitcnt vmcnt(8)
	s_branch .Lmylru_w1_8
